# speedup vs baseline: 1.0085x; 1.0085x over previous
.LBB0_2:
	s_andn2_b64 vcc, exec, s[4:5]
	s_cbranch_vccnz .LBB0_5
	s_load_dwordx8 s[8:15], s[0:1], 0x18
	s_add_i32 s5, s2, 0xfffff800
	s_ashr_i32 s4, s5, 8
	s_bfe_u32 s7, s2, 0x40004
	s_and_b32 s6, s2, 15
	s_cmpk_gt_u32 s5, 0xff
	s_cselect_b64 s[2:3], -1, 0
	s_cmp_eq_u32 s4, 2
	s_waitcnt lgkmcnt(0)
	s_cselect_b32 s13, s13, s15
	s_cselect_b32 s12, s12, s14
	s_cmp_eq_u32 s4, 1
	s_cselect_b32 s10, s10, s12
	s_cselect_b32 s11, s11, s13
	s_cmpk_lt_u32 s5, 0x100
	s_cselect_b32 s5, s9, s11
	s_cselect_b32 s8, s8, s10
	s_lshl_b32 s14, s7, 6
	s_lshl_b32 s9, s6, 8
	v_lshrrev_b32_e32 v6, 6, v0
	s_add_u32 s8, s8, s9
	v_or_b32_e32 v7, s14, v6
	s_addc_u32 s9, s5, 0
	v_lshlrev_b32_e32 v2, 2, v1
	v_mov_b32_e32 v3, 0
	s_movk_i32 s15, 0x104
	v_lshl_add_u64 v[4:5], s[8:9], 0, v[2:3]
	v_mad_u32_u24 v1, v6, s15, v2
	v_lshlrev_b32_e32 v2, 12, v7
	v_lshl_add_u64 v[4:5], v[4:5], 0, v[2:3]
	s_movk_i32 s5, 0x4000
	v_add_co_u32_e32 v6, vcc, s5, v4
	s_mov_b32 s5, 0x8000
	s_nop 0
	v_addc_co_u32_e32 v7, vcc, 0, v5, vcc
	v_add_co_u32_e32 v8, vcc, s5, v4
	s_mov_b32 s5, 0xc000
	s_nop 0
	v_addc_co_u32_e32 v9, vcc, 0, v5, vcc
	v_add_co_u32_e32 v10, vcc, s5, v4
	s_mov_b32 s5, 0x10000
	s_nop 0
	v_addc_co_u32_e32 v11, vcc, 0, v5, vcc
	v_add_co_u32_e32 v12, vcc, s5, v4
	s_mov_b32 s5, 0x14000
	s_nop 0
	v_addc_co_u32_e32 v13, vcc, 0, v5, vcc
	v_add_co_u32_e32 v14, vcc, s5, v4
	s_mov_b32 s5, 0x18000
	s_nop 0
	v_addc_co_u32_e32 v15, vcc, 0, v5, vcc
	v_add_co_u32_e32 v16, vcc, s5, v4
	s_mov_b32 s5, 0x1c000
	s_nop 0
	v_addc_co_u32_e32 v17, vcc, 0, v5, vcc
	v_add_co_u32_e32 v18, vcc, s5, v4
	s_mov_b32 s5, 0x20000
	s_nop 0
	v_addc_co_u32_e32 v19, vcc, 0, v5, vcc
	global_load_dword v2, v[4:5], off nt
	global_load_dword v20, v[6:7], off nt
	global_load_dword v21, v[8:9], off nt
	global_load_dword v22, v[10:11], off nt
	global_load_dword v23, v[12:13], off nt
	global_load_dword v24, v[14:15], off nt
	global_load_dword v25, v[16:17], off nt
	global_load_dword v26, v[18:19], off nt
	v_add_co_u32_e32 v6, vcc, s5, v4
	s_mov_b32 s5, 0x24000
	s_nop 0
	v_addc_co_u32_e32 v7, vcc, 0, v5, vcc
	v_add_co_u32_e32 v8, vcc, s5, v4
	s_mov_b32 s5, 0x28000
	s_nop 0
	v_addc_co_u32_e32 v9, vcc, 0, v5, vcc
	v_add_co_u32_e32 v10, vcc, s5, v4
	s_mov_b32 s5, 0x2c000
	s_nop 0
	v_addc_co_u32_e32 v11, vcc, 0, v5, vcc
	v_add_co_u32_e32 v12, vcc, s5, v4
	s_mov_b32 s5, 0x30000
	s_nop 0
	v_addc_co_u32_e32 v13, vcc, 0, v5, vcc
	v_add_co_u32_e32 v14, vcc, s5, v4
	s_mov_b32 s5, 0x34000
	s_nop 0
	v_addc_co_u32_e32 v15, vcc, 0, v5, vcc
	v_add_co_u32_e32 v16, vcc, s5, v4
	s_mov_b32 s5, 0x38000
	s_nop 0
	v_addc_co_u32_e32 v17, vcc, 0, v5, vcc
	v_add_co_u32_e32 v18, vcc, s5, v4
	s_mov_b32 s5, 0x3c000
	s_nop 0
	v_addc_co_u32_e32 v19, vcc, 0, v5, vcc
	v_add_co_u32_e32 v4, vcc, s5, v4
	s_load_dwordx4 s[8:11], s[0:1], 0x38
	s_nop 0
	v_addc_co_u32_e32 v5, vcc, 0, v5, vcc
	global_load_dword v27, v[6:7], off nt
	global_load_dword v28, v[8:9], off nt
	global_load_dword v29, v[10:11], off nt
	global_load_dword v30, v[12:13], off nt
	global_load_dword v31, v[14:15], off nt
	global_load_dword v32, v[16:17], off nt
	global_load_dword v33, v[18:19], off nt
	global_load_dword v34, v[4:5], off nt
	s_lshr_b32 s16, s6, 1
	s_lshl_b32 s16, s16, 2
	s_and_b32 s17, s6, 1
	s_or_b32 s16, s16, s17
	s_cmp_lt_u32 s4, 2
	s_cselect_b32 s16, s16, s6
	s_cselect_b32 s17, 17, 20
	s_ashr_i32 s5, s4, 31
	s_lshl_b64 s[12:13], s[4:5], s17
	s_waitcnt lgkmcnt(0)
	s_add_u32 s5, s8, s12
	s_addc_u32 s8, s9, s13
	s_cmp_lt_i32 s4, 3
	v_mov_b32_e32 v17, v3
	s_cselect_b32 s4, s5, s10
	s_cselect_b32 s8, s8, s11
	s_add_u32 s4, s4, s14
	s_addc_u32 s5, s8, 0
	v_mov_b32_e32 v18, v3
	s_cmp_lg_u32 s7, 0
	s_waitcnt vmcnt(15)
	ds_write_b32 v1, v2
	s_waitcnt vmcnt(14)
	ds_write_b32 v1, v20 offset:1040
	s_waitcnt vmcnt(13)
	ds_write_b32 v1, v21 offset:2080
	s_waitcnt vmcnt(12)
	ds_write_b32 v1, v22 offset:3120
	s_waitcnt vmcnt(11)
	ds_write_b32 v1, v23 offset:4160
	s_waitcnt vmcnt(10)
	ds_write_b32 v1, v24 offset:5200
	s_waitcnt vmcnt(9)
	ds_write_b32 v1, v25 offset:6240
	s_waitcnt vmcnt(8)
	ds_write_b32 v1, v26 offset:7280
	s_waitcnt vmcnt(7)
	ds_write_b32 v1, v27 offset:8320
	s_waitcnt vmcnt(6)
	ds_write_b32 v1, v28 offset:9360
	s_waitcnt vmcnt(5)
	ds_write_b32 v1, v29 offset:10400
	s_waitcnt vmcnt(4)
	ds_write_b32 v1, v30 offset:11440
	s_waitcnt vmcnt(3)
	ds_write_b32 v1, v31 offset:12480
	s_waitcnt vmcnt(2)
	ds_write_b32 v1, v32 offset:13520
	s_waitcnt vmcnt(1)
	ds_write_b32 v1, v33 offset:14560
	s_waitcnt vmcnt(0)
	ds_write_b32 v1, v34 offset:15600
	v_lshlrev_b32_e32 v1, 2, v0
	v_and_b32_e32 v2, 60, v1
	v_lshrrev_b32_e32 v1, 4, v0
	v_lshlrev_b32_e32 v4, 2, v1
	v_mad_u32_u24 v16, v2, s15, v4
	s_waitcnt lgkmcnt(0)
	s_barrier
	ds_read2_b32 v[4:5], v16 offset1:16
	ds_read2_b32 v[6:7], v16 offset0:65 offset1:81
	ds_read2_b32 v[8:9], v16 offset0:130 offset1:146
	ds_read2_b32 v[10:11], v16 offset0:195 offset1:211
	v_lshl_add_u64 v[12:13], s[4:5], 0, v[2:3]
	v_lshlrev_b32_e32 v1, 10, v1
	s_waitcnt lgkmcnt(3)
	v_mul_f32_e32 v4, 0x44800000, v4
	s_waitcnt lgkmcnt(2)
	v_mul_f32_e32 v6, 0x44800000, v6
	v_cvt_pk_fp8_f32 v17, v4, v6
	s_waitcnt lgkmcnt(1)
	v_mul_f32_e32 v2, 0x44800000, v8
	s_waitcnt lgkmcnt(0)
	v_mul_f32_e32 v4, 0x44800000, v10
	s_cselect_b64 s[4:5], -1, 0
	v_cvt_pk_fp8_f32 v17, v2, v4 op_sel:[0,0,1]
	v_lshl_or_b32 v2, s16, 16, v1
	v_mul_f32_e32 v1, 0x44800000, v5
	v_mul_f32_e32 v4, 0x44800000, v7
	v_cvt_pk_fp8_f32 v18, v1, v4
	v_lshl_add_u64 v[14:15], v[12:13], 0, v[2:3]
	global_store_dword v[14:15], v17, off
	v_mul_f32_e32 v1, 0x44800000, v9
	v_mul_f32_e32 v4, 0x44800000, v11
	v_cvt_pk_fp8_f32 v18, v1, v4 op_sel:[0,0,1]
	ds_read2_b32 v[4:5], v16 offset0:32 offset1:48
	ds_read2_b32 v[6:7], v16 offset0:97 offset1:113
	ds_read2_b32 v[10:11], v16 offset0:162 offset1:178
	ds_read2_b32 v[14:15], v16 offset0:227 offset1:243
	v_or_b32_e32 v8, 0x4000, v2
	v_mov_b32_e32 v9, v3
	s_waitcnt lgkmcnt(3)
	v_mul_f32_e32 v1, 0x44800000, v4
	s_waitcnt lgkmcnt(2)
	v_mul_f32_e32 v4, 0x44800000, v6
	v_mov_b32_e32 v6, v3
	v_cvt_pk_fp8_f32 v6, v1, v4
	s_waitcnt lgkmcnt(1)
	v_mul_f32_e32 v1, 0x44800000, v10
	s_waitcnt lgkmcnt(0)
	v_mul_f32_e32 v4, 0x44800000, v14
	v_lshl_add_u64 v[8:9], v[12:13], 0, v[8:9]
	v_cvt_pk_fp8_f32 v6, v1, v4 op_sel:[0,0,1]
	v_mul_f32_e32 v1, 0x44800000, v5
	v_mul_f32_e32 v4, 0x44800000, v7
	v_mov_b32_e32 v7, v3
	v_cvt_pk_fp8_f32 v7, v1, v4
	global_store_dword v[8:9], v18, off
	v_or_b32_e32 v8, 0x8000, v2
	v_mov_b32_e32 v9, v3
	v_lshl_add_u64 v[4:5], v[12:13], 0, v[8:9]
	v_mul_f32_e32 v1, 0x44800000, v11
	v_mul_f32_e32 v8, 0x44800000, v15
	v_cvt_pk_fp8_f32 v7, v1, v8 op_sel:[0,0,1]
	v_or_b32_e32 v2, 0xc000, v2
	s_or_b64 s[2:3], s[2:3], s[4:5]
	v_lshl_add_u64 v[2:3], v[12:13], 0, v[2:3]
	s_and_b64 vcc, exec, s[2:3]
	global_store_dword v[4:5], v6, off
	global_store_dword v[2:3], v7, off
	s_cbranch_vccnz .LBB0_5
	v_lshl_or_b32 v2, s6, 8, v0
	v_cvt_f32_u32_e32 v0, v2
	s_mov_b32 s2, 0x7f800000
	v_mov_b32_e32 v5, 0xbf1f24be
	s_load_dwordx2 s[0:1], s[0:1], 0x48
	v_mul_f32_e32 v0, 0x3a000000, v0
	v_mul_f32_e32 v1, 0.5, v0
	v_fract_f32_e32 v3, v1
	v_add_f32_e32 v3, v3, v3
	v_cmp_neq_f32_e32 vcc, s2, v1
	s_brev_b32 s3, 1
	v_lshlrev_b32_e32 v2, 3, v2
	v_cndmask_b32_e32 v1, 0, v3, vcc
	v_cmp_lt_f32_e32 vcc, 1.0, v0
	s_nop 1
	v_cndmask_b32_e32 v1, v0, v1, vcc
	v_add_f32_e32 v3, v1, v1
	v_rndne_f32_e32 v3, v3
	v_fmac_f32_e32 v1, -0.5, v3
	v_mul_f32_e32 v4, v1, v1
	v_fmac_f32_e32 v5, 0x3e75aa41, v4
	v_fmaak_f32 v5, v4, v5, 0x40234736
	v_fmaak_f32 v5, v4, v5, 0xc0a55e0e
	v_mul_f32_e32 v6, v1, v4
	v_mul_f32_e32 v5, v6, v5
	v_fmamk_f32 v1, v1, 0x40490fdb, v5
	v_mov_b32_e32 v5, 0x3e642e9d
	v_cvt_i32_f32_e32 v3, v3
	v_fmac_f32_e32 v5, 0x3d4be544, v4
	v_fmaak_f32 v5, v4, v5, 0xbfaad1da
	v_fmaak_f32 v5, v4, v5, 0x4081e0d3
	v_fmaak_f32 v5, v4, v5, 0xc09de9e6
	v_fma_f32 v4, v4, v5, 1.0
	v_lshlrev_b32_e32 v5, 30, v3
	v_and_b32_e32 v3, 1, v3
	v_cmp_eq_u32_e32 vcc, 0, v3
	s_nop 1
	v_cndmask_b32_e32 v3, v4, v1, vcc
	v_xor_b32_e32 v1, 0x80000000, v1
	v_cndmask_b32_e32 v1, v1, v4, vcc
	v_bitop3_b32 v3, v3, v5, s3 bitop3:0x78
	v_bitop3_b32 v4, v1, v5, s3 bitop3:0x78
	v_mov_b32_e32 v1, 0xffc00000
	v_cmp_lg_f32_e32 vcc, s2, v0
	v_mov_b32_e32 v0, 0x7fc00000
	s_nop 0
	v_cndmask_b32_e64 v1, v1, -v3, vcc
	v_cndmask_b32_e32 v0, v0, v4, vcc
	s_waitcnt lgkmcnt(0)
	global_store_dwordx2 v2, v[0:1], s[0:1]

	.amdhsa_kernel _Z6k_prepPK15HIP_vector_typeIfLj4EEPS_IjLj4EEiPKfS6_S6_S6_PtS7_PS_IfLj2EE
		.amdhsa_group_segment_fixed_size 16640
		.amdhsa_private_segment_fixed_size 0
		.amdhsa_kernarg_size 80
		.amdhsa_user_sgpr_count 2
		.amdhsa_user_sgpr_dispatch_ptr 0
		.amdhsa_user_sgpr_queue_ptr 0
		.amdhsa_user_sgpr_kernarg_segment_ptr 1
		.amdhsa_user_sgpr_dispatch_id 0
		.amdhsa_user_sgpr_kernarg_preload_length 0
		.amdhsa_user_sgpr_kernarg_preload_offset 0
		.amdhsa_user_sgpr_private_segment_size 0
		.amdhsa_uses_dynamic_stack 0
		.amdhsa_enable_private_segment 0
		.amdhsa_system_sgpr_workgroup_id_x 1
		.amdhsa_system_sgpr_workgroup_id_y 0
		.amdhsa_system_sgpr_workgroup_id_z 0
		.amdhsa_system_sgpr_workgroup_info 0
		.amdhsa_system_vgpr_workitem_id 0
		.amdhsa_next_free_vgpr 45
		.amdhsa_next_free_sgpr 20
		.amdhsa_accum_offset 48
		.amdhsa_reserve_vcc 1
		.amdhsa_float_round_mode_32 0
		.amdhsa_float_round_mode_16_64 0
		.amdhsa_float_denorm_mode_32 3
		.amdhsa_float_denorm_mode_16_64 3
		.amdhsa_dx10_clamp 1
		.amdhsa_ieee_mode 1
		.amdhsa_fp16_overflow 0
		.amdhsa_tg_split 0
		.amdhsa_exception_fp_ieee_invalid_op 0
		.amdhsa_exception_fp_denorm_src 0
		.amdhsa_exception_fp_ieee_div_zero 0
		.amdhsa_exception_fp_ieee_overflow 0
		.amdhsa_exception_fp_ieee_underflow 0
		.amdhsa_exception_fp_ieee_inexact 0
		.amdhsa_exception_int_div_zero 0
	.end_amdhsa_kernel

_Z5k_fftPKtPtPKDv2_f:
	s_load_dwordx2 s[6:7], s[0:1], 0x10
	s_load_dwordx2 s[8:9], s[0:1], 0x0
	v_and_b32_e32 v1, 0xf0, v0
	v_and_b32_e32 v18, 15, v0
	v_mul_u32_u24_e32 v1, v1, v18
	v_lshlrev_b32_e32 v1, 3, v1
	s_waitcnt lgkmcnt(0)
	global_load_dwordx2 v[86:87], v1, s[6:7]
	s_lshr_b32 s4, s2, 3
	s_and_b32 s3, s2, 7
	s_and_b32 s4, s4, 0x1ffffff8
	s_or_b32 s4, s4, s3
	s_bfe_u32 s16, s2, 0x30003
	s_lshl_b32 s3, s4, 3
	s_or_b32 s3, s3, s16
	s_lshl_b32 s22, s3, 14
	s_add_u32 s22, s8, s22
	s_addc_u32 s23, s9, 0
	s_mov_b32 s11, 0
	s_lshr_b32 s10, s3, 1
	s_lshl_b64 s[10:11], s[10:11], 14
	s_add_u32 s3, s8, s10
	s_addc_u32 s8, s9, s11
	s_lshr_b32 s2, s2, 2
	s_and_b32 s2, s2, 2
	s_add_u32 s2, s3, s2
	v_mov_b32_e32 v3, 0
	v_lshlrev_b32_e32 v2, 2, v0
	s_addc_u32 s3, s8, 0
	s_movk_i32 s5, 0x1000
	v_lshl_add_u64 v[6:7], s[2:3], 0, v[2:3]
	v_add_co_u32_e32 v8, vcc, s5, v6
	s_movk_i32 s12, 0x2000
	s_nop 0
	v_addc_co_u32_e32 v9, vcc, 0, v7, vcc
	v_add_co_u32_e32 v10, vcc, s12, v6
	s_movk_i32 s13, 0x3000
	s_add_u32 s8, s2, 0x1000000
	v_addc_co_u32_e32 v11, vcc, 0, v7, vcc
	s_addc_u32 s9, s3, 0
	s_add_u32 s20, s2, 0x2000000
	s_addc_u32 s21, s3, 0
	v_add_co_u32_e32 v6, vcc, s13, v6
	v_lshl_add_u64 v[12:13], s[8:9], 0, v[2:3]
	s_nop 0
	v_addc_co_u32_e32 v7, vcc, 0, v7, vcc
	v_add_co_u32_e32 v14, vcc, s5, v12
	v_lshlrev_b32_e32 v1, 3, v0
	s_nop 0
	v_addc_co_u32_e32 v15, vcc, 0, v13, vcc
	v_add_co_u32_e32 v16, vcc, s12, v12
	v_or_b32_e32 v19, 0x1000, v2
	s_nop 0
	v_addc_co_u32_e32 v17, vcc, 0, v13, vcc
	v_add_co_u32_e32 v12, vcc, s13, v12
	v_or_b32_e32 v20, 0x2000, v2
	v_or_b32_e32 v21, 0x3000, v2
	v_addc_co_u32_e32 v13, vcc, 0, v13, vcc
	v_mul_u32_u24_e32 v3, 3, v0
	s_movk_i32 s5, 0x888
	v_lshlrev_b32_e32 v3, 3, v3
	s_mov_b32 s10, 0x3ec3ef15
	s_mov_b32 s11, 0xbf6c835e
	s_mov_b32 s14, s11
	s_mov_b32 s15, s10
	s_mov_b32 s12, 0xbf3504f3
	s_mov_b32 s13, s12
	v_mov_b32_e32 v88, v0
	global_load_dword v85, v2, s[22:23] nt
	global_load_dword v84, v2, s[22:23] offset:1024 nt
	global_load_dword v83, v2, s[22:23] offset:2048 nt
	global_load_dword v82, v2, s[22:23] offset:3072 nt
	global_load_dword v81, v19, s[22:23] nt
	global_load_dword v80, v19, s[22:23] offset:1024 nt
	global_load_dword v79, v19, s[22:23] offset:2048 nt
	global_load_dword v78, v19, s[22:23] offset:3072 nt
	global_load_dword v77, v20, s[22:23] nt
	global_load_dword v76, v20, s[22:23] offset:1024 nt
	global_load_dword v75, v20, s[22:23] offset:2048 nt
	global_load_dword v74, v20, s[22:23] offset:3072 nt
	global_load_dword v73, v21, s[22:23] nt
	global_load_dword v72, v21, s[22:23] offset:1024 nt
	global_load_dword v71, v21, s[22:23] offset:2048 nt
	global_load_dword v70, v21, s[22:23] offset:3072 nt
	v_mul_u32_u24_e32 v5, 5, v0
	v_mul_u32_u24_e32 v6, 6, v0
	v_mul_u32_u24_e32 v7, 7, v0
	v_mul_u32_u24_e32 v9, 9, v0
	v_mul_u32_u24_e32 v10, 10, v0
	v_lshrrev_b32_e32 v16, 1, v0
	v_lshlrev_b32_e32 v2, 4, v0
	v_lshlrev_b32_e32 v4, 5, v0
	v_lshlrev_b32_e32 v8, 6, v0
	v_mul_u32_u24_e32 v11, 11, v0
	v_mul_u32_u24_e32 v12, 12, v0
	v_mul_u32_u24_e32 v13, 13, v0
	v_mul_u32_u24_e32 v14, 14, v0
	v_mul_u32_u24_e32 v15, 15, v0
	v_lshlrev_b32_e32 v5, 3, v5
	v_lshlrev_b32_e32 v6, 3, v6
	v_lshlrev_b32_e32 v7, 3, v7
	v_lshlrev_b32_e32 v9, 3, v9
	v_lshlrev_b32_e32 v64, 3, v10
	v_and_b32_e32 v10, 0x78, v16
	v_lshlrev_b32_e32 v65, 3, v11
	v_lshlrev_b32_e32 v66, 3, v12
	v_lshlrev_b32_e32 v67, 3, v13
	v_lshlrev_b32_e32 v68, 3, v14
	v_lshlrev_b32_e32 v69, 3, v15
	v_mad_u32_u24 v96, v18, s5, v10
	global_load_dwordx2 v[30:31], v1, s[6:7]
	global_load_dwordx2 v[28:29], v2, s[6:7]
	global_load_dwordx2 v[24:25], v4, s[6:7]
	global_load_dwordx2 v[22:23], v8, s[6:7]
	s_nop 0
	s_mov_b32 s6, 0x3f6c835e
	s_mov_b32 s7, 0xbec3ef15
	s_mov_b32 s8, 0x3f3504f3
	s_mov_b32 s9, s8
	s_waitcnt vmcnt(19)
	v_cvt_f32_fp8_e32 v32, v85
	s_waitcnt vmcnt(18)
	v_cvt_f32_fp8_sdwa v33, v85 src0_sel:BYTE_2
	s_waitcnt vmcnt(17)
	v_cvt_f32_fp8_e32 v34, v84
	v_cvt_f32_fp8_sdwa v35, v84 src0_sel:BYTE_2
	s_waitcnt vmcnt(16)
	s_waitcnt vmcnt(15)
	v_cvt_f32_fp8_e32 v40, v81
	s_waitcnt vmcnt(14)
	v_cvt_f32_fp8_sdwa v41, v81 src0_sel:BYTE_2
	s_waitcnt vmcnt(13)
	v_cvt_f32_fp8_e32 v42, v80
	v_cvt_f32_fp8_sdwa v43, v80 src0_sel:BYTE_2
	v_cvt_f32_fp8_e32 v36, v83
	v_cvt_f32_fp8_sdwa v37, v83 src0_sel:BYTE_2
	s_waitcnt vmcnt(12)
	v_cvt_f32_fp8_e32 v44, v79
	s_waitcnt vmcnt(11)
	v_cvt_f32_fp8_e32 v48, v77
	s_waitcnt vmcnt(10)
	v_cvt_f32_fp8_sdwa v49, v77 src0_sel:BYTE_2
	s_waitcnt vmcnt(9)
	v_cvt_f32_fp8_e32 v50, v76
	v_cvt_f32_fp8_sdwa v51, v76 src0_sel:BYTE_2
	s_waitcnt vmcnt(8)
	s_waitcnt vmcnt(7)
	v_cvt_f32_fp8_e32 v56, v73
	s_waitcnt vmcnt(6)
	v_cvt_f32_fp8_sdwa v57, v73 src0_sel:BYTE_2
	s_waitcnt vmcnt(5)
	v_cvt_f32_fp8_e32 v58, v72
	v_cvt_f32_fp8_sdwa v59, v72 src0_sel:BYTE_2
	v_cvt_f32_fp8_sdwa v45, v79 src0_sel:BYTE_2
	v_cvt_f32_fp8_e32 v52, v75
	v_cvt_f32_fp8_sdwa v53, v75 src0_sel:BYTE_2
	v_cvt_f32_fp8_e32 v60, v71
	v_cvt_f32_fp8_sdwa v61, v71 src0_sel:BYTE_2
	s_waitcnt vmcnt(4)
	v_cvt_f32_fp8_e32 v38, v82
	v_cvt_f32_fp8_sdwa v39, v82 src0_sel:BYTE_2
	v_cvt_f32_fp8_e32 v46, v78
	v_cvt_f32_fp8_sdwa v47, v78 src0_sel:BYTE_2
	v_cvt_f32_fp8_e32 v54, v74
	v_cvt_f32_fp8_sdwa v55, v74 src0_sel:BYTE_2
	v_cvt_f32_fp8_e32 v62, v70
	v_cvt_f32_fp8_sdwa v63, v70 src0_sel:BYTE_2
	v_pk_add_f32 v[64:65], v[32:33], v[48:49]
	v_pk_add_f32 v[32:33], v[32:33], v[48:49] neg_lo:[0,1] neg_hi:[0,1]
	v_pk_add_f32 v[48:49], v[40:41], v[56:57]
	v_pk_add_f32 v[40:41], v[40:41], v[56:57] neg_lo:[0,1] neg_hi:[0,1]
	v_pk_add_f32 v[56:57], v[64:65], v[48:49]
	v_pk_add_f32 v[48:49], v[64:65], v[48:49] neg_lo:[0,1] neg_hi:[0,1]
	v_pk_add_f32 v[64:65], v[32:33], v[40:41] op_sel:[0,1] op_sel_hi:[1,0] neg_hi:[0,1]
	v_pk_add_f32 v[32:33], v[32:33], v[40:41] op_sel:[0,1] op_sel_hi:[1,0] neg_lo:[0,1]
	v_pk_add_f32 v[40:41], v[34:35], v[50:51]
	v_pk_add_f32 v[34:35], v[34:35], v[50:51] neg_lo:[0,1] neg_hi:[0,1]
	v_pk_add_f32 v[50:51], v[42:43], v[58:59]
	v_pk_add_f32 v[42:43], v[42:43], v[58:59] neg_lo:[0,1] neg_hi:[0,1]
	v_pk_add_f32 v[58:59], v[40:41], v[50:51]
	v_pk_add_f32 v[40:41], v[40:41], v[50:51] neg_lo:[0,1] neg_hi:[0,1]
	v_pk_add_f32 v[50:51], v[34:35], v[42:43] op_sel:[0,1] op_sel_hi:[1,0] neg_hi:[0,1]
	v_pk_add_f32 v[34:35], v[34:35], v[42:43] op_sel:[0,1] op_sel_hi:[1,0] neg_lo:[0,1]
	v_pk_add_f32 v[42:43], v[36:37], v[52:53]
	v_pk_add_f32 v[36:37], v[36:37], v[52:53] neg_lo:[0,1] neg_hi:[0,1]
	v_pk_add_f32 v[52:53], v[44:45], v[60:61]
	v_pk_add_f32 v[44:45], v[44:45], v[60:61] neg_lo:[0,1] neg_hi:[0,1]
	v_pk_add_f32 v[60:61], v[42:43], v[52:53]
	v_pk_add_f32 v[42:43], v[42:43], v[52:53] neg_lo:[0,1] neg_hi:[0,1]
	v_pk_add_f32 v[52:53], v[36:37], v[44:45] op_sel:[0,1] op_sel_hi:[1,0] neg_hi:[0,1]
	v_pk_add_f32 v[36:37], v[36:37], v[44:45] op_sel:[0,1] op_sel_hi:[1,0] neg_lo:[0,1]
	v_pk_add_f32 v[44:45], v[38:39], v[54:55]
	v_pk_add_f32 v[38:39], v[38:39], v[54:55] neg_lo:[0,1] neg_hi:[0,1]
	v_pk_add_f32 v[54:55], v[46:47], v[62:63]
	v_pk_add_f32 v[46:47], v[46:47], v[62:63] neg_lo:[0,1] neg_hi:[0,1]
	v_pk_add_f32 v[62:63], v[44:45], v[54:55]
	v_pk_add_f32 v[44:45], v[44:45], v[54:55] neg_lo:[0,1] neg_hi:[0,1]
	v_pk_add_f32 v[54:55], v[38:39], v[46:47] op_sel:[0,1] op_sel_hi:[1,0] neg_hi:[0,1]
	v_pk_add_f32 v[38:39], v[38:39], v[46:47] op_sel:[0,1] op_sel_hi:[1,0] neg_lo:[0,1]
	v_pk_mul_f32 v[46:47], v[50:51], s[6:7] op_sel:[0,0] op_sel_hi:[0,1]
	v_pk_fma_f32 v[46:47], v[50:51], s[6:7], v[46:47] op_sel:[1,1,0] op_sel_hi:[1,0,1] neg_lo:[0,1,0]
	v_pk_mul_f32 v[50:51], v[34:35], s[10:11] op_sel:[0,0] op_sel_hi:[0,1]
	v_pk_fma_f32 v[50:51], v[34:35], s[10:11], v[50:51] op_sel:[1,1,0] op_sel_hi:[1,0,1] neg_lo:[0,1,0]
	v_pk_add_f32 v[34:35], v[52:53], v[52:53] op_sel:[0,1] op_sel_hi:[1,0] neg_hi:[0,1]
	v_pk_add_f32 v[40:41], v[40:41], v[40:41] op_sel:[0,1] op_sel_hi:[1,0] neg_hi:[0,1]
	s_nop 0
	v_pk_mul_f32 v[52:53], v[54:55], s[10:11] op_sel:[0,0] op_sel_hi:[0,1]
	v_pk_fma_f32 v[52:53], v[54:55], s[10:11], v[52:53] op_sel:[1,1,0] op_sel_hi:[1,0,1] neg_lo:[0,1,0]
	v_pk_mul_f32 v[54:55], v[38:39], s[14:15] op_sel:[0,0] op_sel_hi:[0,1]
	v_pk_fma_f32 v[54:55], v[38:39], s[14:15], v[54:55] op_sel:[1,1,0] op_sel_hi:[1,0,1] neg_lo:[0,1,0]
	v_pk_add_f32 v[38:39], v[56:57], v[60:61]
	v_pk_mul_f32 v[34:35], v[34:35], s[8:9]
	v_pk_add_f32 v[56:57], v[56:57], v[60:61] neg_lo:[0,1] neg_hi:[0,1]
	v_pk_add_f32 v[60:61], v[58:59], v[62:63]
	v_pk_add_f32 v[58:59], v[58:59], v[62:63] neg_lo:[0,1] neg_hi:[0,1]
	v_pk_mul_f32 v[40:41], v[40:41], s[8:9]
	v_pk_add_f32 v[36:37], v[36:37], v[36:37] op_sel:[0,1] op_sel_hi:[1,0] neg_lo:[0,1]
	v_pk_add_f32 v[44:45], v[44:45], v[44:45] op_sel:[0,1] op_sel_hi:[1,0] neg_lo:[0,1]
	v_pk_add_f32 v[62:63], v[38:39], v[60:61]
	v_pk_add_f32 v[38:39], v[38:39], v[60:61] neg_lo:[0,1] neg_hi:[0,1]
	v_pk_add_f32 v[60:61], v[56:57], v[58:59] op_sel:[0,1] op_sel_hi:[1,0] neg_hi:[0,1]
	v_pk_add_f32 v[56:57], v[56:57], v[58:59] op_sel:[0,1] op_sel_hi:[1,0] neg_lo:[0,1]
	v_pk_add_f32 v[58:59], v[64:65], v[34:35]
	v_pk_add_f32 v[34:35], v[64:65], v[34:35] neg_lo:[0,1] neg_hi:[0,1]
	v_pk_add_f32 v[64:65], v[46:47], v[52:53]
	v_pk_add_f32 v[46:47], v[46:47], v[52:53] neg_lo:[0,1] neg_hi:[0,1]
	v_pk_mul_f32 v[36:37], v[36:37], s[12:13]
	v_pk_mul_f32 v[44:45], v[44:45], s[12:13]
	v_pk_add_f32 v[52:53], v[58:59], v[64:65]
	v_pk_add_f32 v[58:59], v[58:59], v[64:65] neg_lo:[0,1] neg_hi:[0,1]
	v_pk_add_f32 v[64:65], v[34:35], v[46:47] op_sel:[0,1] op_sel_hi:[1,0] neg_hi:[0,1]
	v_pk_add_f32 v[34:35], v[34:35], v[46:47] op_sel:[0,1] op_sel_hi:[1,0] neg_lo:[0,1]
	v_pk_add_f32 v[46:47], v[48:49], v[42:43] op_sel:[0,1] op_sel_hi:[1,0] neg_hi:[0,1]
	v_pk_add_f32 v[42:43], v[48:49], v[42:43] op_sel:[0,1] op_sel_hi:[1,0] neg_lo:[0,1]
	v_pk_add_f32 v[48:49], v[40:41], v[44:45]
	v_pk_add_f32 v[40:41], v[40:41], v[44:45] neg_lo:[0,1] neg_hi:[0,1]
	v_pk_add_f32 v[44:45], v[48:49], v[46:47]
	v_pk_add_f32 v[46:47], v[46:47], v[48:49] neg_lo:[0,1] neg_hi:[0,1]
	v_pk_add_f32 v[48:49], v[42:43], v[40:41] op_sel:[0,1] op_sel_hi:[1,0] neg_hi:[0,1]
	v_pk_add_f32 v[40:41], v[42:43], v[40:41] op_sel:[0,1] op_sel_hi:[1,0] neg_lo:[0,1]
	v_pk_add_f32 v[42:43], v[32:33], v[36:37]
	v_pk_add_f32 v[32:33], v[32:33], v[36:37] neg_lo:[0,1] neg_hi:[0,1]
	v_pk_add_f32 v[36:37], v[50:51], v[54:55]
	v_pk_add_f32 v[50:51], v[50:51], v[54:55] neg_lo:[0,1] neg_hi:[0,1]
	v_pk_add_f32 v[54:55], v[42:43], v[36:37]
	v_pk_add_f32 v[36:37], v[42:43], v[36:37] neg_lo:[0,1] neg_hi:[0,1]
	v_pk_add_f32 v[42:43], v[32:33], v[50:51] op_sel:[0,1] op_sel_hi:[1,0] neg_hi:[0,1]
	v_pk_add_f32 v[32:33], v[32:33], v[50:51] op_sel:[0,1] op_sel_hi:[1,0] neg_lo:[0,1]
	s_waitcnt vmcnt(0)
	v_pk_mul_f32 v[26:27], v[30:31], v[28:29] op_sel:[0,0] op_sel_hi:[0,1]
	v_pk_fma_f32 v[26:27], v[30:31], v[28:29], v[26:27] op_sel:[1,1,0] op_sel_hi:[1,0,1] neg_lo:[0,1,0]
	v_pk_mul_f32 v[20:21], v[30:31], v[24:25] op_sel:[0,0] op_sel_hi:[0,1]
	v_pk_fma_f32 v[20:21], v[30:31], v[24:25], v[20:21] op_sel:[1,1,0] op_sel_hi:[1,0,1] neg_lo:[0,1,0]
	v_pk_mul_f32 v[16:17], v[28:29], v[24:25] op_sel:[0,0] op_sel_hi:[0,1]
	v_pk_fma_f32 v[16:17], v[28:29], v[24:25], v[16:17] op_sel:[1,1,0] op_sel_hi:[1,0,1] neg_lo:[0,1,0]
	v_pk_mul_f32 v[18:19], v[30:31], v[22:23] op_sel:[0,0] op_sel_hi:[0,1]
	v_pk_fma_f32 v[18:19], v[30:31], v[22:23], v[18:19] op_sel:[1,1,0] op_sel_hi:[1,0,1] neg_lo:[0,1,0]
	v_pk_mul_f32 v[12:13], v[28:29], v[22:23] op_sel:[0,0] op_sel_hi:[0,1]
	v_pk_fma_f32 v[12:13], v[28:29], v[22:23], v[12:13] op_sel:[1,1,0] op_sel_hi:[1,0,1] neg_lo:[0,1,0]
	v_pk_mul_f32 v[6:7], v[24:25], v[22:23] op_sel:[0,0] op_sel_hi:[0,1]
	v_pk_fma_f32 v[6:7], v[24:25], v[22:23], v[6:7] op_sel:[1,1,0] op_sel_hi:[1,0,1] neg_lo:[0,1,0]
	v_pk_mul_f32 v[10:11], v[26:27], v[24:25] op_sel:[0,0] op_sel_hi:[0,1]
	v_pk_fma_f32 v[10:11], v[26:27], v[24:25], v[10:11] op_sel:[1,1,0] op_sel_hi:[1,0,1] neg_lo:[0,1,0]
	v_pk_mul_f32 v[14:15], v[26:27], v[22:23] op_sel:[0,0] op_sel_hi:[0,1]
	v_pk_fma_f32 v[14:15], v[26:27], v[22:23], v[14:15] op_sel:[1,1,0] op_sel_hi:[1,0,1] neg_lo:[0,1,0]
	v_pk_mul_f32 v[8:9], v[20:21], v[22:23] op_sel:[0,0] op_sel_hi:[0,1]
	v_pk_fma_f32 v[8:9], v[20:21], v[22:23], v[8:9] op_sel:[1,1,0] op_sel_hi:[1,0,1] neg_lo:[0,1,0]
	v_pk_mul_f32 v[4:5], v[16:17], v[22:23] op_sel:[0,0] op_sel_hi:[0,1]
	v_pk_fma_f32 v[4:5], v[16:17], v[22:23], v[4:5] op_sel:[1,1,0] op_sel_hi:[1,0,1] neg_lo:[0,1,0]
	v_pk_mul_f32 v[2:3], v[10:11], v[22:23] op_sel:[0,0] op_sel_hi:[0,1]
	v_pk_fma_f32 v[2:3], v[10:11], v[22:23], v[2:3] op_sel:[1,1,0] op_sel_hi:[1,0,1] neg_lo:[0,1,0]
	v_pk_mul_f32 v[50:51], v[52:53], v[30:31] op_sel:[0,0] op_sel_hi:[0,1]
	v_pk_fma_f32 v[50:51], v[52:53], v[30:31], v[50:51] op_sel:[1,1,0] op_sel_hi:[1,0,1] neg_lo:[0,1,0]
	ds_write_b64 v1, v[50:51] offset:2184
	v_pk_mul_f32 v[50:51], v[44:45], v[28:29] op_sel:[0,0] op_sel_hi:[0,1]
	v_pk_fma_f32 v[50:51], v[44:45], v[28:29], v[50:51] op_sel:[1,1,0] op_sel_hi:[1,0,1] neg_lo:[0,1,0]
	v_pk_mul_f32 v[44:45], v[54:55], v[26:27] op_sel:[0,0] op_sel_hi:[0,1]
	v_pk_fma_f32 v[44:45], v[54:55], v[26:27], v[44:45] op_sel:[1,1,0] op_sel_hi:[1,0,1] neg_lo:[0,1,0]
	ds_write_b64 v1, v[44:45] offset:6552
	v_pk_mul_f32 v[44:45], v[60:61], v[24:25] op_sel:[0,0] op_sel_hi:[0,1]
	v_pk_fma_f32 v[44:45], v[60:61], v[24:25], v[44:45] op_sel:[1,1,0] op_sel_hi:[1,0,1] neg_lo:[0,1,0]
	ds_write_b64 v1, v[44:45] offset:8736
	v_pk_mul_f32 v[44:45], v[64:65], v[20:21] op_sel:[0,0] op_sel_hi:[0,1]
	v_pk_fma_f32 v[44:45], v[64:65], v[20:21], v[44:45] op_sel:[1,1,0] op_sel_hi:[1,0,1] neg_lo:[0,1,0]
	ds_write_b64 v1, v[44:45] offset:10920
	v_pk_mul_f32 v[44:45], v[48:49], v[16:17] op_sel:[0,0] op_sel_hi:[0,1]
	v_pk_fma_f32 v[44:45], v[48:49], v[16:17], v[44:45] op_sel:[1,1,0] op_sel_hi:[1,0,1] neg_lo:[0,1,0]
	ds_write_b64 v1, v[44:45] offset:13104
	v_pk_mul_f32 v[44:45], v[42:43], v[10:11] op_sel:[0,0] op_sel_hi:[0,1]
	v_pk_fma_f32 v[44:45], v[42:43], v[10:11], v[44:45] op_sel:[1,1,0] op_sel_hi:[1,0,1] neg_lo:[0,1,0]
	v_pk_mul_f32 v[42:43], v[38:39], v[22:23] op_sel:[0,0] op_sel_hi:[0,1]
	v_pk_fma_f32 v[42:43], v[38:39], v[22:23], v[42:43] op_sel:[1,1,0] op_sel_hi:[1,0,1] neg_lo:[0,1,0]
	v_pk_mul_f32 v[38:39], v[58:59], v[18:19] op_sel:[0,0] op_sel_hi:[0,1]
	v_pk_fma_f32 v[38:39], v[58:59], v[18:19], v[38:39] op_sel:[1,1,0] op_sel_hi:[1,0,1] neg_lo:[0,1,0]
	ds_write_b64 v1, v[38:39] offset:19656
	v_pk_mul_f32 v[38:39], v[46:47], v[12:13] op_sel:[0,0] op_sel_hi:[0,1]
	v_pk_fma_f32 v[38:39], v[46:47], v[12:13], v[38:39] op_sel:[1,1,0] op_sel_hi:[1,0,1] neg_lo:[0,1,0]
	ds_write_b64 v1, v[38:39] offset:21840
	v_pk_mul_f32 v[38:39], v[36:37], v[14:15] op_sel:[0,0] op_sel_hi:[0,1]
	v_pk_fma_f32 v[38:39], v[36:37], v[14:15], v[38:39] op_sel:[1,1,0] op_sel_hi:[1,0,1] neg_lo:[0,1,0]
	v_pk_mul_f32 v[36:37], v[56:57], v[6:7] op_sel:[0,0] op_sel_hi:[0,1]
	v_pk_fma_f32 v[36:37], v[56:57], v[6:7], v[36:37] op_sel:[1,1,0] op_sel_hi:[1,0,1] neg_lo:[0,1,0]
	ds_write_b64 v1, v[36:37] offset:26208
	v_pk_mul_f32 v[36:37], v[34:35], v[8:9] op_sel:[0,0] op_sel_hi:[0,1]
	v_pk_fma_f32 v[36:37], v[34:35], v[8:9], v[36:37] op_sel:[1,1,0] op_sel_hi:[1,0,1] neg_lo:[0,1,0]
	v_pk_mul_f32 v[34:35], v[40:41], v[4:5] op_sel:[0,0] op_sel_hi:[0,1]
	v_pk_fma_f32 v[34:35], v[40:41], v[4:5], v[34:35] op_sel:[1,1,0] op_sel_hi:[1,0,1] neg_lo:[0,1,0]
	ds_write_b64 v1, v[34:35] offset:30576
	v_pk_mul_f32 v[34:35], v[32:33], v[2:3] op_sel:[0,0] op_sel_hi:[0,1]
	v_pk_fma_f32 v[34:35], v[32:33], v[2:3], v[34:35] op_sel:[1,1,0] op_sel_hi:[1,0,1] neg_lo:[0,1,0]
	ds_write_b64 v1, v[62:63]
	ds_write_b64 v1, v[50:51] offset:4368
	ds_write_b64 v1, v[44:45] offset:15288
	ds_write_b64 v1, v[42:43] offset:17472
	ds_write_b64 v1, v[38:39] offset:24024
	ds_write_b64 v1, v[36:37] offset:28392
	ds_write_b64 v1, v[34:35] offset:32760
	ds_write_b64 v1, v[86:87] offset:34816
	s_waitcnt lgkmcnt(0)
	s_barrier
	ds_read2_b64 v[32:35], v96 offset1:16
	ds_read2_b64 v[36:39], v96 offset0:32 offset1:48
	ds_read2_b64 v[40:43], v96 offset0:64 offset1:80
	ds_read2_b64 v[44:47], v96 offset0:128 offset1:144
	ds_read2_b64 v[48:51], v96 offset0:96 offset1:112
	ds_read2_b64 v[52:55], v96 offset0:192 offset1:208
	ds_read2_b64 v[56:59], v96 offset0:160 offset1:176
	ds_read2_b64 v[60:63], v96 offset0:224 offset1:240
	v_lshlrev_b32_e32 v115, 2, v0
	v_lshlrev_b32_e32 v119, 2, v0
	v_lshlrev_b32_e32 v123, 2, v0
	v_lshlrev_b32_e32 v127, 2, v0
	v_or_b32_e32 v119, 0x1000, v119
	v_or_b32_e32 v123, 0x2000, v123
	v_or_b32_e32 v127, 0x3000, v127
	global_load_ushort v112, v115, s[20:21]
	global_load_ushort v113, v115, s[20:21] offset:1024
	global_load_ushort v114, v115, s[20:21] offset:2048
	global_load_ushort v115, v115, s[20:21] offset:3072
	global_load_ushort v116, v119, s[20:21]
	global_load_ushort v117, v119, s[20:21] offset:1024
	global_load_ushort v118, v119, s[20:21] offset:2048
	global_load_ushort v119, v119, s[20:21] offset:3072
	global_load_ushort v120, v123, s[20:21]
	global_load_ushort v121, v123, s[20:21] offset:1024
	global_load_ushort v122, v123, s[20:21] offset:2048
	global_load_ushort v123, v123, s[20:21] offset:3072
	global_load_ushort v124, v127, s[20:21]
	global_load_ushort v125, v127, s[20:21] offset:1024
	global_load_ushort v126, v127, s[20:21] offset:2048
	global_load_ushort v127, v127, s[20:21] offset:3072
	s_waitcnt lgkmcnt(4)
	v_pk_add_f32 v[64:65], v[32:33], v[44:45]
	v_pk_add_f32 v[32:33], v[32:33], v[44:45] neg_lo:[0,1] neg_hi:[0,1]
	s_waitcnt lgkmcnt(2)
	v_pk_add_f32 v[44:45], v[40:41], v[52:53]
	v_pk_add_f32 v[40:41], v[40:41], v[52:53] neg_lo:[0,1] neg_hi:[0,1]
	v_pk_add_f32 v[52:53], v[64:65], v[44:45]
	v_pk_add_f32 v[44:45], v[64:65], v[44:45] neg_lo:[0,1] neg_hi:[0,1]
	v_pk_add_f32 v[64:65], v[32:33], v[40:41] op_sel:[0,1] op_sel_hi:[1,0] neg_hi:[0,1]
	v_pk_add_f32 v[32:33], v[32:33], v[40:41] op_sel:[0,1] op_sel_hi:[1,0] neg_lo:[0,1]
	v_pk_add_f32 v[40:41], v[34:35], v[46:47]
	v_pk_add_f32 v[34:35], v[34:35], v[46:47] neg_lo:[0,1] neg_hi:[0,1]
	v_pk_add_f32 v[46:47], v[42:43], v[54:55]
	v_pk_add_f32 v[42:43], v[42:43], v[54:55] neg_lo:[0,1] neg_hi:[0,1]
	v_pk_add_f32 v[54:55], v[40:41], v[46:47]
	v_pk_add_f32 v[40:41], v[40:41], v[46:47] neg_lo:[0,1] neg_hi:[0,1]
	v_pk_add_f32 v[46:47], v[34:35], v[42:43] op_sel:[0,1] op_sel_hi:[1,0] neg_hi:[0,1]
	v_pk_add_f32 v[34:35], v[34:35], v[42:43] op_sel:[0,1] op_sel_hi:[1,0] neg_lo:[0,1]
	s_waitcnt lgkmcnt(1)
	v_pk_add_f32 v[42:43], v[36:37], v[56:57]
	v_pk_add_f32 v[36:37], v[36:37], v[56:57] neg_lo:[0,1] neg_hi:[0,1]
	s_waitcnt lgkmcnt(0)
	v_pk_add_f32 v[56:57], v[48:49], v[60:61]
	v_pk_add_f32 v[48:49], v[48:49], v[60:61] neg_lo:[0,1] neg_hi:[0,1]
	v_pk_add_f32 v[60:61], v[42:43], v[56:57]
	v_pk_add_f32 v[42:43], v[42:43], v[56:57] neg_lo:[0,1] neg_hi:[0,1]
	v_pk_add_f32 v[56:57], v[36:37], v[48:49] op_sel:[0,1] op_sel_hi:[1,0] neg_hi:[0,1]
	v_pk_add_f32 v[36:37], v[36:37], v[48:49] op_sel:[0,1] op_sel_hi:[1,0] neg_lo:[0,1]
	v_pk_add_f32 v[48:49], v[38:39], v[58:59]
	v_pk_add_f32 v[38:39], v[38:39], v[58:59] neg_lo:[0,1] neg_hi:[0,1]
	v_pk_add_f32 v[58:59], v[50:51], v[62:63]
	v_pk_add_f32 v[50:51], v[50:51], v[62:63] neg_lo:[0,1] neg_hi:[0,1]
	v_pk_add_f32 v[62:63], v[48:49], v[58:59]
	v_pk_add_f32 v[48:49], v[48:49], v[58:59] neg_lo:[0,1] neg_hi:[0,1]
	v_pk_add_f32 v[58:59], v[38:39], v[50:51] op_sel:[0,1] op_sel_hi:[1,0] neg_hi:[0,1]
	v_pk_add_f32 v[38:39], v[38:39], v[50:51] op_sel:[0,1] op_sel_hi:[1,0] neg_lo:[0,1]
	v_pk_mul_f32 v[50:51], v[46:47], s[6:7] op_sel:[0,0] op_sel_hi:[0,1]
	v_pk_fma_f32 v[50:51], v[46:47], s[6:7], v[50:51] op_sel:[1,1,0] op_sel_hi:[1,0,1] neg_lo:[0,1,0]
	v_pk_mul_f32 v[46:47], v[34:35], s[10:11] op_sel:[0,0] op_sel_hi:[0,1]
	v_pk_fma_f32 v[46:47], v[34:35], s[10:11], v[46:47] op_sel:[1,1,0] op_sel_hi:[1,0,1] neg_lo:[0,1,0]
	v_pk_add_f32 v[34:35], v[56:57], v[56:57] op_sel:[0,1] op_sel_hi:[1,0] neg_hi:[0,1]
	v_pk_add_f32 v[40:41], v[40:41], v[40:41] op_sel:[0,1] op_sel_hi:[1,0] neg_hi:[0,1]
	s_nop 0
	v_pk_mul_f32 v[56:57], v[58:59], s[10:11] op_sel:[0,0] op_sel_hi:[0,1]
	v_pk_fma_f32 v[56:57], v[58:59], s[10:11], v[56:57] op_sel:[1,1,0] op_sel_hi:[1,0,1] neg_lo:[0,1,0]
	v_pk_mul_f32 v[58:59], v[38:39], s[14:15] op_sel:[0,0] op_sel_hi:[0,1]
	v_pk_fma_f32 v[58:59], v[38:39], s[14:15], v[58:59] op_sel:[1,1,0] op_sel_hi:[1,0,1] neg_lo:[0,1,0]
	v_pk_add_f32 v[38:39], v[52:53], v[60:61]
	v_pk_mul_f32 v[34:35], v[34:35], s[8:9]
	v_pk_add_f32 v[52:53], v[52:53], v[60:61] neg_lo:[0,1] neg_hi:[0,1]
	v_pk_add_f32 v[60:61], v[54:55], v[62:63]
	v_pk_add_f32 v[54:55], v[54:55], v[62:63] neg_lo:[0,1] neg_hi:[0,1]
	v_pk_add_f32 v[36:37], v[36:37], v[36:37] op_sel:[0,1] op_sel_hi:[1,0] neg_lo:[0,1]
	v_pk_add_f32 v[48:49], v[48:49], v[48:49] op_sel:[0,1] op_sel_hi:[1,0] neg_lo:[0,1]
	v_pk_add_f32 v[62:63], v[38:39], v[60:61]
	v_pk_add_f32 v[60:61], v[38:39], v[60:61] neg_lo:[0,1] neg_hi:[0,1]
	v_pk_add_f32 v[66:67], v[52:53], v[54:55] op_sel:[0,1] op_sel_hi:[1,0] neg_hi:[0,1]
	v_pk_add_f32 v[52:53], v[52:53], v[54:55] op_sel:[0,1] op_sel_hi:[1,0] neg_lo:[0,1]
	v_pk_add_f32 v[38:39], v[64:65], v[34:35]
	v_pk_add_f32 v[34:35], v[64:65], v[34:35] neg_lo:[0,1] neg_hi:[0,1]
	v_pk_add_f32 v[54:55], v[50:51], v[56:57]
	v_pk_add_f32 v[50:51], v[50:51], v[56:57] neg_lo:[0,1] neg_hi:[0,1]
	v_pk_mul_f32 v[40:41], v[40:41], s[8:9]
	v_pk_mul_f32 v[36:37], v[36:37], s[12:13]
	v_pk_mul_f32 v[48:49], v[48:49], s[12:13]
	v_pk_add_f32 v[56:57], v[38:39], v[54:55]
	v_pk_add_f32 v[54:55], v[38:39], v[54:55] neg_lo:[0,1] neg_hi:[0,1]
	v_pk_add_f32 v[64:65], v[34:35], v[50:51] op_sel:[0,1] op_sel_hi:[1,0] neg_hi:[0,1]
	v_pk_add_f32 v[50:51], v[34:35], v[50:51] op_sel:[0,1] op_sel_hi:[1,0] neg_lo:[0,1]
	v_pk_add_f32 v[34:35], v[44:45], v[42:43] op_sel:[0,1] op_sel_hi:[1,0] neg_hi:[0,1]
	v_pk_add_f32 v[38:39], v[44:45], v[42:43] op_sel:[0,1] op_sel_hi:[1,0] neg_lo:[0,1]
	v_pk_add_f32 v[42:43], v[40:41], v[48:49]
	v_pk_add_f32 v[40:41], v[40:41], v[48:49] neg_lo:[0,1] neg_hi:[0,1]
	v_pk_add_f32 v[44:45], v[42:43], v[34:35]
	v_pk_add_f32 v[42:43], v[34:35], v[42:43] neg_lo:[0,1] neg_hi:[0,1]
	v_pk_add_f32 v[34:35], v[32:33], v[36:37]
	v_pk_add_f32 v[36:37], v[32:33], v[36:37] neg_lo:[0,1] neg_hi:[0,1]
	v_pk_add_f32 v[32:33], v[46:47], v[58:59]
	v_pk_add_f32 v[48:49], v[38:39], v[40:41] op_sel:[0,1] op_sel_hi:[1,0] neg_hi:[0,1]
	v_pk_add_f32 v[40:41], v[38:39], v[40:41] op_sel:[0,1] op_sel_hi:[1,0] neg_lo:[0,1]
	v_pk_add_f32 v[38:39], v[46:47], v[58:59] neg_lo:[0,1] neg_hi:[0,1]
	v_pk_add_f32 v[46:47], v[34:35], v[32:33]
	v_pk_add_f32 v[58:59], v[34:35], v[32:33] neg_lo:[0,1] neg_hi:[0,1]
	v_pk_add_f32 v[68:69], v[36:37], v[38:39] op_sel:[0,1] op_sel_hi:[1,0] neg_hi:[0,1]
	v_pk_add_f32 v[86:87], v[36:37], v[38:39] op_sel:[0,1] op_sel_hi:[1,0] neg_lo:[0,1]
	s_nop 0
	v_ashrrev_i32_e32 v32, 4, v88
	v_lshlrev_b32_e32 v90, 3, v32
	v_add_u32_e32 v91, 0x8800, v90
	v_and_b32_e32 v36, 15, v88
	ds_read2_b64 v[32:35], v91 offset0:16 offset1:32
	v_mad_u32_u24 v92, v36, s5, v90
	ds_read2_b64 v[36:39], v91 offset0:48 offset1:64
	s_waitcnt lgkmcnt(1)
	v_pk_mul_f32 v[88:89], v[56:57], v[32:33] op_sel:[0,0] op_sel_hi:[0,1]
	v_pk_fma_f32 v[88:89], v[56:57], v[32:33], v[88:89] op_sel:[1,1,0] op_sel_hi:[1,0,1] neg_lo:[0,1,0]
	v_pk_mul_f32 v[56:57], v[44:45], v[34:35] op_sel:[0,0] op_sel_hi:[0,1]
	v_pk_fma_f32 v[56:57], v[44:45], v[34:35], v[56:57] op_sel:[1,1,0] op_sel_hi:[1,0,1] neg_lo:[0,1,0]
	s_waitcnt lgkmcnt(0)
	v_pk_mul_f32 v[44:45], v[46:47], v[36:37] op_sel:[0,0] op_sel_hi:[0,1]
	v_pk_fma_f32 v[44:45], v[46:47], v[36:37], v[44:45] op_sel:[1,1,0] op_sel_hi:[1,0,1] neg_lo:[0,1,0]
	ds_write2_b64 v92, v[56:57], v[44:45] offset0:32 offset1:48
	v_pk_mul_f32 v[44:45], v[66:67], v[38:39] op_sel:[0,0] op_sel_hi:[0,1]
	v_pk_fma_f32 v[44:45], v[66:67], v[38:39], v[44:45] op_sel:[1,1,0] op_sel_hi:[1,0,1] neg_lo:[0,1,0]
	ds_read2_b64 v[32:35], v91 offset0:80 offset1:96
	s_waitcnt lgkmcnt(0)
	v_pk_mul_f32 v[46:47], v[64:65], v[32:33] op_sel:[0,0] op_sel_hi:[0,1]
	v_pk_fma_f32 v[46:47], v[64:65], v[32:33], v[46:47] op_sel:[1,1,0] op_sel_hi:[1,0,1] neg_lo:[0,1,0]
	ds_write2_b64 v92, v[44:45], v[46:47] offset0:64 offset1:80
	v_pk_mul_f32 v[44:45], v[48:49], v[34:35] op_sel:[0,0] op_sel_hi:[0,1]
	v_pk_fma_f32 v[44:45], v[48:49], v[34:35], v[44:45] op_sel:[1,1,0] op_sel_hi:[1,0,1] neg_lo:[0,1,0]
	ds_read2_b64 v[36:39], v91 offset0:112 offset1:128
	ds_read2_b64 v[32:35], v91 offset0:144 offset1:160
	s_waitcnt lgkmcnt(1)
	v_pk_mul_f32 v[46:47], v[68:69], v[36:37] op_sel:[0,0] op_sel_hi:[0,1]
	v_pk_fma_f32 v[46:47], v[68:69], v[36:37], v[46:47] op_sel:[1,1,0] op_sel_hi:[1,0,1] neg_lo:[0,1,0]
	ds_write2_b64 v92, v[44:45], v[46:47] offset0:96 offset1:112
	v_pk_mul_f32 v[44:45], v[60:61], v[38:39] op_sel:[0,0] op_sel_hi:[0,1]
	v_pk_fma_f32 v[44:45], v[60:61], v[38:39], v[44:45] op_sel:[1,1,0] op_sel_hi:[1,0,1] neg_lo:[0,1,0]
	ds_read2_b64 v[36:39], v91 offset0:176 offset1:192
	s_waitcnt lgkmcnt(2)
	v_pk_mul_f32 v[46:47], v[54:55], v[32:33] op_sel:[0,0] op_sel_hi:[0,1]
	v_pk_fma_f32 v[46:47], v[54:55], v[32:33], v[46:47] op_sel:[1,1,0] op_sel_hi:[1,0,1] neg_lo:[0,1,0]
	ds_write2_b64 v92, v[44:45], v[46:47] offset0:128 offset1:144
	v_pk_mul_f32 v[44:45], v[42:43], v[34:35] op_sel:[0,0] op_sel_hi:[0,1]
	v_pk_fma_f32 v[44:45], v[42:43], v[34:35], v[44:45] op_sel:[1,1,0] op_sel_hi:[1,0,1] neg_lo:[0,1,0]
	ds_read2_b64 v[32:35], v91 offset0:208 offset1:224
	s_waitcnt lgkmcnt(2)
	v_pk_mul_f32 v[42:43], v[58:59], v[36:37] op_sel:[0,0] op_sel_hi:[0,1]
	v_pk_fma_f32 v[42:43], v[58:59], v[36:37], v[42:43] op_sel:[1,1,0] op_sel_hi:[1,0,1] neg_lo:[0,1,0]
	ds_write2_b64 v92, v[44:45], v[42:43] offset0:160 offset1:176
	v_pk_mul_f32 v[42:43], v[52:53], v[38:39] op_sel:[0,0] op_sel_hi:[0,1]
	v_pk_fma_f32 v[42:43], v[52:53], v[38:39], v[42:43] op_sel:[1,1,0] op_sel_hi:[1,0,1] neg_lo:[0,1,0]
	s_waitcnt lgkmcnt(1)
	v_pk_mul_f32 v[38:39], v[50:51], v[32:33] op_sel:[0,0] op_sel_hi:[0,1]
	v_pk_fma_f32 v[38:39], v[50:51], v[32:33], v[38:39] op_sel:[1,1,0] op_sel_hi:[1,0,1] neg_lo:[0,1,0]
	v_pk_mul_f32 v[32:33], v[40:41], v[34:35] op_sel:[0,0] op_sel_hi:[0,1]
	v_pk_fma_f32 v[32:33], v[40:41], v[34:35], v[32:33] op_sel:[1,1,0] op_sel_hi:[1,0,1] neg_lo:[0,1,0]
	ds_read_b64 v[36:37], v90 offset:36736
	s_waitcnt lgkmcnt(0)
	v_pk_mul_f32 v[34:35], v[86:87], v[36:37] op_sel:[0,0] op_sel_hi:[0,1]
	v_pk_fma_f32 v[34:35], v[86:87], v[36:37], v[34:35] op_sel:[1,1,0] op_sel_hi:[1,0,1] neg_lo:[0,1,0]
	ds_write2_b64 v92, v[32:33], v[34:35] offset0:224 offset1:240
	v_mov_b32_e32 v32, v0
	ds_write2_b64 v92, v[62:63], v[88:89] offset1:16
	ds_write2_b64 v92, v[42:43], v[38:39] offset0:192 offset1:208
	s_waitcnt lgkmcnt(0)
	s_barrier
	s_nop 0
	v_and_b32_e32 v33, 15, v32
	v_and_b32_e32 v32, 0x1ffffff0, v32
	v_lshlrev_b32_e32 v32, 3, v32
	v_mad_u32_u24 v60, v33, s5, v32
	ds_read2_b64 v[32:35], v60 offset1:1
	ds_read2_b64 v[36:39], v60 offset0:2 offset1:3
	ds_read2_b64 v[40:43], v60 offset0:8 offset1:9
	ds_read2_b64 v[44:47], v60 offset0:4 offset1:5
	ds_read2_b64 v[48:51], v60 offset0:6 offset1:7
	ds_read2_b64 v[52:55], v60 offset0:12 offset1:13
	ds_read2_b64 v[56:59], v60 offset0:10 offset1:11
	ds_read2_b64 v[60:63], v60 offset0:14 offset1:15
	s_waitcnt lgkmcnt(5)
	v_pk_add_f32 v[64:65], v[32:33], v[40:41]
	v_pk_add_f32 v[32:33], v[32:33], v[40:41] neg_lo:[0,1] neg_hi:[0,1]
	s_waitcnt lgkmcnt(2)
	v_pk_add_f32 v[40:41], v[44:45], v[52:53]
	v_pk_add_f32 v[44:45], v[44:45], v[52:53] neg_lo:[0,1] neg_hi:[0,1]
	v_pk_add_f32 v[52:53], v[64:65], v[40:41]
	v_pk_add_f32 v[40:41], v[64:65], v[40:41] neg_lo:[0,1] neg_hi:[0,1]
	v_pk_add_f32 v[64:65], v[32:33], v[44:45] op_sel:[0,1] op_sel_hi:[1,0] neg_hi:[0,1]
	v_pk_add_f32 v[66:67], v[32:33], v[44:45] op_sel:[0,1] op_sel_hi:[1,0] neg_lo:[0,1]
	v_pk_add_f32 v[32:33], v[34:35], v[42:43]
	v_pk_add_f32 v[34:35], v[34:35], v[42:43] neg_lo:[0,1] neg_hi:[0,1]
	v_pk_add_f32 v[42:43], v[46:47], v[54:55]
	v_pk_add_f32 v[44:45], v[46:47], v[54:55] neg_lo:[0,1] neg_hi:[0,1]
	v_pk_add_f32 v[46:47], v[32:33], v[42:43]
	v_pk_add_f32 v[32:33], v[32:33], v[42:43] neg_lo:[0,1] neg_hi:[0,1]
	v_pk_add_f32 v[42:43], v[34:35], v[44:45] op_sel:[0,1] op_sel_hi:[1,0] neg_hi:[0,1]
	v_pk_add_f32 v[34:35], v[34:35], v[44:45] op_sel:[0,1] op_sel_hi:[1,0] neg_lo:[0,1]
	s_waitcnt lgkmcnt(1)
	v_pk_add_f32 v[44:45], v[36:37], v[56:57]
	s_waitcnt lgkmcnt(0)
	v_pk_add_f32 v[54:55], v[48:49], v[60:61]
	v_pk_add_f32 v[32:33], v[32:33], v[32:33] op_sel:[0,1] op_sel_hi:[1,0] neg_hi:[0,1]
	v_pk_add_f32 v[36:37], v[36:37], v[56:57] neg_lo:[0,1] neg_hi:[0,1]
	v_pk_add_f32 v[48:49], v[48:49], v[60:61] neg_lo:[0,1] neg_hi:[0,1]
	v_pk_add_f32 v[56:57], v[44:45], v[54:55]
	v_pk_add_f32 v[54:55], v[44:45], v[54:55] neg_lo:[0,1] neg_hi:[0,1]
	v_pk_add_f32 v[44:45], v[36:37], v[48:49] op_sel:[0,1] op_sel_hi:[1,0] neg_hi:[0,1]
	v_pk_mul_f32 v[68:69], v[32:33], s[8:9]
	v_pk_add_f32 v[36:37], v[36:37], v[48:49] op_sel:[0,1] op_sel_hi:[1,0] neg_lo:[0,1]
	v_pk_add_f32 v[48:49], v[38:39], v[58:59]
	v_pk_add_f32 v[32:33], v[44:45], v[44:45] op_sel:[0,1] op_sel_hi:[1,0] neg_hi:[0,1]
	v_pk_add_f32 v[38:39], v[38:39], v[58:59] neg_lo:[0,1] neg_hi:[0,1]
	v_pk_add_f32 v[58:59], v[50:51], v[62:63]
	v_pk_mul_f32 v[86:87], v[34:35], s[10:11] op_sel:[0,0] op_sel_hi:[0,1]
	v_pk_fma_f32 v[86:87], v[34:35], s[10:11], v[86:87] op_sel:[1,1,0] op_sel_hi:[1,0,1] neg_lo:[0,1,0]
	v_pk_mul_f32 v[34:35], v[32:33], s[8:9]
	v_pk_add_f32 v[32:33], v[36:37], v[36:37] op_sel:[0,1] op_sel_hi:[1,0] neg_lo:[0,1]
	v_pk_add_f32 v[50:51], v[50:51], v[62:63] neg_lo:[0,1] neg_hi:[0,1]
	v_pk_add_f32 v[60:61], v[48:49], v[58:59]
	v_pk_add_f32 v[48:49], v[48:49], v[58:59] neg_lo:[0,1] neg_hi:[0,1]
	v_pk_add_f32 v[58:59], v[38:39], v[50:51] op_sel:[0,1] op_sel_hi:[1,0] neg_hi:[0,1]
	v_pk_add_f32 v[38:39], v[38:39], v[50:51] op_sel:[0,1] op_sel_hi:[1,0] neg_lo:[0,1]
	v_pk_mul_f32 v[88:89], v[32:33], s[12:13]
	v_pk_add_f32 v[36:37], v[46:47], v[60:61]
	v_pk_add_f32 v[32:33], v[48:49], v[48:49] op_sel:[0,1] op_sel_hi:[1,0] neg_lo:[0,1]
	v_pk_mul_f32 v[44:45], v[58:59], s[10:11] op_sel:[0,0] op_sel_hi:[0,1]
	v_pk_fma_f32 v[44:45], v[58:59], s[10:11], v[44:45] op_sel:[1,1,0] op_sel_hi:[1,0,1] neg_lo:[0,1,0]
	v_pk_mul_f32 v[58:59], v[38:39], s[14:15] op_sel:[0,0] op_sel_hi:[0,1]
	v_pk_fma_f32 v[58:59], v[38:39], s[14:15], v[58:59] op_sel:[1,1,0] op_sel_hi:[1,0,1] neg_lo:[0,1,0]
	v_pk_add_f32 v[38:39], v[52:53], v[56:57] neg_lo:[0,1] neg_hi:[0,1]
	v_pk_mul_f32 v[48:49], v[32:33], s[12:13]
	v_pk_add_f32 v[32:33], v[52:53], v[56:57]
	v_pk_add_f32 v[46:47], v[46:47], v[60:61] neg_lo:[0,1] neg_hi:[0,1]
	v_pk_mul_f32 v[62:63], v[42:43], s[6:7] op_sel:[0,0] op_sel_hi:[0,1]
	v_pk_fma_f32 v[62:63], v[42:43], s[6:7], v[62:63] op_sel:[1,1,0] op_sel_hi:[1,0,1] neg_lo:[0,1,0]
	v_pk_add_f32 v[50:51], v[32:33], v[36:37]
	v_pk_add_f32 v[36:37], v[32:33], v[36:37] neg_lo:[0,1] neg_hi:[0,1]
	v_pk_add_f32 v[42:43], v[38:39], v[46:47] op_sel:[0,1] op_sel_hi:[1,0] neg_hi:[0,1]
	v_pk_add_f32 v[32:33], v[38:39], v[46:47] op_sel:[0,1] op_sel_hi:[1,0] neg_lo:[0,1]
	v_pk_add_f32 v[38:39], v[64:65], v[34:35]
	v_pk_add_f32 v[34:35], v[64:65], v[34:35] neg_lo:[0,1] neg_hi:[0,1]
	v_pk_add_f32 v[46:47], v[62:63], v[44:45]
	v_pk_add_f32 v[56:57], v[62:63], v[44:45] neg_lo:[0,1] neg_hi:[0,1]
	v_pk_add_f32 v[52:53], v[38:39], v[46:47]
	v_pk_add_f32 v[38:39], v[38:39], v[46:47] neg_lo:[0,1] neg_hi:[0,1]
	v_pk_add_f32 v[44:45], v[34:35], v[56:57] op_sel:[0,1] op_sel_hi:[1,0] neg_hi:[0,1]
	v_pk_add_f32 v[34:35], v[34:35], v[56:57] op_sel:[0,1] op_sel_hi:[1,0] neg_lo:[0,1]
	v_pk_add_f32 v[46:47], v[40:41], v[54:55] op_sel:[0,1] op_sel_hi:[1,0] neg_hi:[0,1]
	v_pk_add_f32 v[56:57], v[40:41], v[54:55] op_sel:[0,1] op_sel_hi:[1,0] neg_lo:[0,1]
	v_pk_add_f32 v[40:41], v[68:69], v[48:49]
	v_pk_add_f32 v[60:61], v[68:69], v[48:49] neg_lo:[0,1] neg_hi:[0,1]
	v_pk_add_f32 v[54:55], v[40:41], v[46:47]
	v_pk_add_f32 v[40:41], v[46:47], v[40:41] neg_lo:[0,1] neg_hi:[0,1]
	v_pk_add_f32 v[46:47], v[66:67], v[88:89]
	v_pk_add_f32 v[62:63], v[86:87], v[58:59]
	v_pk_add_f32 v[58:59], v[86:87], v[58:59] neg_lo:[0,1] neg_hi:[0,1]
	v_pk_add_f32 v[48:49], v[56:57], v[60:61] op_sel:[0,1] op_sel_hi:[1,0] neg_hi:[0,1]
	v_pk_add_f32 v[64:65], v[56:57], v[60:61] op_sel:[0,1] op_sel_hi:[1,0] neg_lo:[0,1]
	v_pk_add_f32 v[60:61], v[66:67], v[88:89] neg_lo:[0,1] neg_hi:[0,1]
	v_pk_add_f32 v[56:57], v[46:47], v[62:63]
	v_pk_add_f32 v[68:69], v[46:47], v[62:63] neg_lo:[0,1] neg_hi:[0,1]
	v_pk_add_f32 v[46:47], v[60:61], v[58:59] op_sel:[0,1] op_sel_hi:[1,0] neg_hi:[0,1]
	v_pk_add_f32 v[66:67], v[60:61], v[58:59] op_sel:[0,1] op_sel_hi:[1,0] neg_lo:[0,1]
	v_mov_b32_e32 v58, v0
	s_nop 0
	v_and_b32_e32 v59, -16, v58
	v_and_b32_e32 v60, 15, v58
	v_lshlrev_b32_e32 v61, 3, v59
	v_mad_u32_u24 v61, v60, s5, v61
	v_cmp_ne_u32_e32 vcc, 0, v60
	ds_write2_b64 v61, v[50:51], v[52:53] offset1:1
	ds_write2_b64 v61, v[54:55], v[56:57] offset0:2 offset1:3
	ds_write2_b64 v61, v[42:43], v[44:45] offset0:4 offset1:5
	ds_write2_b64 v61, v[48:49], v[46:47] offset0:6 offset1:7
	ds_write2_b64 v61, v[36:37], v[38:39] offset0:8 offset1:9
	ds_write2_b64 v61, v[40:41], v[68:69] offset0:10 offset1:11
	ds_write2_b64 v61, v[32:33], v[34:35] offset0:12 offset1:13
	ds_write2_b64 v61, v[64:65], v[66:67] offset0:14 offset1:15
	s_waitcnt lgkmcnt(0)
	s_barrier
	s_and_saveexec_b64 s[6:7], vcc
	s_xor_b64 s[6:7], exec, s[6:7]
	v_sub_u32_e32 v60, 16, v60
	v_mul_u32_u24_e32 v60, 0x111, v60
	v_sub_u32_e32 v59, v60, v59
	v_add_u32_e32 v61, 0xf0, v59
	s_andn2_saveexec_b64 s[6:7], s[6:7]
	v_sub_u32_e32 v59, 0x100, v58
	v_cmp_lt_u32_e32 vcc, 15, v58
	s_nop 1
	v_cndmask_b32_e32 v61, 1, v59, vcc
	s_or_b64 exec, exec, s[6:7]
	v_mov_b32_e32 v59, 0
	v_lshlrev_b32_e32 v92, 3, v61
	ds_read_b64 v[90:91], v59
	ds_read2_b64 v[60:63], v92 offset0:14 offset1:15
	ds_read2_b64 v[86:89], v92 offset0:12 offset1:13
	v_cmp_eq_u32_e32 vcc, 0, v58
	v_cvt_f32_fp8_sdwa v93, v74 src0_sel:BYTE_3
	v_cvt_f32_fp8_sdwa v94, v72 src0_sel:BYTE_1
	s_waitcnt lgkmcnt(1)
	v_cndmask_b32_e32 v59, v63, v91, vcc
	v_cndmask_b32_e32 v58, v62, v90, vcc
	v_pk_add_f32 v[90:91], v[50:51], v[58:59] neg_hi:[0,1]
	v_pk_add_f32 v[50:51], v[50:51], v[58:59] neg_lo:[0,1]
	v_cvt_f32_fp8_sdwa v95, v72 src0_sel:BYTE_3
	v_pk_mul_f32 v[62:63], v[90:91], v[50:51] op_sel:[0,0] op_sel_hi:[0,1]
	v_pk_fma_f32 v[62:63], v[90:91], v[50:51], v[62:63] op_sel:[1,1,0] op_sel_hi:[1,0,1] neg_hi:[0,1,0]
	v_pk_add_f32 v[50:51], v[52:53], v[60:61] neg_hi:[0,1]
	v_pk_add_f32 v[52:53], v[52:53], v[60:61] neg_lo:[0,1]
	v_cvt_f32_fp8_sdwa v72, v71 src0_sel:BYTE_1
	v_pk_mul_f32 v[60:61], v[50:51], v[52:53] op_sel:[0,0] op_sel_hi:[0,1]
	v_pk_fma_f32 v[60:61], v[50:51], v[52:53], v[60:61] op_sel:[1,1,0] op_sel_hi:[1,0,1] neg_hi:[0,1,0]
	s_waitcnt lgkmcnt(0)
	v_pk_add_f32 v[50:51], v[54:55], v[88:89] neg_hi:[0,1]
	v_pk_add_f32 v[52:53], v[54:55], v[88:89] neg_lo:[0,1]
	v_pk_add_f32 v[54:55], v[56:57], v[86:87] neg_hi:[0,1]
	v_pk_add_f32 v[86:87], v[56:57], v[86:87] neg_lo:[0,1]
	v_cvt_f32_fp8_sdwa v98, v70 src0_sel:BYTE_1
	v_pk_mul_f32 v[58:59], v[50:51], v[52:53] op_sel:[0,0] op_sel_hi:[0,1]
	v_pk_fma_f32 v[58:59], v[50:51], v[52:53], v[58:59] op_sel:[1,1,0] op_sel_hi:[1,0,1] neg_hi:[0,1,0]
	ds_read2_b64 v[50:53], v92 offset0:10 offset1:11
	v_pk_mul_f32 v[56:57], v[54:55], v[86:87] op_sel:[0,0] op_sel_hi:[0,1]
	v_pk_fma_f32 v[56:57], v[54:55], v[86:87], v[56:57] op_sel:[1,1,0] op_sel_hi:[1,0,1] neg_hi:[0,1,0]
	ds_read2_b64 v[86:89], v92 offset0:8 offset1:9
	s_waitcnt lgkmcnt(1)
	v_pk_add_f32 v[90:91], v[42:43], v[52:53] neg_hi:[0,1]
	v_pk_add_f32 v[42:43], v[42:43], v[52:53] neg_lo:[0,1]
	v_cvt_f32_fp8_sdwa v99, v70 src0_sel:BYTE_3
	v_pk_mul_f32 v[54:55], v[90:91], v[42:43] op_sel:[0,0] op_sel_hi:[0,1]
	v_pk_fma_f32 v[54:55], v[90:91], v[42:43], v[54:55] op_sel:[1,1,0] op_sel_hi:[1,0,1] neg_hi:[0,1,0]
	v_pk_add_f32 v[42:43], v[44:45], v[50:51] neg_hi:[0,1]
	v_pk_add_f32 v[44:45], v[44:45], v[50:51] neg_lo:[0,1]
	s_mov_b32 s6, 0x3f6c835e
	v_pk_mul_f32 v[52:53], v[42:43], v[44:45] op_sel:[0,0] op_sel_hi:[0,1]
	v_pk_fma_f32 v[52:53], v[42:43], v[44:45], v[52:53] op_sel:[1,1,0] op_sel_hi:[1,0,1] neg_hi:[0,1,0]
	s_waitcnt lgkmcnt(0)
	v_pk_add_f32 v[42:43], v[48:49], v[88:89] neg_hi:[0,1]
	v_pk_add_f32 v[44:45], v[48:49], v[88:89] neg_lo:[0,1]
	v_pk_add_f32 v[88:89], v[46:47], v[86:87] neg_hi:[0,1]
	v_pk_add_f32 v[46:47], v[46:47], v[86:87] neg_lo:[0,1]
	s_mov_b32 s7, 0xbec3ef15
	v_pk_mul_f32 v[50:51], v[42:43], v[44:45] op_sel:[0,0] op_sel_hi:[0,1]
	v_pk_fma_f32 v[50:51], v[42:43], v[44:45], v[50:51] op_sel:[1,1,0] op_sel_hi:[1,0,1] neg_hi:[0,1,0]
	ds_read2_b64 v[42:45], v92 offset0:6 offset1:7
	v_pk_mul_f32 v[48:49], v[88:89], v[46:47] op_sel:[0,0] op_sel_hi:[0,1]
	v_pk_fma_f32 v[48:49], v[88:89], v[46:47], v[48:49] op_sel:[1,1,0] op_sel_hi:[1,0,1] neg_hi:[0,1,0]
	ds_read2_b64 v[86:89], v92 offset0:4 offset1:5
	s_waitcnt lgkmcnt(1)
	v_pk_add_f32 v[90:91], v[36:37], v[44:45] neg_hi:[0,1]
	v_pk_add_f32 v[36:37], v[36:37], v[44:45] neg_lo:[0,1]
	s_mov_b32 s9, s8
	v_pk_mul_f32 v[46:47], v[90:91], v[36:37] op_sel:[0,0] op_sel_hi:[0,1]
	v_pk_fma_f32 v[46:47], v[90:91], v[36:37], v[46:47] op_sel:[1,1,0] op_sel_hi:[1,0,1] neg_hi:[0,1,0]
	v_pk_add_f32 v[36:37], v[38:39], v[42:43] neg_hi:[0,1]
	v_pk_add_f32 v[38:39], v[38:39], v[42:43] neg_lo:[0,1]
	v_cvt_f32_fp8_sdwa v90, v76 src0_sel:BYTE_1
	v_pk_mul_f32 v[44:45], v[36:37], v[38:39] op_sel:[0,0] op_sel_hi:[0,1]
	v_pk_fma_f32 v[44:45], v[36:37], v[38:39], v[44:45] op_sel:[1,1,0] op_sel_hi:[1,0,1] neg_hi:[0,1,0]
	s_waitcnt lgkmcnt(0)
	v_pk_add_f32 v[36:37], v[40:41], v[88:89] neg_hi:[0,1]
	v_pk_add_f32 v[38:39], v[40:41], v[88:89] neg_lo:[0,1]
	v_pk_add_f32 v[88:89], v[68:69], v[86:87] neg_hi:[0,1]
	v_pk_add_f32 v[68:69], v[68:69], v[86:87] neg_lo:[0,1]
	v_cvt_f32_fp8_sdwa v91, v76 src0_sel:BYTE_3
	v_pk_mul_f32 v[42:43], v[36:37], v[38:39] op_sel:[0,0] op_sel_hi:[0,1]
	v_pk_fma_f32 v[42:43], v[36:37], v[38:39], v[42:43] op_sel:[1,1,0] op_sel_hi:[1,0,1] neg_hi:[0,1,0]
	ds_read2_b64 v[36:39], v92 offset0:2 offset1:3
	v_pk_mul_f32 v[40:41], v[88:89], v[68:69] op_sel:[0,0] op_sel_hi:[0,1]
	v_pk_fma_f32 v[40:41], v[88:89], v[68:69], v[40:41] op_sel:[1,1,0] op_sel_hi:[1,0,1] neg_hi:[0,1,0]
	ds_read2_b64 v[86:89], v92 offset1:1
	s_waitcnt lgkmcnt(1)
	v_pk_add_f32 v[68:69], v[32:33], v[38:39] neg_hi:[0,1]
	v_pk_add_f32 v[32:33], v[32:33], v[38:39] neg_lo:[0,1]
	v_cvt_f32_fp8_sdwa v76, v75 src0_sel:BYTE_1
	v_pk_mul_f32 v[38:39], v[68:69], v[32:33] op_sel:[0,0] op_sel_hi:[0,1]
	v_pk_fma_f32 v[38:39], v[68:69], v[32:33], v[38:39] op_sel:[1,1,0] op_sel_hi:[1,0,1] neg_hi:[0,1,0]
	v_pk_add_f32 v[32:33], v[34:35], v[36:37] neg_hi:[0,1]
	v_pk_add_f32 v[34:35], v[34:35], v[36:37] neg_lo:[0,1]
	v_cvt_f32_fp8_sdwa v68, v83 src0_sel:BYTE_1
	v_pk_mul_f32 v[36:37], v[32:33], v[34:35] op_sel:[0,0] op_sel_hi:[0,1]
	v_pk_fma_f32 v[36:37], v[32:33], v[34:35], v[36:37] op_sel:[1,1,0] op_sel_hi:[1,0,1] neg_hi:[0,1,0]
	s_waitcnt lgkmcnt(0)
	v_pk_add_f32 v[32:33], v[64:65], v[88:89] neg_hi:[0,1]
	v_pk_add_f32 v[64:65], v[64:65], v[88:89] neg_lo:[0,1]
	v_cvt_f32_fp8_sdwa v69, v83 src0_sel:BYTE_3
	v_pk_mul_f32 v[34:35], v[32:33], v[64:65] op_sel:[0,0] op_sel_hi:[0,1]
	v_pk_fma_f32 v[34:35], v[32:33], v[64:65], v[34:35] op_sel:[1,1,0] op_sel_hi:[1,0,1] neg_hi:[0,1,0]
	v_pk_add_f32 v[64:65], v[66:67], v[86:87] neg_hi:[0,1]
	v_pk_add_f32 v[66:67], v[66:67], v[86:87] neg_lo:[0,1]
	v_cvt_f32_fp8_sdwa v83, v81 src0_sel:BYTE_3
	v_pk_mul_f32 v[32:33], v[64:65], v[66:67] op_sel:[0,0] op_sel_hi:[0,1]
	v_pk_fma_f32 v[32:33], v[64:65], v[66:67], v[32:33] op_sel:[1,1,0] op_sel_hi:[1,0,1] neg_hi:[0,1,0]
	v_cvt_f32_fp8_sdwa v64, v85 src0_sel:BYTE_1
	v_cvt_f32_fp8_sdwa v65, v85 src0_sel:BYTE_3
	v_cvt_f32_fp8_sdwa v66, v84 src0_sel:BYTE_1
	v_cvt_f32_fp8_sdwa v67, v84 src0_sel:BYTE_3
	v_cvt_f32_fp8_sdwa v84, v82 src0_sel:BYTE_1
	v_cvt_f32_fp8_sdwa v85, v82 src0_sel:BYTE_3
	v_cvt_f32_fp8_sdwa v82, v81 src0_sel:BYTE_1
	v_cvt_f32_fp8_sdwa v86, v80 src0_sel:BYTE_1
	v_cvt_f32_fp8_sdwa v87, v80 src0_sel:BYTE_3
	v_cvt_f32_fp8_sdwa v80, v79 src0_sel:BYTE_1
	v_cvt_f32_fp8_sdwa v81, v79 src0_sel:BYTE_3
	v_cvt_f32_fp8_sdwa v88, v78 src0_sel:BYTE_1
	v_cvt_f32_fp8_sdwa v89, v78 src0_sel:BYTE_3
	v_cvt_f32_fp8_sdwa v78, v77 src0_sel:BYTE_1
	v_cvt_f32_fp8_sdwa v79, v77 src0_sel:BYTE_3
	v_cvt_f32_fp8_sdwa v77, v75 src0_sel:BYTE_3
	v_cvt_f32_fp8_sdwa v92, v74 src0_sel:BYTE_1
	v_cvt_f32_fp8_sdwa v74, v73 src0_sel:BYTE_1
	v_cvt_f32_fp8_sdwa v75, v73 src0_sel:BYTE_3
	v_cvt_f32_fp8_sdwa v73, v71 src0_sel:BYTE_3
	v_pk_add_f32 v[70:71], v[64:65], v[78:79]
	v_pk_add_f32 v[64:65], v[64:65], v[78:79] neg_lo:[0,1] neg_hi:[0,1]
	v_pk_add_f32 v[78:79], v[82:83], v[74:75]
	v_pk_add_f32 v[74:75], v[82:83], v[74:75] neg_lo:[0,1] neg_hi:[0,1]
	v_pk_add_f32 v[82:83], v[70:71], v[78:79]
	v_pk_add_f32 v[70:71], v[70:71], v[78:79] neg_lo:[0,1] neg_hi:[0,1]
	v_pk_add_f32 v[78:79], v[64:65], v[74:75] op_sel:[0,1] op_sel_hi:[1,0] neg_hi:[0,1]
	v_pk_add_f32 v[64:65], v[64:65], v[74:75] op_sel:[0,1] op_sel_hi:[1,0] neg_lo:[0,1]
	v_pk_add_f32 v[74:75], v[66:67], v[90:91]
	v_pk_add_f32 v[66:67], v[66:67], v[90:91] neg_lo:[0,1] neg_hi:[0,1]
	v_pk_add_f32 v[90:91], v[86:87], v[94:95]
	v_pk_add_f32 v[86:87], v[86:87], v[94:95] neg_lo:[0,1] neg_hi:[0,1]
	v_pk_add_f32 v[94:95], v[74:75], v[90:91]
	v_pk_add_f32 v[74:75], v[74:75], v[90:91] neg_lo:[0,1] neg_hi:[0,1]
	v_pk_add_f32 v[90:91], v[66:67], v[86:87] op_sel:[0,1] op_sel_hi:[1,0] neg_hi:[0,1]
	v_pk_add_f32 v[66:67], v[66:67], v[86:87] op_sel:[0,1] op_sel_hi:[1,0] neg_lo:[0,1]
	v_pk_add_f32 v[86:87], v[68:69], v[76:77]
	v_pk_add_f32 v[68:69], v[68:69], v[76:77] neg_lo:[0,1] neg_hi:[0,1]
	v_pk_add_f32 v[76:77], v[80:81], v[72:73]
	v_pk_add_f32 v[72:73], v[80:81], v[72:73] neg_lo:[0,1] neg_hi:[0,1]
	v_pk_add_f32 v[80:81], v[86:87], v[76:77]
	v_pk_add_f32 v[76:77], v[86:87], v[76:77] neg_lo:[0,1] neg_hi:[0,1]
	v_pk_add_f32 v[86:87], v[68:69], v[72:73] op_sel:[0,1] op_sel_hi:[1,0] neg_hi:[0,1]
	v_pk_add_f32 v[68:69], v[68:69], v[72:73] op_sel:[0,1] op_sel_hi:[1,0] neg_lo:[0,1]
	v_pk_add_f32 v[72:73], v[84:85], v[92:93]
	v_pk_add_f32 v[84:85], v[84:85], v[92:93] neg_lo:[0,1] neg_hi:[0,1]
	v_pk_add_f32 v[92:93], v[88:89], v[98:99]
	v_pk_add_f32 v[88:89], v[88:89], v[98:99] neg_lo:[0,1] neg_hi:[0,1]
	v_pk_add_f32 v[98:99], v[72:73], v[92:93]
	v_pk_add_f32 v[72:73], v[72:73], v[92:93] neg_lo:[0,1] neg_hi:[0,1]
	v_pk_add_f32 v[92:93], v[84:85], v[88:89] op_sel:[0,1] op_sel_hi:[1,0] neg_hi:[0,1]
	v_pk_add_f32 v[84:85], v[84:85], v[88:89] op_sel:[0,1] op_sel_hi:[1,0] neg_lo:[0,1]
	v_pk_mul_f32 v[88:89], v[90:91], s[6:7] op_sel:[0,0] op_sel_hi:[0,1]
	v_pk_fma_f32 v[88:89], v[90:91], s[6:7], v[88:89] op_sel:[1,1,0] op_sel_hi:[1,0,1] neg_lo:[0,1,0]
	v_pk_mul_f32 v[90:91], v[66:67], s[10:11] op_sel:[0,0] op_sel_hi:[0,1]
	v_pk_fma_f32 v[90:91], v[66:67], s[10:11], v[90:91] op_sel:[1,1,0] op_sel_hi:[1,0,1] neg_lo:[0,1,0]
	v_pk_add_f32 v[66:67], v[86:87], v[86:87] op_sel:[0,1] op_sel_hi:[1,0] neg_hi:[0,1]
	s_nop 0
	v_pk_add_f32 v[72:73], v[72:73], v[72:73] op_sel:[0,1] op_sel_hi:[1,0] neg_lo:[0,1]
	v_pk_mul_f32 v[86:87], v[92:93], s[10:11] op_sel:[0,0] op_sel_hi:[0,1]
	v_pk_fma_f32 v[86:87], v[92:93], s[10:11], v[86:87] op_sel:[1,1,0] op_sel_hi:[1,0,1] neg_lo:[0,1,0]
	s_mov_b32 s14, s11
	v_pk_mul_f32 v[66:67], v[66:67], s[8:9]
	s_mov_b32 s15, s10
	v_pk_mul_f32 v[92:93], v[84:85], s[14:15] op_sel:[0,0] op_sel_hi:[0,1]
	v_pk_fma_f32 v[92:93], v[84:85], s[14:15], v[92:93] op_sel:[1,1,0] op_sel_hi:[1,0,1] neg_lo:[0,1,0]
	v_pk_add_f32 v[84:85], v[82:83], v[80:81]
	v_pk_add_f32 v[80:81], v[82:83], v[80:81] neg_lo:[0,1] neg_hi:[0,1]
	v_pk_add_f32 v[82:83], v[94:95], v[98:99]
	v_pk_add_f32 v[94:95], v[94:95], v[98:99] neg_lo:[0,1] neg_hi:[0,1]
	v_pk_add_f32 v[74:75], v[74:75], v[74:75] op_sel:[0,1] op_sel_hi:[1,0] neg_hi:[0,1]
	v_pk_add_f32 v[68:69], v[68:69], v[68:69] op_sel:[0,1] op_sel_hi:[1,0] neg_lo:[0,1]
	s_mov_b32 s13, s12
	v_pk_mul_f32 v[72:73], v[72:73], s[12:13]
	v_pk_add_f32 v[98:99], v[84:85], v[82:83]
	v_pk_add_f32 v[82:83], v[84:85], v[82:83] neg_lo:[0,1] neg_hi:[0,1]
	v_pk_add_f32 v[84:85], v[80:81], v[94:95] op_sel:[0,1] op_sel_hi:[1,0] neg_hi:[0,1]
	v_pk_add_f32 v[80:81], v[80:81], v[94:95] op_sel:[0,1] op_sel_hi:[1,0] neg_lo:[0,1]
	v_pk_add_f32 v[94:95], v[78:79], v[66:67]
	v_pk_add_f32 v[66:67], v[78:79], v[66:67] neg_lo:[0,1] neg_hi:[0,1]
	v_pk_add_f32 v[78:79], v[88:89], v[86:87]
	v_pk_add_f32 v[86:87], v[88:89], v[86:87] neg_lo:[0,1] neg_hi:[0,1]
	v_pk_mul_f32 v[74:75], v[74:75], s[8:9]
	v_pk_mul_f32 v[68:69], v[68:69], s[12:13]
	v_pk_add_f32 v[88:89], v[94:95], v[78:79]
	v_pk_add_f32 v[78:79], v[94:95], v[78:79] neg_lo:[0,1] neg_hi:[0,1]
	v_pk_add_f32 v[94:95], v[66:67], v[86:87] op_sel:[0,1] op_sel_hi:[1,0] neg_hi:[0,1]
	v_pk_add_f32 v[66:67], v[66:67], v[86:87] op_sel:[0,1] op_sel_hi:[1,0] neg_lo:[0,1]
	v_pk_add_f32 v[86:87], v[70:71], v[76:77] op_sel:[0,1] op_sel_hi:[1,0] neg_hi:[0,1]
	v_pk_add_f32 v[70:71], v[70:71], v[76:77] op_sel:[0,1] op_sel_hi:[1,0] neg_lo:[0,1]
	v_pk_add_f32 v[76:77], v[74:75], v[72:73]
	v_pk_add_f32 v[72:73], v[74:75], v[72:73] neg_lo:[0,1] neg_hi:[0,1]
	v_pk_add_f32 v[74:75], v[76:77], v[86:87]
	v_pk_add_f32 v[76:77], v[86:87], v[76:77] neg_lo:[0,1] neg_hi:[0,1]
	v_pk_add_f32 v[86:87], v[70:71], v[72:73] op_sel:[0,1] op_sel_hi:[1,0] neg_hi:[0,1]
	v_pk_add_f32 v[70:71], v[70:71], v[72:73] op_sel:[0,1] op_sel_hi:[1,0] neg_lo:[0,1]
	v_pk_add_f32 v[72:73], v[64:65], v[68:69]
	v_pk_add_f32 v[64:65], v[64:65], v[68:69] neg_lo:[0,1] neg_hi:[0,1]
	v_pk_add_f32 v[68:69], v[90:91], v[92:93]
	v_pk_add_f32 v[90:91], v[90:91], v[92:93] neg_lo:[0,1] neg_hi:[0,1]
	v_pk_add_f32 v[92:93], v[72:73], v[68:69]
	v_pk_add_f32 v[68:69], v[72:73], v[68:69] neg_lo:[0,1] neg_hi:[0,1]
	v_pk_add_f32 v[72:73], v[64:65], v[90:91] op_sel:[0,1] op_sel_hi:[1,0] neg_hi:[0,1]
	v_pk_add_f32 v[64:65], v[64:65], v[90:91] op_sel:[0,1] op_sel_hi:[1,0] neg_lo:[0,1]
	v_pk_mul_f32 v[90:91], v[88:89], v[30:31] op_sel:[0,0] op_sel_hi:[0,1]
	v_pk_fma_f32 v[90:91], v[88:89], v[30:31], v[90:91] op_sel:[1,1,0] op_sel_hi:[1,0,1] neg_lo:[0,1,0]
	v_pk_mul_f32 v[88:89], v[74:75], v[28:29] op_sel:[0,0] op_sel_hi:[0,1]
	v_pk_fma_f32 v[88:89], v[74:75], v[28:29], v[88:89] op_sel:[1,1,0] op_sel_hi:[1,0,1] neg_lo:[0,1,0]
	v_pk_mul_f32 v[74:75], v[92:93], v[26:27] op_sel:[0,0] op_sel_hi:[0,1]
	v_pk_fma_f32 v[74:75], v[92:93], v[26:27], v[74:75] op_sel:[1,1,0] op_sel_hi:[1,0,1] neg_lo:[0,1,0]
	s_barrier
	ds_write_b64 v1, v[74:75] offset:6552
	v_pk_mul_f32 v[74:75], v[84:85], v[24:25] op_sel:[0,0] op_sel_hi:[0,1]
	v_pk_fma_f32 v[74:75], v[84:85], v[24:25], v[74:75] op_sel:[1,1,0] op_sel_hi:[1,0,1] neg_lo:[0,1,0]
	ds_write_b64 v1, v[74:75] offset:8736
	v_pk_mul_f32 v[74:75], v[94:95], v[20:21] op_sel:[0,0] op_sel_hi:[0,1]
	v_pk_fma_f32 v[74:75], v[94:95], v[20:21], v[74:75] op_sel:[1,1,0] op_sel_hi:[1,0,1] neg_lo:[0,1,0]
	ds_write_b64 v1, v[74:75] offset:10920
	v_pk_mul_f32 v[74:75], v[86:87], v[16:17] op_sel:[0,0] op_sel_hi:[0,1]
	v_pk_fma_f32 v[74:75], v[86:87], v[16:17], v[74:75] op_sel:[1,1,0] op_sel_hi:[1,0,1] neg_lo:[0,1,0]
	ds_write_b64 v1, v[74:75] offset:13104
	v_pk_mul_f32 v[74:75], v[72:73], v[10:11] op_sel:[0,0] op_sel_hi:[0,1]
	v_pk_fma_f32 v[74:75], v[72:73], v[10:11], v[74:75] op_sel:[1,1,0] op_sel_hi:[1,0,1] neg_lo:[0,1,0]
	v_pk_mul_f32 v[72:73], v[82:83], v[22:23] op_sel:[0,0] op_sel_hi:[0,1]
	v_pk_fma_f32 v[72:73], v[82:83], v[22:23], v[72:73] op_sel:[1,1,0] op_sel_hi:[1,0,1] neg_lo:[0,1,0]
	ds_write_b64 v1, v[72:73] offset:17472
	v_pk_mul_f32 v[72:73], v[78:79], v[18:19] op_sel:[0,0] op_sel_hi:[0,1]
	v_pk_fma_f32 v[72:73], v[78:79], v[18:19], v[72:73] op_sel:[1,1,0] op_sel_hi:[1,0,1] neg_lo:[0,1,0]
	ds_write_b64 v1, v[72:73] offset:19656
	v_pk_mul_f32 v[72:73], v[76:77], v[12:13] op_sel:[0,0] op_sel_hi:[0,1]
	v_pk_fma_f32 v[72:73], v[76:77], v[12:13], v[72:73] op_sel:[1,1,0] op_sel_hi:[1,0,1] neg_lo:[0,1,0]
	ds_write_b64 v1, v[72:73] offset:21840
	v_pk_mul_f32 v[72:73], v[68:69], v[14:15] op_sel:[0,0] op_sel_hi:[0,1]
	v_pk_fma_f32 v[72:73], v[68:69], v[14:15], v[72:73] op_sel:[1,1,0] op_sel_hi:[1,0,1] neg_lo:[0,1,0]
	v_pk_mul_f32 v[68:69], v[80:81], v[6:7] op_sel:[0,0] op_sel_hi:[0,1]
	v_pk_fma_f32 v[68:69], v[80:81], v[6:7], v[68:69] op_sel:[1,1,0] op_sel_hi:[1,0,1] neg_lo:[0,1,0]
	ds_write_b64 v1, v[68:69] offset:26208
	v_pk_mul_f32 v[68:69], v[66:67], v[8:9] op_sel:[0,0] op_sel_hi:[0,1]
	v_pk_fma_f32 v[68:69], v[66:67], v[8:9], v[68:69] op_sel:[1,1,0] op_sel_hi:[1,0,1] neg_lo:[0,1,0]
	v_pk_mul_f32 v[66:67], v[70:71], v[4:5] op_sel:[0,0] op_sel_hi:[0,1]
	v_pk_fma_f32 v[66:67], v[70:71], v[4:5], v[66:67] op_sel:[1,1,0] op_sel_hi:[1,0,1] neg_lo:[0,1,0]
	ds_write_b64 v1, v[66:67] offset:30576
	v_pk_mul_f32 v[66:67], v[64:65], v[2:3] op_sel:[0,0] op_sel_hi:[0,1]
	v_pk_fma_f32 v[66:67], v[64:65], v[2:3], v[66:67] op_sel:[1,1,0] op_sel_hi:[1,0,1] neg_lo:[0,1,0]
	ds_write_b64 v1, v[98:99]
	ds_write_b64 v1, v[90:91] offset:2184
	ds_write_b64 v1, v[88:89] offset:4368
	ds_write_b64 v1, v[74:75] offset:15288
	ds_write_b64 v1, v[72:73] offset:24024
	ds_write_b64 v1, v[68:69] offset:28392
	ds_write_b64 v1, v[66:67] offset:32760
	s_waitcnt lgkmcnt(0)
	s_barrier
	ds_read2_b64 v[64:67], v96 offset1:16
	ds_read2_b64 v[68:71], v96 offset0:32 offset1:48
	ds_read2_b64 v[72:75], v96 offset0:64 offset1:80
	ds_read2_b64 v[76:79], v96 offset0:128 offset1:144
	ds_read2_b64 v[80:83], v96 offset0:96 offset1:112
	ds_read2_b64 v[84:87], v96 offset0:192 offset1:208
	ds_read2_b64 v[88:91], v96 offset0:160 offset1:176
	ds_read2_b64 v[92:95], v96 offset0:224 offset1:240
	s_waitcnt lgkmcnt(4)
	v_pk_add_f32 v[98:99], v[64:65], v[76:77]
	v_pk_add_f32 v[64:65], v[64:65], v[76:77] neg_lo:[0,1] neg_hi:[0,1]
	s_waitcnt lgkmcnt(2)
	v_pk_add_f32 v[76:77], v[72:73], v[84:85]
	v_pk_add_f32 v[72:73], v[72:73], v[84:85] neg_lo:[0,1] neg_hi:[0,1]
	v_pk_add_f32 v[84:85], v[98:99], v[76:77]
	v_pk_add_f32 v[76:77], v[98:99], v[76:77] neg_lo:[0,1] neg_hi:[0,1]
	v_pk_add_f32 v[98:99], v[64:65], v[72:73] op_sel:[0,1] op_sel_hi:[1,0] neg_hi:[0,1]
	v_pk_add_f32 v[64:65], v[64:65], v[72:73] op_sel:[0,1] op_sel_hi:[1,0] neg_lo:[0,1]
	v_pk_add_f32 v[72:73], v[66:67], v[78:79]
	v_pk_add_f32 v[66:67], v[66:67], v[78:79] neg_lo:[0,1] neg_hi:[0,1]
	v_pk_add_f32 v[78:79], v[74:75], v[86:87]
	v_pk_add_f32 v[74:75], v[74:75], v[86:87] neg_lo:[0,1] neg_hi:[0,1]
	v_pk_add_f32 v[86:87], v[72:73], v[78:79]
	v_pk_add_f32 v[72:73], v[72:73], v[78:79] neg_lo:[0,1] neg_hi:[0,1]
	v_pk_add_f32 v[78:79], v[66:67], v[74:75] op_sel:[0,1] op_sel_hi:[1,0] neg_hi:[0,1]
	v_pk_add_f32 v[66:67], v[66:67], v[74:75] op_sel:[0,1] op_sel_hi:[1,0] neg_lo:[0,1]
	s_waitcnt lgkmcnt(1)
	v_pk_add_f32 v[74:75], v[68:69], v[88:89]
	v_pk_add_f32 v[68:69], v[68:69], v[88:89] neg_lo:[0,1] neg_hi:[0,1]
	s_waitcnt lgkmcnt(0)
	v_pk_add_f32 v[88:89], v[80:81], v[92:93]
	v_pk_add_f32 v[80:81], v[80:81], v[92:93] neg_lo:[0,1] neg_hi:[0,1]
	v_pk_add_f32 v[92:93], v[74:75], v[88:89]
	v_pk_add_f32 v[74:75], v[74:75], v[88:89] neg_lo:[0,1] neg_hi:[0,1]
	v_pk_add_f32 v[88:89], v[68:69], v[80:81] op_sel:[0,1] op_sel_hi:[1,0] neg_hi:[0,1]
	v_pk_add_f32 v[68:69], v[68:69], v[80:81] op_sel:[0,1] op_sel_hi:[1,0] neg_lo:[0,1]
	v_pk_add_f32 v[80:81], v[70:71], v[90:91]
	v_pk_add_f32 v[70:71], v[70:71], v[90:91] neg_lo:[0,1] neg_hi:[0,1]
	v_pk_add_f32 v[90:91], v[82:83], v[94:95]
	v_pk_add_f32 v[82:83], v[82:83], v[94:95] neg_lo:[0,1] neg_hi:[0,1]
	v_pk_add_f32 v[94:95], v[80:81], v[90:91]
	v_pk_add_f32 v[80:81], v[80:81], v[90:91] neg_lo:[0,1] neg_hi:[0,1]
	v_pk_add_f32 v[90:91], v[70:71], v[82:83] op_sel:[0,1] op_sel_hi:[1,0] neg_hi:[0,1]
	v_pk_add_f32 v[70:71], v[70:71], v[82:83] op_sel:[0,1] op_sel_hi:[1,0] neg_lo:[0,1]
	v_pk_mul_f32 v[82:83], v[78:79], s[6:7] op_sel:[0,0] op_sel_hi:[0,1]
	v_pk_fma_f32 v[82:83], v[78:79], s[6:7], v[82:83] op_sel:[1,1,0] op_sel_hi:[1,0,1] neg_lo:[0,1,0]
	v_pk_mul_f32 v[78:79], v[66:67], s[10:11] op_sel:[0,0] op_sel_hi:[0,1]
	v_pk_fma_f32 v[78:79], v[66:67], s[10:11], v[78:79] op_sel:[1,1,0] op_sel_hi:[1,0,1] neg_lo:[0,1,0]
	v_pk_add_f32 v[66:67], v[88:89], v[88:89] op_sel:[0,1] op_sel_hi:[1,0] neg_hi:[0,1]
	v_pk_add_f32 v[72:73], v[72:73], v[72:73] op_sel:[0,1] op_sel_hi:[1,0] neg_hi:[0,1]
	s_nop 0
	v_pk_mul_f32 v[88:89], v[90:91], s[10:11] op_sel:[0,0] op_sel_hi:[0,1]
	v_pk_fma_f32 v[88:89], v[90:91], s[10:11], v[88:89] op_sel:[1,1,0] op_sel_hi:[1,0,1] neg_lo:[0,1,0]
	v_pk_mul_f32 v[90:91], v[70:71], s[14:15] op_sel:[0,0] op_sel_hi:[0,1]
	v_pk_fma_f32 v[90:91], v[70:71], s[14:15], v[90:91] op_sel:[1,1,0] op_sel_hi:[1,0,1] neg_lo:[0,1,0]
	v_pk_add_f32 v[70:71], v[84:85], v[92:93]
	v_pk_mul_f32 v[66:67], v[66:67], s[8:9]
	v_pk_add_f32 v[84:85], v[84:85], v[92:93] neg_lo:[0,1] neg_hi:[0,1]
	v_pk_add_f32 v[92:93], v[86:87], v[94:95]
	v_pk_add_f32 v[86:87], v[86:87], v[94:95] neg_lo:[0,1] neg_hi:[0,1]
	v_pk_add_f32 v[68:69], v[68:69], v[68:69] op_sel:[0,1] op_sel_hi:[1,0] neg_lo:[0,1]
	v_pk_add_f32 v[80:81], v[80:81], v[80:81] op_sel:[0,1] op_sel_hi:[1,0] neg_lo:[0,1]
	v_pk_add_f32 v[94:95], v[70:71], v[92:93]
	v_pk_add_f32 v[92:93], v[70:71], v[92:93] neg_lo:[0,1] neg_hi:[0,1]
	v_pk_add_f32 v[100:101], v[84:85], v[86:87] op_sel:[0,1] op_sel_hi:[1,0] neg_hi:[0,1]
	v_pk_add_f32 v[84:85], v[84:85], v[86:87] op_sel:[0,1] op_sel_hi:[1,0] neg_lo:[0,1]
	v_pk_add_f32 v[70:71], v[98:99], v[66:67]
	v_pk_add_f32 v[66:67], v[98:99], v[66:67] neg_lo:[0,1] neg_hi:[0,1]
	v_pk_add_f32 v[86:87], v[82:83], v[88:89]
	v_pk_add_f32 v[82:83], v[82:83], v[88:89] neg_lo:[0,1] neg_hi:[0,1]
	v_pk_mul_f32 v[72:73], v[72:73], s[8:9]
	v_pk_mul_f32 v[68:69], v[68:69], s[12:13]
	v_pk_mul_f32 v[80:81], v[80:81], s[12:13]
	v_pk_add_f32 v[88:89], v[70:71], v[86:87]
	v_pk_add_f32 v[86:87], v[70:71], v[86:87] neg_lo:[0,1] neg_hi:[0,1]
	v_pk_add_f32 v[98:99], v[66:67], v[82:83] op_sel:[0,1] op_sel_hi:[1,0] neg_hi:[0,1]
	v_pk_add_f32 v[82:83], v[66:67], v[82:83] op_sel:[0,1] op_sel_hi:[1,0] neg_lo:[0,1]
	v_pk_add_f32 v[66:67], v[76:77], v[74:75] op_sel:[0,1] op_sel_hi:[1,0] neg_hi:[0,1]
	v_pk_add_f32 v[70:71], v[76:77], v[74:75] op_sel:[0,1] op_sel_hi:[1,0] neg_lo:[0,1]
	v_pk_add_f32 v[74:75], v[72:73], v[80:81]
	v_pk_add_f32 v[72:73], v[72:73], v[80:81] neg_lo:[0,1] neg_hi:[0,1]
	v_pk_add_f32 v[76:77], v[74:75], v[66:67]
	v_pk_add_f32 v[74:75], v[66:67], v[74:75] neg_lo:[0,1] neg_hi:[0,1]
	v_pk_add_f32 v[66:67], v[64:65], v[68:69]
	v_pk_add_f32 v[64:65], v[64:65], v[68:69] neg_lo:[0,1] neg_hi:[0,1]
	v_pk_add_f32 v[68:69], v[78:79], v[90:91]
	v_pk_add_f32 v[80:81], v[70:71], v[72:73] op_sel:[0,1] op_sel_hi:[1,0] neg_hi:[0,1]
	v_pk_add_f32 v[72:73], v[70:71], v[72:73] op_sel:[0,1] op_sel_hi:[1,0] neg_lo:[0,1]
	v_pk_add_f32 v[70:71], v[78:79], v[90:91] neg_lo:[0,1] neg_hi:[0,1]
	v_pk_add_f32 v[78:79], v[66:67], v[68:69]
	v_pk_add_f32 v[90:91], v[66:67], v[68:69] neg_lo:[0,1] neg_hi:[0,1]
	v_mov_b32_e32 v68, v0
	v_pk_add_f32 v[102:103], v[64:65], v[70:71] op_sel:[0,1] op_sel_hi:[1,0] neg_hi:[0,1]
	v_pk_add_f32 v[104:105], v[64:65], v[70:71] op_sel:[0,1] op_sel_hi:[1,0] neg_lo:[0,1]
	s_nop 0
	v_ashrrev_i32_e32 v64, 4, v68
	v_lshlrev_b32_e32 v97, 3, v64
	v_add_u32_e32 v108, 0x8800, v97
	v_and_b32_e32 v68, 15, v68
	ds_read2_b64 v[64:67], v108 offset0:16 offset1:32
	v_mad_u32_u24 v109, v68, s5, v97
	ds_read2_b64 v[68:71], v108 offset0:48 offset1:64
	s_waitcnt lgkmcnt(1)
	v_pk_mul_f32 v[106:107], v[88:89], v[64:65] op_sel:[0,0] op_sel_hi:[0,1]
	v_pk_fma_f32 v[106:107], v[88:89], v[64:65], v[106:107] op_sel:[1,1,0] op_sel_hi:[1,0,1] neg_lo:[0,1,0]
	v_pk_mul_f32 v[88:89], v[76:77], v[66:67] op_sel:[0,0] op_sel_hi:[0,1]
	v_pk_fma_f32 v[88:89], v[76:77], v[66:67], v[88:89] op_sel:[1,1,0] op_sel_hi:[1,0,1] neg_lo:[0,1,0]
	s_waitcnt lgkmcnt(0)
	v_pk_mul_f32 v[76:77], v[78:79], v[68:69] op_sel:[0,0] op_sel_hi:[0,1]
	v_pk_fma_f32 v[76:77], v[78:79], v[68:69], v[76:77] op_sel:[1,1,0] op_sel_hi:[1,0,1] neg_lo:[0,1,0]
	ds_write2_b64 v109, v[88:89], v[76:77] offset0:32 offset1:48
	v_pk_mul_f32 v[76:77], v[100:101], v[70:71] op_sel:[0,0] op_sel_hi:[0,1]
	v_pk_fma_f32 v[76:77], v[100:101], v[70:71], v[76:77] op_sel:[1,1,0] op_sel_hi:[1,0,1] neg_lo:[0,1,0]
	ds_read2_b64 v[64:67], v108 offset0:80 offset1:96
	s_waitcnt lgkmcnt(0)
	v_pk_mul_f32 v[78:79], v[98:99], v[64:65] op_sel:[0,0] op_sel_hi:[0,1]
	v_pk_fma_f32 v[78:79], v[98:99], v[64:65], v[78:79] op_sel:[1,1,0] op_sel_hi:[1,0,1] neg_lo:[0,1,0]
	ds_write2_b64 v109, v[76:77], v[78:79] offset0:64 offset1:80
	v_pk_mul_f32 v[76:77], v[80:81], v[66:67] op_sel:[0,0] op_sel_hi:[0,1]
	v_pk_fma_f32 v[76:77], v[80:81], v[66:67], v[76:77] op_sel:[1,1,0] op_sel_hi:[1,0,1] neg_lo:[0,1,0]
	ds_read2_b64 v[68:71], v108 offset0:112 offset1:128
	ds_read2_b64 v[64:67], v108 offset0:144 offset1:160
	s_waitcnt lgkmcnt(1)
	v_pk_mul_f32 v[78:79], v[102:103], v[68:69] op_sel:[0,0] op_sel_hi:[0,1]
	v_pk_fma_f32 v[78:79], v[102:103], v[68:69], v[78:79] op_sel:[1,1,0] op_sel_hi:[1,0,1] neg_lo:[0,1,0]
	ds_write2_b64 v109, v[76:77], v[78:79] offset0:96 offset1:112
	v_pk_mul_f32 v[76:77], v[92:93], v[70:71] op_sel:[0,0] op_sel_hi:[0,1]
	v_pk_fma_f32 v[76:77], v[92:93], v[70:71], v[76:77] op_sel:[1,1,0] op_sel_hi:[1,0,1] neg_lo:[0,1,0]
	ds_read2_b64 v[68:71], v108 offset0:176 offset1:192
	s_waitcnt lgkmcnt(2)
	v_pk_mul_f32 v[78:79], v[86:87], v[64:65] op_sel:[0,0] op_sel_hi:[0,1]
	v_pk_fma_f32 v[78:79], v[86:87], v[64:65], v[78:79] op_sel:[1,1,0] op_sel_hi:[1,0,1] neg_lo:[0,1,0]
	ds_write2_b64 v109, v[76:77], v[78:79] offset0:128 offset1:144
	v_pk_mul_f32 v[76:77], v[74:75], v[66:67] op_sel:[0,0] op_sel_hi:[0,1]
	v_pk_fma_f32 v[76:77], v[74:75], v[66:67], v[76:77] op_sel:[1,1,0] op_sel_hi:[1,0,1] neg_lo:[0,1,0]
	ds_read2_b64 v[64:67], v108 offset0:208 offset1:224
	s_waitcnt lgkmcnt(2)
	v_pk_mul_f32 v[74:75], v[90:91], v[68:69] op_sel:[0,0] op_sel_hi:[0,1]
	v_pk_fma_f32 v[74:75], v[90:91], v[68:69], v[74:75] op_sel:[1,1,0] op_sel_hi:[1,0,1] neg_lo:[0,1,0]
	ds_write2_b64 v109, v[76:77], v[74:75] offset0:160 offset1:176
	v_pk_mul_f32 v[74:75], v[84:85], v[70:71] op_sel:[0,0] op_sel_hi:[0,1]
	v_pk_fma_f32 v[74:75], v[84:85], v[70:71], v[74:75] op_sel:[1,1,0] op_sel_hi:[1,0,1] neg_lo:[0,1,0]
	s_waitcnt lgkmcnt(1)
	v_pk_mul_f32 v[70:71], v[82:83], v[64:65] op_sel:[0,0] op_sel_hi:[0,1]
	v_pk_fma_f32 v[70:71], v[82:83], v[64:65], v[70:71] op_sel:[1,1,0] op_sel_hi:[1,0,1] neg_lo:[0,1,0]
	v_pk_mul_f32 v[64:65], v[72:73], v[66:67] op_sel:[0,0] op_sel_hi:[0,1]
	v_pk_fma_f32 v[64:65], v[72:73], v[66:67], v[64:65] op_sel:[1,1,0] op_sel_hi:[1,0,1] neg_lo:[0,1,0]
	ds_read_b64 v[68:69], v97 offset:36736
	s_waitcnt lgkmcnt(0)
	v_pk_mul_f32 v[66:67], v[104:105], v[68:69] op_sel:[0,0] op_sel_hi:[0,1]
	v_pk_fma_f32 v[66:67], v[104:105], v[68:69], v[66:67] op_sel:[1,1,0] op_sel_hi:[1,0,1] neg_lo:[0,1,0]
	ds_write2_b64 v109, v[64:65], v[66:67] offset0:224 offset1:240
	v_mov_b32_e32 v64, v0
	ds_write2_b64 v109, v[94:95], v[106:107] offset1:16
	ds_write2_b64 v109, v[74:75], v[70:71] offset0:192 offset1:208
	s_waitcnt lgkmcnt(0)
	s_barrier
	s_nop 0
	v_and_b32_e32 v65, 15, v64
	v_and_b32_e32 v64, 0x1ffffff0, v64
	v_lshlrev_b32_e32 v64, 3, v64
	v_mad_u32_u24 v92, v65, s5, v64
	ds_read2_b64 v[64:67], v92 offset1:1
	ds_read2_b64 v[68:71], v92 offset0:2 offset1:3
	ds_read2_b64 v[72:75], v92 offset0:8 offset1:9
	ds_read2_b64 v[76:79], v92 offset0:4 offset1:5
	ds_read2_b64 v[80:83], v92 offset0:6 offset1:7
	ds_read2_b64 v[84:87], v92 offset0:12 offset1:13
	ds_read2_b64 v[88:91], v92 offset0:10 offset1:11
	ds_read2_b64 v[92:95], v92 offset0:14 offset1:15
	s_waitcnt lgkmcnt(5)
	v_pk_add_f32 v[98:99], v[64:65], v[72:73]
	v_pk_add_f32 v[64:65], v[64:65], v[72:73] neg_lo:[0,1] neg_hi:[0,1]
	s_waitcnt lgkmcnt(2)
	v_pk_add_f32 v[72:73], v[76:77], v[84:85]
	v_pk_add_f32 v[76:77], v[76:77], v[84:85] neg_lo:[0,1] neg_hi:[0,1]
	v_pk_add_f32 v[84:85], v[98:99], v[72:73]
	v_pk_add_f32 v[98:99], v[98:99], v[72:73] neg_lo:[0,1] neg_hi:[0,1]
	v_pk_add_f32 v[100:101], v[64:65], v[76:77] op_sel:[0,1] op_sel_hi:[1,0] neg_hi:[0,1]
	v_pk_add_f32 v[102:103], v[64:65], v[76:77] op_sel:[0,1] op_sel_hi:[1,0] neg_lo:[0,1]
	v_pk_add_f32 v[64:65], v[66:67], v[74:75]
	v_pk_add_f32 v[72:73], v[78:79], v[86:87]
	v_pk_add_f32 v[66:67], v[66:67], v[74:75] neg_lo:[0,1] neg_hi:[0,1]
	v_pk_add_f32 v[74:75], v[78:79], v[86:87] neg_lo:[0,1] neg_hi:[0,1]
	v_pk_add_f32 v[76:77], v[64:65], v[72:73]
	v_pk_add_f32 v[64:65], v[64:65], v[72:73] neg_lo:[0,1] neg_hi:[0,1]
	v_pk_add_f32 v[72:73], v[66:67], v[74:75] op_sel:[0,1] op_sel_hi:[1,0] neg_hi:[0,1]
	v_pk_add_f32 v[66:67], v[66:67], v[74:75] op_sel:[0,1] op_sel_hi:[1,0] neg_lo:[0,1]
	s_waitcnt lgkmcnt(1)
	v_pk_add_f32 v[74:75], v[68:69], v[88:89]
	s_waitcnt lgkmcnt(0)
	v_pk_add_f32 v[78:79], v[80:81], v[92:93]
	v_pk_add_f32 v[64:65], v[64:65], v[64:65] op_sel:[0,1] op_sel_hi:[1,0] neg_hi:[0,1]
	v_pk_add_f32 v[68:69], v[68:69], v[88:89] neg_lo:[0,1] neg_hi:[0,1]
	v_pk_add_f32 v[80:81], v[80:81], v[92:93] neg_lo:[0,1] neg_hi:[0,1]
	v_pk_add_f32 v[86:87], v[74:75], v[78:79]
	v_pk_add_f32 v[78:79], v[74:75], v[78:79] neg_lo:[0,1] neg_hi:[0,1]
	v_pk_add_f32 v[74:75], v[68:69], v[80:81] op_sel:[0,1] op_sel_hi:[1,0] neg_hi:[0,1]
	v_pk_mul_f32 v[92:93], v[64:65], s[8:9]
	v_pk_add_f32 v[68:69], v[68:69], v[80:81] op_sel:[0,1] op_sel_hi:[1,0] neg_lo:[0,1]
	v_pk_add_f32 v[80:81], v[70:71], v[90:91]
	v_pk_add_f32 v[64:65], v[74:75], v[74:75] op_sel:[0,1] op_sel_hi:[1,0] neg_hi:[0,1]
	v_pk_add_f32 v[70:71], v[70:71], v[90:91] neg_lo:[0,1] neg_hi:[0,1]
	v_pk_add_f32 v[88:89], v[82:83], v[94:95]
	v_pk_add_f32 v[82:83], v[82:83], v[94:95] neg_lo:[0,1] neg_hi:[0,1]
	v_pk_mul_f32 v[94:95], v[66:67], s[10:11] op_sel:[0,0] op_sel_hi:[0,1]
	v_pk_fma_f32 v[94:95], v[66:67], s[10:11], v[94:95] op_sel:[1,1,0] op_sel_hi:[1,0,1] neg_lo:[0,1,0]
	v_pk_mul_f32 v[66:67], v[64:65], s[8:9]
	v_pk_add_f32 v[64:65], v[68:69], v[68:69] op_sel:[0,1] op_sel_hi:[1,0] neg_lo:[0,1]
	v_pk_add_f32 v[90:91], v[80:81], v[88:89]
	v_pk_add_f32 v[80:81], v[80:81], v[88:89] neg_lo:[0,1] neg_hi:[0,1]
	v_pk_add_f32 v[88:89], v[70:71], v[82:83] op_sel:[0,1] op_sel_hi:[1,0] neg_hi:[0,1]
	v_pk_add_f32 v[70:71], v[70:71], v[82:83] op_sel:[0,1] op_sel_hi:[1,0] neg_lo:[0,1]
	v_pk_mul_f32 v[104:105], v[64:65], s[12:13]
	v_pk_mul_f32 v[82:83], v[72:73], s[6:7] op_sel:[0,0] op_sel_hi:[0,1]
	v_pk_fma_f32 v[82:83], v[72:73], s[6:7], v[82:83] op_sel:[1,1,0] op_sel_hi:[1,0,1] neg_lo:[0,1,0]
	v_pk_add_f32 v[72:73], v[76:77], v[90:91]
	v_pk_add_f32 v[64:65], v[80:81], v[80:81] op_sel:[0,1] op_sel_hi:[1,0] neg_lo:[0,1]
	v_pk_mul_f32 v[68:69], v[88:89], s[10:11] op_sel:[0,0] op_sel_hi:[0,1]
	v_pk_fma_f32 v[68:69], v[88:89], s[10:11], v[68:69] op_sel:[1,1,0] op_sel_hi:[1,0,1] neg_lo:[0,1,0]
	v_pk_mul_f32 v[108:109], v[70:71], s[14:15] op_sel:[0,0] op_sel_hi:[0,1]
	v_pk_fma_f32 v[108:109], v[70:71], s[14:15], v[108:109] op_sel:[1,1,0] op_sel_hi:[1,0,1] neg_lo:[0,1,0]
	v_pk_add_f32 v[70:71], v[84:85], v[86:87] neg_lo:[0,1] neg_hi:[0,1]
	v_pk_mul_f32 v[106:107], v[64:65], s[12:13]
	v_pk_add_f32 v[64:65], v[84:85], v[86:87]
	v_pk_add_f32 v[74:75], v[76:77], v[90:91] neg_lo:[0,1] neg_hi:[0,1]
	v_pk_add_f32 v[88:89], v[64:65], v[72:73]
	v_pk_add_f32 v[72:73], v[64:65], v[72:73] neg_lo:[0,1] neg_hi:[0,1]
	v_pk_add_f32 v[80:81], v[70:71], v[74:75] op_sel:[0,1] op_sel_hi:[1,0] neg_hi:[0,1]
	v_pk_add_f32 v[64:65], v[70:71], v[74:75] op_sel:[0,1] op_sel_hi:[1,0] neg_lo:[0,1]
	v_pk_add_f32 v[70:71], v[100:101], v[66:67]
	v_pk_add_f32 v[66:67], v[100:101], v[66:67] neg_lo:[0,1] neg_hi:[0,1]
	v_pk_add_f32 v[74:75], v[82:83], v[68:69]
	v_pk_add_f32 v[68:69], v[82:83], v[68:69] neg_lo:[0,1] neg_hi:[0,1]
	v_pk_add_f32 v[90:91], v[70:71], v[74:75]
	v_pk_add_f32 v[74:75], v[70:71], v[74:75] neg_lo:[0,1] neg_hi:[0,1]
	v_pk_add_f32 v[82:83], v[66:67], v[68:69] op_sel:[0,1] op_sel_hi:[1,0] neg_hi:[0,1]
	v_pk_add_f32 v[66:67], v[66:67], v[68:69] op_sel:[0,1] op_sel_hi:[1,0] neg_lo:[0,1]
	v_pk_add_f32 v[68:69], v[98:99], v[78:79] op_sel:[0,1] op_sel_hi:[1,0] neg_hi:[0,1]
	v_pk_add_f32 v[70:71], v[98:99], v[78:79] op_sel:[0,1] op_sel_hi:[1,0] neg_lo:[0,1]
	v_pk_add_f32 v[76:77], v[92:93], v[106:107]
	v_pk_add_f32 v[78:79], v[92:93], v[106:107] neg_lo:[0,1] neg_hi:[0,1]
	v_pk_add_f32 v[92:93], v[76:77], v[68:69]
	v_pk_add_f32 v[76:77], v[68:69], v[76:77] neg_lo:[0,1] neg_hi:[0,1]
	v_pk_add_f32 v[86:87], v[70:71], v[78:79] op_sel:[0,1] op_sel_hi:[1,0] neg_hi:[0,1]
	v_pk_add_f32 v[68:69], v[70:71], v[78:79] op_sel:[0,1] op_sel_hi:[1,0] neg_lo:[0,1]
	v_pk_add_f32 v[70:71], v[102:103], v[104:105]
	v_pk_add_f32 v[98:99], v[102:103], v[104:105] neg_lo:[0,1] neg_hi:[0,1]
	v_pk_add_f32 v[78:79], v[94:95], v[108:109]
	v_pk_add_f32 v[100:101], v[94:95], v[108:109] neg_lo:[0,1] neg_hi:[0,1]
	v_pk_add_f32 v[94:95], v[70:71], v[78:79]
	v_pk_add_f32 v[78:79], v[70:71], v[78:79] neg_lo:[0,1] neg_hi:[0,1]
	v_pk_add_f32 v[84:85], v[98:99], v[100:101] op_sel:[0,1] op_sel_hi:[1,0] neg_hi:[0,1]
	v_pk_add_f32 v[70:71], v[98:99], v[100:101] op_sel:[0,1] op_sel_hi:[1,0] neg_lo:[0,1]
	v_mov_b32_e32 v98, v0
	s_nop 0
	v_and_b32_e32 v97, -16, v98
	v_and_b32_e32 v99, 15, v98
	v_lshlrev_b32_e32 v100, 3, v97
	v_mad_u32_u24 v100, v99, s5, v100
	v_cmp_ne_u32_e32 vcc, 0, v99
	ds_write2_b64 v100, v[88:89], v[90:91] offset1:1
	ds_write2_b64 v100, v[92:93], v[94:95] offset0:2 offset1:3
	ds_write2_b64 v100, v[80:81], v[82:83] offset0:4 offset1:5
	ds_write2_b64 v100, v[86:87], v[84:85] offset0:6 offset1:7
	ds_write2_b64 v100, v[72:73], v[74:75] offset0:8 offset1:9
	ds_write2_b64 v100, v[76:77], v[78:79] offset0:10 offset1:11
	ds_write2_b64 v100, v[64:65], v[66:67] offset0:12 offset1:13
	ds_write2_b64 v100, v[68:69], v[70:71] offset0:14 offset1:15
	s_waitcnt lgkmcnt(0)
	s_barrier
	s_and_saveexec_b64 s[6:7], vcc
	s_xor_b64 s[6:7], exec, s[6:7]
	v_sub_u32_e32 v99, 16, v99
	v_mul_u32_u24_e32 v99, 0x111, v99
	v_sub_u32_e32 v97, v99, v97
	v_add_u32_e32 v100, 0xf0, v97
	s_andn2_saveexec_b64 s[6:7], s[6:7]
	v_sub_u32_e32 v97, 0x100, v98
	v_cmp_lt_u32_e32 vcc, 15, v98
	s_nop 1
	v_cndmask_b32_e32 v100, 1, v97, vcc
	s_or_b64 exec, exec, s[6:7]
	v_mov_b32_e32 v97, 0
	v_lshlrev_b32_e32 v110, 3, v100
	ds_read_b64 v[108:109], v97
	ds_read2_b64 v[100:103], v110 offset0:14 offset1:15
	v_cmp_eq_u32_e32 vcc, 0, v98
	ds_read2_b64 v[104:107], v110 offset0:12 offset1:13
	s_mov_b32 s6, 0x3f6c835e
	s_mov_b32 s7, 0xbec3ef15
	s_waitcnt lgkmcnt(1)
	v_cndmask_b32_e32 v99, v103, v109, vcc
	v_cndmask_b32_e32 v98, v102, v108, vcc
	v_pk_add_f32 v[102:103], v[88:89], v[98:99] neg_hi:[0,1]
	v_pk_add_f32 v[88:89], v[88:89], v[98:99] neg_lo:[0,1]
	s_mov_b32 s9, s8
	v_pk_mul_f32 v[98:99], v[102:103], v[88:89] op_sel:[0,0] op_sel_hi:[0,1]
	v_pk_fma_f32 v[98:99], v[102:103], v[88:89], v[98:99] op_sel:[1,1,0] op_sel_hi:[1,0,1] neg_hi:[0,1,0]
	v_pk_add_f32 v[88:89], v[90:91], v[100:101] neg_hi:[0,1]
	v_pk_add_f32 v[90:91], v[90:91], v[100:101] neg_lo:[0,1]
	s_mov_b32 s14, s11
	v_pk_add_f32 v[62:63], v[62:63], v[98:99] op_sel:[1,0] op_sel_hi:[0,1] neg_lo:[0,1] neg_hi:[1,1]
	v_pk_mul_f32 v[98:99], v[88:89], v[90:91] op_sel:[0,0] op_sel_hi:[0,1]
	v_pk_fma_f32 v[98:99], v[88:89], v[90:91], v[98:99] op_sel:[1,1,0] op_sel_hi:[1,0,1] neg_hi:[0,1,0]
	s_waitcnt lgkmcnt(0)
	v_pk_add_f32 v[88:89], v[92:93], v[106:107] neg_hi:[0,1]
	v_pk_add_f32 v[90:91], v[92:93], v[106:107] neg_lo:[0,1]
	s_mov_b32 s15, s10
	v_pk_mul_f32 v[92:93], v[88:89], v[90:91] op_sel:[0,0] op_sel_hi:[0,1]
	v_pk_fma_f32 v[92:93], v[88:89], v[90:91], v[92:93] op_sel:[1,1,0] op_sel_hi:[1,0,1] neg_hi:[0,1,0]
	v_pk_add_f32 v[60:61], v[60:61], v[98:99] op_sel:[1,0] op_sel_hi:[0,1] neg_lo:[0,1] neg_hi:[1,1]
	ds_read2_b64 v[88:91], v110 offset0:10 offset1:11
	v_pk_add_f32 v[58:59], v[58:59], v[92:93] op_sel:[1,0] op_sel_hi:[0,1] neg_lo:[0,1] neg_hi:[1,1]
	v_pk_add_f32 v[92:93], v[94:95], v[104:105] neg_hi:[0,1]
	v_pk_add_f32 v[94:95], v[94:95], v[104:105] neg_lo:[0,1]
	s_mov_b32 s13, s12
	v_pk_mul_f32 v[98:99], v[92:93], v[94:95] op_sel:[0,0] op_sel_hi:[0,1]
	v_pk_fma_f32 v[98:99], v[92:93], v[94:95], v[98:99] op_sel:[1,1,0] op_sel_hi:[1,0,1] neg_hi:[0,1,0]
	ds_read2_b64 v[92:95], v110 offset0:8 offset1:9
	v_pk_add_f32 v[56:57], v[56:57], v[98:99] op_sel:[1,0] op_sel_hi:[0,1] neg_lo:[0,1] neg_hi:[1,1]
	s_waitcnt lgkmcnt(1)
	v_pk_add_f32 v[98:99], v[80:81], v[90:91] neg_hi:[0,1]
	v_pk_add_f32 v[80:81], v[80:81], v[90:91] neg_lo:[0,1]
	s_add_u32 s2, s2, 0x2000000
	v_pk_mul_f32 v[90:91], v[98:99], v[80:81] op_sel:[0,0] op_sel_hi:[0,1]
	v_pk_fma_f32 v[90:91], v[98:99], v[80:81], v[90:91] op_sel:[1,1,0] op_sel_hi:[1,0,1] neg_hi:[0,1,0]
	v_pk_add_f32 v[80:81], v[82:83], v[88:89] neg_hi:[0,1]
	v_pk_add_f32 v[82:83], v[82:83], v[88:89] neg_lo:[0,1]
	s_addc_u32 s3, s3, 0
	v_pk_mul_f32 v[88:89], v[80:81], v[82:83] op_sel:[0,0] op_sel_hi:[0,1]
	v_pk_fma_f32 v[88:89], v[80:81], v[82:83], v[88:89] op_sel:[1,1,0] op_sel_hi:[1,0,1] neg_hi:[0,1,0]
	s_waitcnt lgkmcnt(0)
	v_pk_add_f32 v[80:81], v[86:87], v[94:95] neg_lo:[0,1]
	v_pk_add_f32 v[54:55], v[54:55], v[90:91] op_sel:[1,0] op_sel_hi:[0,1] neg_lo:[0,1] neg_hi:[1,1]
	s_load_dwordx2 s[0:1], s[0:1], 0x8
	v_pk_add_f32 v[88:89], v[52:53], v[88:89] op_sel:[1,0] op_sel_hi:[0,1] neg_lo:[0,1] neg_hi:[1,1]
	v_pk_add_f32 v[52:53], v[86:87], v[94:95] neg_hi:[0,1]
	s_nop 0
	v_pk_mul_f32 v[82:83], v[52:53], v[80:81] op_sel:[0,0] op_sel_hi:[0,1]
	v_pk_fma_f32 v[82:83], v[52:53], v[80:81], v[82:83] op_sel:[1,1,0] op_sel_hi:[1,0,1] neg_hi:[0,1,0]
	v_pk_add_f32 v[80:81], v[84:85], v[92:93] neg_hi:[0,1]
	s_nop 0
	v_pk_add_f32 v[86:87], v[50:51], v[82:83] op_sel:[1,0] op_sel_hi:[0,1] neg_lo:[0,1] neg_hi:[1,1]
	ds_read2_b64 v[50:53], v110 offset0:6 offset1:7
	v_pk_add_f32 v[82:83], v[84:85], v[92:93] neg_lo:[0,1]
	s_nop 0
	v_pk_mul_f32 v[84:85], v[80:81], v[82:83] op_sel:[0,0] op_sel_hi:[0,1]
	v_pk_fma_f32 v[84:85], v[80:81], v[82:83], v[84:85] op_sel:[1,1,0] op_sel_hi:[1,0,1] neg_hi:[0,1,0]
	ds_read2_b64 v[80:83], v110 offset0:4 offset1:5
	v_pk_add_f32 v[84:85], v[48:49], v[84:85] op_sel:[1,0] op_sel_hi:[0,1] neg_lo:[0,1] neg_hi:[1,1]
	s_waitcnt lgkmcnt(0)
	v_pk_add_f32 v[48:49], v[72:73], v[52:53] neg_hi:[0,1]
	v_pk_add_f32 v[52:53], v[72:73], v[52:53] neg_lo:[0,1]
	s_nop 0
	v_pk_mul_f32 v[72:73], v[48:49], v[52:53] op_sel:[0,0] op_sel_hi:[0,1]
	v_pk_fma_f32 v[72:73], v[48:49], v[52:53], v[72:73] op_sel:[1,1,0] op_sel_hi:[1,0,1] neg_hi:[0,1,0]
	v_pk_add_f32 v[48:49], v[74:75], v[50:51] neg_lo:[0,1]
	s_nop 0
	v_pk_add_f32 v[52:53], v[46:47], v[72:73] op_sel:[1,0] op_sel_hi:[0,1] neg_lo:[0,1] neg_hi:[1,1]
	v_pk_add_f32 v[46:47], v[74:75], v[50:51] neg_hi:[0,1]
	s_nop 0
	v_pk_mul_f32 v[50:51], v[46:47], v[48:49] op_sel:[0,0] op_sel_hi:[0,1]
	v_pk_fma_f32 v[50:51], v[46:47], v[48:49], v[50:51] op_sel:[1,1,0] op_sel_hi:[1,0,1] neg_hi:[0,1,0]
	v_pk_add_f32 v[46:47], v[76:77], v[82:83] neg_lo:[0,1]
	s_nop 0
	v_pk_add_f32 v[50:51], v[44:45], v[50:51] op_sel:[1,0] op_sel_hi:[0,1] neg_lo:[0,1] neg_hi:[1,1]
	v_pk_add_f32 v[44:45], v[76:77], v[82:83] neg_hi:[0,1]
	s_nop 0
	v_pk_mul_f32 v[48:49], v[44:45], v[46:47] op_sel:[0,0] op_sel_hi:[0,1]
	v_pk_fma_f32 v[48:49], v[44:45], v[46:47], v[48:49] op_sel:[1,1,0] op_sel_hi:[1,0,1] neg_hi:[0,1,0]
	v_pk_add_f32 v[46:47], v[78:79], v[80:81] neg_hi:[0,1]
	s_nop 0
	v_pk_add_f32 v[72:73], v[42:43], v[48:49] op_sel:[1,0] op_sel_hi:[0,1] neg_lo:[0,1] neg_hi:[1,1]
	ds_read2_b64 v[42:45], v110 offset0:2 offset1:3
	v_pk_add_f32 v[48:49], v[78:79], v[80:81] neg_lo:[0,1]
	s_nop 0
	v_pk_mul_f32 v[74:75], v[46:47], v[48:49] op_sel:[0,0] op_sel_hi:[0,1]
	v_pk_fma_f32 v[74:75], v[46:47], v[48:49], v[74:75] op_sel:[1,1,0] op_sel_hi:[1,0,1] neg_hi:[0,1,0]
	ds_read2_b64 v[46:49], v110 offset1:1
	v_pk_add_f32 v[40:41], v[40:41], v[74:75] op_sel:[1,0] op_sel_hi:[0,1] neg_lo:[0,1] neg_hi:[1,1]
	s_waitcnt lgkmcnt(1)
	v_pk_add_f32 v[74:75], v[64:65], v[44:45] neg_hi:[0,1]
	v_pk_add_f32 v[44:45], v[64:65], v[44:45] neg_lo:[0,1]
	s_waitcnt lgkmcnt(0)
	v_pk_mul_f32 v[64:65], v[74:75], v[44:45] op_sel:[0,0] op_sel_hi:[0,1]
	v_pk_fma_f32 v[64:65], v[74:75], v[44:45], v[64:65] op_sel:[1,1,0] op_sel_hi:[1,0,1] neg_hi:[0,1,0]
	v_pk_add_f32 v[44:45], v[66:67], v[42:43] neg_hi:[0,1]
	v_pk_add_f32 v[42:43], v[66:67], v[42:43] neg_lo:[0,1]
	s_barrier
	v_pk_add_f32 v[38:39], v[38:39], v[64:65] op_sel:[1,0] op_sel_hi:[0,1] neg_lo:[0,1] neg_hi:[1,1]
	v_pk_mul_f32 v[64:65], v[44:45], v[42:43] op_sel:[0,0] op_sel_hi:[0,1]
	v_pk_fma_f32 v[64:65], v[44:45], v[42:43], v[64:65] op_sel:[1,1,0] op_sel_hi:[1,0,1] neg_hi:[0,1,0]
	v_pk_add_f32 v[42:43], v[68:69], v[48:49] neg_hi:[0,1]
	v_pk_add_f32 v[44:45], v[68:69], v[48:49] neg_lo:[0,1]
	s_nop 0
	v_pk_mul_f32 v[48:49], v[42:43], v[44:45] op_sel:[0,0] op_sel_hi:[0,1]
	v_pk_fma_f32 v[48:49], v[42:43], v[44:45], v[48:49] op_sel:[1,1,0] op_sel_hi:[1,0,1] neg_hi:[0,1,0]
	v_pk_add_f32 v[42:43], v[70:71], v[46:47] neg_hi:[0,1]
	v_pk_add_f32 v[44:45], v[70:71], v[46:47] neg_lo:[0,1]
	v_pk_add_f32 v[36:37], v[36:37], v[64:65] op_sel:[1,0] op_sel_hi:[0,1] neg_lo:[0,1] neg_hi:[1,1]
	s_nop 0
	v_pk_mul_f32 v[46:47], v[42:43], v[44:45] op_sel:[0,0] op_sel_hi:[0,1]
	v_pk_fma_f32 v[46:47], v[42:43], v[44:45], v[46:47] op_sel:[1,1,0] op_sel_hi:[1,0,1] neg_hi:[0,1,0]
	v_pk_add_f32 v[42:43], v[62:63], v[52:53]
	v_pk_add_f32 v[32:33], v[32:33], v[46:47] op_sel:[1,0] op_sel_hi:[0,1] neg_lo:[0,1] neg_hi:[1,1]
	v_pk_add_f32 v[44:45], v[62:63], v[52:53] neg_lo:[0,1] neg_hi:[0,1]
	v_pk_add_f32 v[46:47], v[54:55], v[38:39]
	v_pk_add_f32 v[38:39], v[54:55], v[38:39] neg_lo:[0,1] neg_hi:[0,1]
	v_pk_add_f32 v[34:35], v[34:35], v[48:49] op_sel:[1,0] op_sel_hi:[0,1] neg_lo:[0,1] neg_hi:[1,1]
	v_pk_add_f32 v[48:49], v[42:43], v[46:47]
	v_pk_add_f32 v[42:43], v[42:43], v[46:47] neg_lo:[0,1] neg_hi:[0,1]
	v_pk_add_f32 v[46:47], v[44:45], v[38:39] op_sel:[0,1] op_sel_hi:[1,0] neg_hi:[0,1]
	v_pk_add_f32 v[38:39], v[44:45], v[38:39] op_sel:[0,1] op_sel_hi:[1,0] neg_lo:[0,1]
	v_pk_add_f32 v[44:45], v[60:61], v[50:51]
	v_pk_add_f32 v[50:51], v[60:61], v[50:51] neg_lo:[0,1] neg_hi:[0,1]
	v_pk_add_f32 v[52:53], v[88:89], v[36:37]
	v_pk_add_f32 v[36:37], v[88:89], v[36:37] neg_lo:[0,1] neg_hi:[0,1]
	v_pk_add_f32 v[54:55], v[44:45], v[52:53]
	v_pk_add_f32 v[44:45], v[44:45], v[52:53] neg_lo:[0,1] neg_hi:[0,1]
	v_pk_add_f32 v[52:53], v[50:51], v[36:37] op_sel:[0,1] op_sel_hi:[1,0] neg_hi:[0,1]
	v_pk_add_f32 v[36:37], v[50:51], v[36:37] op_sel:[0,1] op_sel_hi:[1,0] neg_lo:[0,1]
	v_pk_add_f32 v[50:51], v[58:59], v[72:73]
	v_pk_add_f32 v[58:59], v[58:59], v[72:73] neg_lo:[0,1] neg_hi:[0,1]
	v_pk_add_f32 v[60:61], v[86:87], v[34:35]
	v_pk_add_f32 v[34:35], v[86:87], v[34:35] neg_lo:[0,1] neg_hi:[0,1]
	v_pk_add_f32 v[62:63], v[50:51], v[60:61]
	v_pk_add_f32 v[50:51], v[50:51], v[60:61] neg_lo:[0,1] neg_hi:[0,1]
	v_pk_add_f32 v[60:61], v[58:59], v[34:35] op_sel:[0,1] op_sel_hi:[1,0] neg_hi:[0,1]
	v_pk_add_f32 v[34:35], v[58:59], v[34:35] op_sel:[0,1] op_sel_hi:[1,0] neg_lo:[0,1]
	v_pk_add_f32 v[58:59], v[56:57], v[40:41]
	v_pk_add_f32 v[40:41], v[56:57], v[40:41] neg_lo:[0,1] neg_hi:[0,1]
	v_pk_add_f32 v[56:57], v[84:85], v[32:33]
	v_pk_add_f32 v[32:33], v[84:85], v[32:33] neg_lo:[0,1] neg_hi:[0,1]
	v_pk_add_f32 v[64:65], v[58:59], v[56:57]
	v_pk_add_f32 v[56:57], v[58:59], v[56:57] neg_lo:[0,1] neg_hi:[0,1]
	v_pk_add_f32 v[58:59], v[40:41], v[32:33] op_sel:[0,1] op_sel_hi:[1,0] neg_hi:[0,1]
	v_pk_add_f32 v[32:33], v[40:41], v[32:33] op_sel:[0,1] op_sel_hi:[1,0] neg_lo:[0,1]
	v_pk_mul_f32 v[40:41], v[52:53], s[6:7] op_sel:[0,0] op_sel_hi:[0,1]
	v_pk_fma_f32 v[40:41], v[52:53], s[6:7], v[40:41] op_sel:[1,1,0] op_sel_hi:[1,0,1] neg_lo:[0,1,0]
	v_pk_mul_f32 v[52:53], v[36:37], s[10:11] op_sel:[0,0] op_sel_hi:[0,1]
	v_pk_fma_f32 v[52:53], v[36:37], s[10:11], v[52:53] op_sel:[1,1,0] op_sel_hi:[1,0,1] neg_lo:[0,1,0]
	v_pk_add_f32 v[36:37], v[60:61], v[60:61] op_sel:[0,1] op_sel_hi:[1,0] neg_hi:[0,1]
	v_pk_add_f32 v[44:45], v[44:45], v[44:45] op_sel:[0,1] op_sel_hi:[1,0] neg_hi:[0,1]
	s_nop 0
	v_pk_mul_f32 v[60:61], v[58:59], s[10:11] op_sel:[0,0] op_sel_hi:[0,1]
	v_pk_fma_f32 v[60:61], v[58:59], s[10:11], v[60:61] op_sel:[1,1,0] op_sel_hi:[1,0,1] neg_lo:[0,1,0]
	v_pk_mul_f32 v[58:59], v[32:33], s[14:15] op_sel:[0,0] op_sel_hi:[0,1]
	v_pk_fma_f32 v[58:59], v[32:33], s[14:15], v[58:59] op_sel:[1,1,0] op_sel_hi:[1,0,1] neg_lo:[0,1,0]
	v_pk_add_f32 v[32:33], v[48:49], v[62:63]
	v_pk_mul_f32 v[36:37], v[36:37], s[8:9]
	v_pk_add_f32 v[48:49], v[48:49], v[62:63] neg_lo:[0,1] neg_hi:[0,1]
	v_pk_add_f32 v[62:63], v[54:55], v[64:65]
	v_pk_add_f32 v[54:55], v[54:55], v[64:65] neg_lo:[0,1] neg_hi:[0,1]
	v_pk_mul_f32 v[44:45], v[44:45], s[8:9]
	v_pk_add_f32 v[34:35], v[34:35], v[34:35] op_sel:[0,1] op_sel_hi:[1,0] neg_lo:[0,1]
	v_pk_add_f32 v[56:57], v[56:57], v[56:57] op_sel:[0,1] op_sel_hi:[1,0] neg_lo:[0,1]
	v_pk_add_f32 v[64:65], v[32:33], v[62:63]
	v_pk_add_f32 v[32:33], v[32:33], v[62:63] neg_lo:[0,1] neg_hi:[0,1]
	v_pk_add_f32 v[62:63], v[48:49], v[54:55] op_sel:[0,1] op_sel_hi:[1,0] neg_hi:[0,1]
	v_pk_add_f32 v[48:49], v[48:49], v[54:55] op_sel:[0,1] op_sel_hi:[1,0] neg_lo:[0,1]
	v_pk_add_f32 v[54:55], v[46:47], v[36:37]
	v_pk_add_f32 v[36:37], v[46:47], v[36:37] neg_lo:[0,1] neg_hi:[0,1]
	v_pk_add_f32 v[46:47], v[40:41], v[60:61]
	v_pk_add_f32 v[40:41], v[40:41], v[60:61] neg_lo:[0,1] neg_hi:[0,1]
	v_pk_mul_f32 v[34:35], v[34:35], s[12:13]
	v_pk_mul_f32 v[56:57], v[56:57], s[12:13]
	v_pk_add_f32 v[60:61], v[54:55], v[46:47]
	v_pk_add_f32 v[46:47], v[54:55], v[46:47] neg_lo:[0,1] neg_hi:[0,1]
	v_pk_add_f32 v[54:55], v[36:37], v[40:41] op_sel:[0,1] op_sel_hi:[1,0] neg_hi:[0,1]
	v_pk_add_f32 v[36:37], v[36:37], v[40:41] op_sel:[0,1] op_sel_hi:[1,0] neg_lo:[0,1]
	v_pk_add_f32 v[40:41], v[42:43], v[50:51] op_sel:[0,1] op_sel_hi:[1,0] neg_hi:[0,1]
	v_pk_add_f32 v[42:43], v[42:43], v[50:51] op_sel:[0,1] op_sel_hi:[1,0] neg_lo:[0,1]
	v_pk_add_f32 v[50:51], v[44:45], v[56:57]
	v_pk_add_f32 v[44:45], v[44:45], v[56:57] neg_lo:[0,1] neg_hi:[0,1]
	v_pk_add_f32 v[56:57], v[50:51], v[40:41]
	v_pk_add_f32 v[40:41], v[40:41], v[50:51] neg_lo:[0,1] neg_hi:[0,1]
	v_pk_add_f32 v[50:51], v[42:43], v[44:45] op_sel:[0,1] op_sel_hi:[1,0] neg_hi:[0,1]
	v_pk_add_f32 v[42:43], v[42:43], v[44:45] op_sel:[0,1] op_sel_hi:[1,0] neg_lo:[0,1]
	v_pk_add_f32 v[44:45], v[38:39], v[34:35]
	v_pk_add_f32 v[34:35], v[38:39], v[34:35] neg_lo:[0,1] neg_hi:[0,1]
	v_pk_add_f32 v[38:39], v[52:53], v[58:59]
	v_pk_add_f32 v[52:53], v[52:53], v[58:59] neg_lo:[0,1] neg_hi:[0,1]
	v_pk_add_f32 v[58:59], v[44:45], v[38:39]
	v_pk_add_f32 v[38:39], v[44:45], v[38:39] neg_lo:[0,1] neg_hi:[0,1]
	v_pk_add_f32 v[44:45], v[34:35], v[52:53] op_sel:[0,1] op_sel_hi:[1,0] neg_hi:[0,1]
	v_pk_add_f32 v[34:35], v[34:35], v[52:53] op_sel:[0,1] op_sel_hi:[1,0] neg_lo:[0,1]
	v_pk_mul_f32 v[52:53], v[60:61], v[30:31] op_sel:[0,0] op_sel_hi:[0,1]
	v_pk_fma_f32 v[52:53], v[60:61], v[30:31], v[52:53] op_sel:[1,1,0] op_sel_hi:[1,0,1] neg_lo:[0,1,0]
	v_pk_mul_f32 v[30:31], v[56:57], v[28:29] op_sel:[0,0] op_sel_hi:[0,1]
	v_pk_fma_f32 v[30:31], v[56:57], v[28:29], v[30:31] op_sel:[1,1,0] op_sel_hi:[1,0,1] neg_lo:[0,1,0]
	v_pk_mul_f32 v[28:29], v[58:59], v[26:27] op_sel:[0,0] op_sel_hi:[0,1]
	v_pk_fma_f32 v[28:29], v[58:59], v[26:27], v[28:29] op_sel:[1,1,0] op_sel_hi:[1,0,1] neg_lo:[0,1,0]
	v_pk_mul_f32 v[26:27], v[62:63], v[24:25] op_sel:[0,0] op_sel_hi:[0,1]
	v_pk_fma_f32 v[26:27], v[62:63], v[24:25], v[26:27] op_sel:[1,1,0] op_sel_hi:[1,0,1] neg_lo:[0,1,0]
	v_pk_mul_f32 v[24:25], v[54:55], v[20:21] op_sel:[0,0] op_sel_hi:[0,1]
	v_pk_fma_f32 v[24:25], v[54:55], v[20:21], v[24:25] op_sel:[1,1,0] op_sel_hi:[1,0,1] neg_lo:[0,1,0]
	v_pk_mul_f32 v[20:21], v[50:51], v[16:17] op_sel:[0,0] op_sel_hi:[0,1]
	v_pk_fma_f32 v[20:21], v[50:51], v[16:17], v[20:21] op_sel:[1,1,0] op_sel_hi:[1,0,1] neg_lo:[0,1,0]
	s_nop 0
	v_pk_mul_f32 v[16:17], v[44:45], v[10:11] op_sel:[0,0] op_sel_hi:[0,1]
	v_pk_fma_f32 v[16:17], v[44:45], v[10:11], v[16:17] op_sel:[1,1,0] op_sel_hi:[1,0,1] neg_lo:[0,1,0]
	v_pk_mul_f32 v[10:11], v[32:33], v[22:23] op_sel:[0,0] op_sel_hi:[0,1]
	v_pk_fma_f32 v[10:11], v[32:33], v[22:23], v[10:11] op_sel:[1,1,0] op_sel_hi:[1,0,1] neg_lo:[0,1,0]
	ds_write_b64 v1, v[10:11] offset:17472
	v_pk_mul_f32 v[10:11], v[46:47], v[18:19] op_sel:[0,0] op_sel_hi:[0,1]
	v_pk_fma_f32 v[10:11], v[46:47], v[18:19], v[10:11] op_sel:[1,1,0] op_sel_hi:[1,0,1] neg_lo:[0,1,0]
	ds_write_b64 v1, v[10:11] offset:19656
	v_pk_mul_f32 v[10:11], v[40:41], v[12:13] op_sel:[0,0] op_sel_hi:[0,1]
	v_pk_fma_f32 v[10:11], v[40:41], v[12:13], v[10:11] op_sel:[1,1,0] op_sel_hi:[1,0,1] neg_lo:[0,1,0]
	ds_write_b64 v1, v[10:11] offset:21840
	v_pk_mul_f32 v[10:11], v[38:39], v[14:15] op_sel:[0,0] op_sel_hi:[0,1]
	v_pk_fma_f32 v[10:11], v[38:39], v[14:15], v[10:11] op_sel:[1,1,0] op_sel_hi:[1,0,1] neg_lo:[0,1,0]
	ds_write_b64 v1, v[10:11] offset:24024
	v_pk_mul_f32 v[10:11], v[48:49], v[6:7] op_sel:[0,0] op_sel_hi:[0,1]
	v_pk_fma_f32 v[10:11], v[48:49], v[6:7], v[10:11] op_sel:[1,1,0] op_sel_hi:[1,0,1] neg_lo:[0,1,0]
	v_pk_mul_f32 v[6:7], v[36:37], v[8:9] op_sel:[0,0] op_sel_hi:[0,1]
	v_pk_fma_f32 v[6:7], v[36:37], v[8:9], v[6:7] op_sel:[1,1,0] op_sel_hi:[1,0,1] neg_lo:[0,1,0]
	ds_write_b64 v1, v[6:7] offset:28392
	v_pk_mul_f32 v[6:7], v[42:43], v[4:5] op_sel:[0,0] op_sel_hi:[0,1]
	v_pk_fma_f32 v[6:7], v[42:43], v[4:5], v[6:7] op_sel:[1,1,0] op_sel_hi:[1,0,1] neg_lo:[0,1,0]
	v_pk_mul_f32 v[4:5], v[34:35], v[2:3] op_sel:[0,0] op_sel_hi:[0,1]
	v_pk_fma_f32 v[4:5], v[34:35], v[2:3], v[4:5] op_sel:[1,1,0] op_sel_hi:[1,0,1] neg_lo:[0,1,0]
	ds_write_b64 v1, v[64:65]
	ds_write_b64 v1, v[52:53] offset:2184
	ds_write_b64 v1, v[30:31] offset:4368
	ds_write_b64 v1, v[28:29] offset:6552
	ds_write_b64 v1, v[26:27] offset:8736
	ds_write_b64 v1, v[24:25] offset:10920
	ds_write_b64 v1, v[20:21] offset:13104
	ds_write_b64 v1, v[16:17] offset:15288
	ds_write_b64 v1, v[10:11] offset:26208
	ds_write_b64 v1, v[6:7] offset:30576
	ds_write_b64 v1, v[4:5] offset:32760
	s_waitcnt lgkmcnt(0)
	s_barrier
	ds_read2_b64 v[2:5], v96 offset1:16
	ds_read2_b64 v[6:9], v96 offset0:32 offset1:48
	ds_read2_b64 v[10:13], v96 offset0:64 offset1:80
	ds_read2_b64 v[14:17], v96 offset0:128 offset1:144
	ds_read2_b64 v[18:21], v96 offset0:96 offset1:112
	ds_read2_b64 v[22:25], v96 offset0:192 offset1:208
	ds_read2_b64 v[26:29], v96 offset0:160 offset1:176
	ds_read2_b64 v[30:33], v96 offset0:224 offset1:240
	s_waitcnt lgkmcnt(4)
	v_pk_add_f32 v[34:35], v[2:3], v[14:15]
	v_pk_add_f32 v[2:3], v[2:3], v[14:15] neg_lo:[0,1] neg_hi:[0,1]
	s_waitcnt lgkmcnt(2)
	v_pk_add_f32 v[14:15], v[10:11], v[22:23]
	v_pk_add_f32 v[10:11], v[10:11], v[22:23] neg_lo:[0,1] neg_hi:[0,1]
	v_pk_add_f32 v[22:23], v[34:35], v[14:15]
	v_pk_add_f32 v[14:15], v[34:35], v[14:15] neg_lo:[0,1] neg_hi:[0,1]
	v_pk_add_f32 v[34:35], v[2:3], v[10:11] op_sel:[0,1] op_sel_hi:[1,0] neg_hi:[0,1]
	v_pk_add_f32 v[2:3], v[2:3], v[10:11] op_sel:[0,1] op_sel_hi:[1,0] neg_lo:[0,1]
	v_pk_add_f32 v[10:11], v[4:5], v[16:17]
	v_pk_add_f32 v[4:5], v[4:5], v[16:17] neg_lo:[0,1] neg_hi:[0,1]
	v_pk_add_f32 v[16:17], v[12:13], v[24:25]
	v_pk_add_f32 v[12:13], v[12:13], v[24:25] neg_lo:[0,1] neg_hi:[0,1]
	v_pk_add_f32 v[24:25], v[10:11], v[16:17]
	v_pk_add_f32 v[10:11], v[10:11], v[16:17] neg_lo:[0,1] neg_hi:[0,1]
	v_pk_add_f32 v[16:17], v[4:5], v[12:13] op_sel:[0,1] op_sel_hi:[1,0] neg_hi:[0,1]
	v_pk_add_f32 v[4:5], v[4:5], v[12:13] op_sel:[0,1] op_sel_hi:[1,0] neg_lo:[0,1]
	s_waitcnt lgkmcnt(1)
	v_pk_add_f32 v[12:13], v[6:7], v[26:27]
	v_pk_add_f32 v[6:7], v[6:7], v[26:27] neg_lo:[0,1] neg_hi:[0,1]
	s_waitcnt lgkmcnt(0)
	v_pk_add_f32 v[26:27], v[18:19], v[30:31]
	v_pk_add_f32 v[18:19], v[18:19], v[30:31] neg_lo:[0,1] neg_hi:[0,1]
	v_pk_add_f32 v[30:31], v[12:13], v[26:27]
	v_pk_add_f32 v[12:13], v[12:13], v[26:27] neg_lo:[0,1] neg_hi:[0,1]
	v_pk_add_f32 v[26:27], v[6:7], v[18:19] op_sel:[0,1] op_sel_hi:[1,0] neg_hi:[0,1]
	v_pk_add_f32 v[6:7], v[6:7], v[18:19] op_sel:[0,1] op_sel_hi:[1,0] neg_lo:[0,1]
	v_pk_add_f32 v[18:19], v[8:9], v[28:29]
	v_pk_add_f32 v[8:9], v[8:9], v[28:29] neg_lo:[0,1] neg_hi:[0,1]
	v_pk_add_f32 v[28:29], v[20:21], v[32:33]
	v_pk_add_f32 v[20:21], v[20:21], v[32:33] neg_lo:[0,1] neg_hi:[0,1]
	v_pk_add_f32 v[32:33], v[18:19], v[28:29]
	v_pk_add_f32 v[18:19], v[18:19], v[28:29] neg_lo:[0,1] neg_hi:[0,1]
	v_pk_add_f32 v[28:29], v[8:9], v[20:21] op_sel:[0,1] op_sel_hi:[1,0] neg_hi:[0,1]
	v_pk_add_f32 v[8:9], v[8:9], v[20:21] op_sel:[0,1] op_sel_hi:[1,0] neg_lo:[0,1]
	v_pk_mul_f32 v[20:21], v[16:17], s[6:7] op_sel:[0,0] op_sel_hi:[0,1]
	v_pk_fma_f32 v[20:21], v[16:17], s[6:7], v[20:21] op_sel:[1,1,0] op_sel_hi:[1,0,1] neg_lo:[0,1,0]
	v_pk_mul_f32 v[16:17], v[4:5], s[10:11] op_sel:[0,0] op_sel_hi:[0,1]
	v_pk_fma_f32 v[16:17], v[4:5], s[10:11], v[16:17] op_sel:[1,1,0] op_sel_hi:[1,0,1] neg_lo:[0,1,0]
	v_pk_add_f32 v[4:5], v[26:27], v[26:27] op_sel:[0,1] op_sel_hi:[1,0] neg_hi:[0,1]
	v_pk_add_f32 v[10:11], v[10:11], v[10:11] op_sel:[0,1] op_sel_hi:[1,0] neg_hi:[0,1]
	s_nop 0
	v_pk_mul_f32 v[26:27], v[28:29], s[10:11] op_sel:[0,0] op_sel_hi:[0,1]
	v_pk_fma_f32 v[26:27], v[28:29], s[10:11], v[26:27] op_sel:[1,1,0] op_sel_hi:[1,0,1] neg_lo:[0,1,0]
	v_pk_mul_f32 v[28:29], v[8:9], s[14:15] op_sel:[0,0] op_sel_hi:[0,1]
	v_pk_fma_f32 v[28:29], v[8:9], s[14:15], v[28:29] op_sel:[1,1,0] op_sel_hi:[1,0,1] neg_lo:[0,1,0]
	v_pk_add_f32 v[8:9], v[22:23], v[30:31]
	v_pk_mul_f32 v[4:5], v[4:5], s[8:9]
	v_pk_add_f32 v[22:23], v[22:23], v[30:31] neg_lo:[0,1] neg_hi:[0,1]
	v_pk_add_f32 v[30:31], v[24:25], v[32:33]
	v_pk_add_f32 v[24:25], v[24:25], v[32:33] neg_lo:[0,1] neg_hi:[0,1]
	v_pk_add_f32 v[18:19], v[18:19], v[18:19] op_sel:[0,1] op_sel_hi:[1,0] neg_lo:[0,1]
	v_pk_add_f32 v[32:33], v[8:9], v[30:31]
	v_pk_add_f32 v[30:31], v[8:9], v[30:31] neg_lo:[0,1] neg_hi:[0,1]
	v_pk_add_f32 v[36:37], v[22:23], v[24:25] op_sel:[0,1] op_sel_hi:[1,0] neg_hi:[0,1]
	v_pk_add_f32 v[22:23], v[22:23], v[24:25] op_sel:[0,1] op_sel_hi:[1,0] neg_lo:[0,1]
	v_pk_add_f32 v[8:9], v[34:35], v[4:5]
	v_pk_add_f32 v[4:5], v[34:35], v[4:5] neg_lo:[0,1] neg_hi:[0,1]
	v_pk_add_f32 v[24:25], v[20:21], v[26:27]
	v_pk_add_f32 v[20:21], v[20:21], v[26:27] neg_lo:[0,1] neg_hi:[0,1]
	v_pk_mul_f32 v[10:11], v[10:11], s[8:9]
	v_pk_add_f32 v[6:7], v[6:7], v[6:7] op_sel:[0,1] op_sel_hi:[1,0] neg_lo:[0,1]
	v_pk_mul_f32 v[18:19], v[18:19], s[12:13]
	v_pk_add_f32 v[26:27], v[8:9], v[24:25]
	v_pk_add_f32 v[24:25], v[8:9], v[24:25] neg_lo:[0,1] neg_hi:[0,1]
	v_pk_add_f32 v[34:35], v[4:5], v[20:21] op_sel:[0,1] op_sel_hi:[1,0] neg_hi:[0,1]
	v_pk_add_f32 v[20:21], v[4:5], v[20:21] op_sel:[0,1] op_sel_hi:[1,0] neg_lo:[0,1]
	v_pk_add_f32 v[4:5], v[14:15], v[12:13] op_sel:[0,1] op_sel_hi:[1,0] neg_hi:[0,1]
	v_pk_add_f32 v[8:9], v[14:15], v[12:13] op_sel:[0,1] op_sel_hi:[1,0] neg_lo:[0,1]
	v_pk_add_f32 v[12:13], v[10:11], v[18:19]
	v_pk_mul_f32 v[6:7], v[6:7], s[12:13]
	v_pk_add_f32 v[10:11], v[10:11], v[18:19] neg_lo:[0,1] neg_hi:[0,1]
	v_pk_add_f32 v[14:15], v[12:13], v[4:5]
	v_pk_add_f32 v[12:13], v[4:5], v[12:13] neg_lo:[0,1] neg_hi:[0,1]
	v_pk_add_f32 v[4:5], v[2:3], v[6:7]
	v_pk_add_f32 v[2:3], v[2:3], v[6:7] neg_lo:[0,1] neg_hi:[0,1]
	v_mov_b32_e32 v1, v0
	v_pk_add_f32 v[18:19], v[8:9], v[10:11] op_sel:[0,1] op_sel_hi:[1,0] neg_hi:[0,1]
	v_pk_add_f32 v[10:11], v[8:9], v[10:11] op_sel:[0,1] op_sel_hi:[1,0] neg_lo:[0,1]
	v_pk_add_f32 v[8:9], v[16:17], v[28:29] neg_lo:[0,1] neg_hi:[0,1]
	v_pk_add_f32 v[6:7], v[16:17], v[28:29]
	v_pk_add_f32 v[38:39], v[2:3], v[8:9] op_sel:[0,1] op_sel_hi:[1,0] neg_hi:[0,1]
	v_pk_add_f32 v[40:41], v[2:3], v[8:9] op_sel:[0,1] op_sel_hi:[1,0] neg_lo:[0,1]
	v_ashrrev_i32_e32 v2, 4, v1
	v_lshlrev_b32_e32 v44, 3, v2
	v_add_u32_e32 v45, 0x8800, v44
	v_and_b32_e32 v1, 15, v1
	v_pk_add_f32 v[16:17], v[4:5], v[6:7]
	v_pk_add_f32 v[28:29], v[4:5], v[6:7] neg_lo:[0,1] neg_hi:[0,1]
	ds_read2_b64 v[2:5], v45 offset0:16 offset1:32
	v_mad_u32_u24 v1, v1, s5, v44
	ds_read2_b64 v[6:9], v45 offset0:48 offset1:64
	s_waitcnt lgkmcnt(1)
	v_pk_mul_f32 v[42:43], v[26:27], v[2:3] op_sel:[0,0] op_sel_hi:[0,1]
	v_pk_fma_f32 v[42:43], v[26:27], v[2:3], v[42:43] op_sel:[1,1,0] op_sel_hi:[1,0,1] neg_lo:[0,1,0]
	v_pk_mul_f32 v[26:27], v[14:15], v[4:5] op_sel:[0,0] op_sel_hi:[0,1]
	v_pk_fma_f32 v[26:27], v[14:15], v[4:5], v[26:27] op_sel:[1,1,0] op_sel_hi:[1,0,1] neg_lo:[0,1,0]
	s_waitcnt lgkmcnt(0)
	v_pk_mul_f32 v[14:15], v[16:17], v[6:7] op_sel:[0,0] op_sel_hi:[0,1]
	v_pk_fma_f32 v[14:15], v[16:17], v[6:7], v[14:15] op_sel:[1,1,0] op_sel_hi:[1,0,1] neg_lo:[0,1,0]
	ds_write2_b64 v1, v[26:27], v[14:15] offset0:32 offset1:48
	v_pk_mul_f32 v[14:15], v[36:37], v[8:9] op_sel:[0,0] op_sel_hi:[0,1]
	v_pk_fma_f32 v[14:15], v[36:37], v[8:9], v[14:15] op_sel:[1,1,0] op_sel_hi:[1,0,1] neg_lo:[0,1,0]
	ds_read2_b64 v[2:5], v45 offset0:80 offset1:96
	s_waitcnt lgkmcnt(0)
	v_pk_mul_f32 v[16:17], v[34:35], v[2:3] op_sel:[0,0] op_sel_hi:[0,1]
	v_pk_fma_f32 v[16:17], v[34:35], v[2:3], v[16:17] op_sel:[1,1,0] op_sel_hi:[1,0,1] neg_lo:[0,1,0]
	ds_write2_b64 v1, v[14:15], v[16:17] offset0:64 offset1:80
	v_pk_mul_f32 v[14:15], v[18:19], v[4:5] op_sel:[0,0] op_sel_hi:[0,1]
	v_pk_fma_f32 v[14:15], v[18:19], v[4:5], v[14:15] op_sel:[1,1,0] op_sel_hi:[1,0,1] neg_lo:[0,1,0]
	ds_read2_b64 v[6:9], v45 offset0:112 offset1:128
	ds_read2_b64 v[2:5], v45 offset0:144 offset1:160
	s_waitcnt lgkmcnt(1)
	v_pk_mul_f32 v[16:17], v[38:39], v[6:7] op_sel:[0,0] op_sel_hi:[0,1]
	v_pk_fma_f32 v[16:17], v[38:39], v[6:7], v[16:17] op_sel:[1,1,0] op_sel_hi:[1,0,1] neg_lo:[0,1,0]
	ds_write2_b64 v1, v[14:15], v[16:17] offset0:96 offset1:112
	v_pk_mul_f32 v[14:15], v[30:31], v[8:9] op_sel:[0,0] op_sel_hi:[0,1]
	v_pk_fma_f32 v[14:15], v[30:31], v[8:9], v[14:15] op_sel:[1,1,0] op_sel_hi:[1,0,1] neg_lo:[0,1,0]
	ds_read2_b64 v[6:9], v45 offset0:176 offset1:192
	s_waitcnt lgkmcnt(2)
	v_pk_mul_f32 v[16:17], v[24:25], v[2:3] op_sel:[0,0] op_sel_hi:[0,1]
	v_pk_fma_f32 v[16:17], v[24:25], v[2:3], v[16:17] op_sel:[1,1,0] op_sel_hi:[1,0,1] neg_lo:[0,1,0]
	ds_write2_b64 v1, v[14:15], v[16:17] offset0:128 offset1:144
	v_pk_mul_f32 v[14:15], v[12:13], v[4:5] op_sel:[0,0] op_sel_hi:[0,1]
	v_pk_fma_f32 v[14:15], v[12:13], v[4:5], v[14:15] op_sel:[1,1,0] op_sel_hi:[1,0,1] neg_lo:[0,1,0]
	ds_read2_b64 v[2:5], v45 offset0:208 offset1:224
	s_waitcnt lgkmcnt(2)
	v_pk_mul_f32 v[12:13], v[28:29], v[6:7] op_sel:[0,0] op_sel_hi:[0,1]
	v_pk_fma_f32 v[12:13], v[28:29], v[6:7], v[12:13] op_sel:[1,1,0] op_sel_hi:[1,0,1] neg_lo:[0,1,0]
	ds_write2_b64 v1, v[32:33], v[42:43] offset1:16
	ds_write2_b64 v1, v[14:15], v[12:13] offset0:160 offset1:176
	ds_read_b64 v[6:7], v44 offset:36736
	v_pk_mul_f32 v[12:13], v[22:23], v[8:9] op_sel:[0,0] op_sel_hi:[0,1]
	v_pk_fma_f32 v[12:13], v[22:23], v[8:9], v[12:13] op_sel:[1,1,0] op_sel_hi:[1,0,1] neg_lo:[0,1,0]
	s_waitcnt lgkmcnt(3)
	v_pk_mul_f32 v[8:9], v[20:21], v[2:3] op_sel:[0,0] op_sel_hi:[0,1]
	v_pk_fma_f32 v[8:9], v[20:21], v[2:3], v[8:9] op_sel:[1,1,0] op_sel_hi:[1,0,1] neg_lo:[0,1,0]
	ds_write2_b64 v1, v[12:13], v[8:9] offset0:192 offset1:208
	v_pk_mul_f32 v[2:3], v[10:11], v[4:5] op_sel:[0,0] op_sel_hi:[0,1]
	v_pk_fma_f32 v[2:3], v[10:11], v[4:5], v[2:3] op_sel:[1,1,0] op_sel_hi:[1,0,1] neg_lo:[0,1,0]
	s_waitcnt lgkmcnt(1)
	v_pk_mul_f32 v[4:5], v[40:41], v[6:7] op_sel:[0,0] op_sel_hi:[0,1]
	v_pk_fma_f32 v[4:5], v[40:41], v[6:7], v[4:5] op_sel:[1,1,0] op_sel_hi:[1,0,1] neg_lo:[0,1,0]
	ds_write2_b64 v1, v[2:3], v[4:5] offset0:224 offset1:240
	v_mov_b32_e32 v1, v0
	s_waitcnt lgkmcnt(0)
	s_barrier
	v_mov_b32_e32 v53, 0
	v_and_b32_e32 v2, 15, v1
	v_and_b32_e32 v1, 0x1ffffff0, v1
	v_lshlrev_b32_e32 v1, 3, v1
	v_mad_u32_u24 v1, v2, s5, v1
	ds_read2_b64 v[2:5], v1 offset1:1
	ds_read2_b64 v[6:9], v1 offset0:2 offset1:3
	ds_read2_b64 v[10:13], v1 offset0:8 offset1:9
	ds_read2_b64 v[18:21], v1 offset0:4 offset1:5
	ds_read2_b64 v[22:25], v1 offset0:6 offset1:7
	ds_read2_b64 v[26:29], v1 offset0:12 offset1:13
	ds_read2_b64 v[30:33], v1 offset0:10 offset1:11
	ds_read2_b64 v[34:37], v1 offset0:14 offset1:15
	s_waitcnt lgkmcnt(5)
	v_pk_add_f32 v[14:15], v[2:3], v[10:11]
	v_pk_add_f32 v[2:3], v[2:3], v[10:11] neg_lo:[0,1] neg_hi:[0,1]
	s_waitcnt lgkmcnt(2)
	v_pk_add_f32 v[10:11], v[18:19], v[26:27]
	v_pk_add_f32 v[18:19], v[18:19], v[26:27] neg_lo:[0,1] neg_hi:[0,1]
	v_pk_add_f32 v[26:27], v[14:15], v[10:11]
	v_pk_add_f32 v[16:17], v[14:15], v[10:11] neg_lo:[0,1] neg_hi:[0,1]
	v_pk_add_f32 v[14:15], v[2:3], v[18:19] op_sel:[0,1] op_sel_hi:[1,0] neg_hi:[0,1]
	v_pk_add_f32 v[18:19], v[2:3], v[18:19] op_sel:[0,1] op_sel_hi:[1,0] neg_lo:[0,1]
	v_pk_add_f32 v[2:3], v[4:5], v[12:13]
	v_pk_add_f32 v[10:11], v[20:21], v[28:29]
	v_pk_add_f32 v[4:5], v[4:5], v[12:13] neg_lo:[0,1] neg_hi:[0,1]
	v_pk_add_f32 v[12:13], v[20:21], v[28:29] neg_lo:[0,1] neg_hi:[0,1]
	v_pk_add_f32 v[28:29], v[2:3], v[10:11]
	v_pk_add_f32 v[2:3], v[2:3], v[10:11] neg_lo:[0,1] neg_hi:[0,1]
	v_pk_add_f32 v[10:11], v[4:5], v[12:13] op_sel:[0,1] op_sel_hi:[1,0] neg_hi:[0,1]
	v_pk_add_f32 v[4:5], v[4:5], v[12:13] op_sel:[0,1] op_sel_hi:[1,0] neg_lo:[0,1]
	s_waitcnt lgkmcnt(1)
	v_pk_add_f32 v[12:13], v[6:7], v[30:31]
	s_waitcnt lgkmcnt(0)
	v_pk_add_f32 v[20:21], v[22:23], v[34:35]
	v_pk_add_f32 v[2:3], v[2:3], v[2:3] op_sel:[0,1] op_sel_hi:[1,0] neg_hi:[0,1]
	v_pk_add_f32 v[6:7], v[6:7], v[30:31] neg_lo:[0,1] neg_hi:[0,1]
	v_pk_add_f32 v[22:23], v[22:23], v[34:35] neg_lo:[0,1] neg_hi:[0,1]
	v_pk_add_f32 v[30:31], v[12:13], v[20:21]
	v_pk_add_f32 v[20:21], v[12:13], v[20:21] neg_lo:[0,1] neg_hi:[0,1]
	v_pk_add_f32 v[12:13], v[6:7], v[22:23] op_sel:[0,1] op_sel_hi:[1,0] neg_hi:[0,1]
	v_pk_mul_f32 v[44:45], v[2:3], s[8:9]
	v_pk_add_f32 v[6:7], v[6:7], v[22:23] op_sel:[0,1] op_sel_hi:[1,0] neg_lo:[0,1]
	v_pk_add_f32 v[22:23], v[8:9], v[32:33]
	v_pk_add_f32 v[2:3], v[12:13], v[12:13] op_sel:[0,1] op_sel_hi:[1,0] neg_hi:[0,1]
	v_pk_add_f32 v[8:9], v[8:9], v[32:33] neg_lo:[0,1] neg_hi:[0,1]
	v_pk_add_f32 v[32:33], v[24:25], v[36:37]
	v_pk_mul_f32 v[12:13], v[2:3], s[8:9]
	v_pk_add_f32 v[2:3], v[6:7], v[6:7] op_sel:[0,1] op_sel_hi:[1,0] neg_lo:[0,1]
	v_pk_add_f32 v[24:25], v[24:25], v[36:37] neg_lo:[0,1] neg_hi:[0,1]
	v_pk_add_f32 v[34:35], v[22:23], v[32:33]
	v_pk_add_f32 v[32:33], v[22:23], v[32:33] neg_lo:[0,1] neg_hi:[0,1]
	v_pk_mul_f32 v[54:55], v[2:3], s[12:13]
	v_pk_add_f32 v[36:37], v[8:9], v[24:25] op_sel:[0,1] op_sel_hi:[1,0] neg_hi:[0,1]
	v_pk_add_f32 v[8:9], v[8:9], v[24:25] op_sel:[0,1] op_sel_hi:[1,0] neg_lo:[0,1]
	v_pk_mul_f32 v[22:23], v[4:5], s[10:11] op_sel:[0,0] op_sel_hi:[0,1]
	v_pk_fma_f32 v[22:23], v[4:5], s[10:11], v[22:23] op_sel:[1,1,0] op_sel_hi:[1,0,1] neg_lo:[0,1,0]
	v_pk_add_f32 v[4:5], v[28:29], v[34:35]
	v_pk_add_f32 v[2:3], v[32:33], v[32:33] op_sel:[0,1] op_sel_hi:[1,0] neg_lo:[0,1]
	v_pk_add_f32 v[28:29], v[28:29], v[34:35] neg_lo:[0,1] neg_hi:[0,1]
	v_pk_mul_f32 v[32:33], v[2:3], s[12:13]
	v_pk_add_f32 v[2:3], v[26:27], v[30:31]
	v_pk_add_f32 v[26:27], v[26:27], v[30:31] neg_lo:[0,1] neg_hi:[0,1]
	v_pk_mul_f32 v[24:25], v[10:11], s[6:7] op_sel:[0,0] op_sel_hi:[0,1]
	v_pk_fma_f32 v[24:25], v[10:11], s[6:7], v[24:25] op_sel:[1,1,0] op_sel_hi:[1,0,1] neg_lo:[0,1,0]
	v_pk_mul_f32 v[6:7], v[36:37], s[10:11] op_sel:[0,0] op_sel_hi:[0,1]
	v_pk_fma_f32 v[6:7], v[36:37], s[10:11], v[6:7] op_sel:[1,1,0] op_sel_hi:[1,0,1] neg_lo:[0,1,0]
	v_pk_mul_f32 v[56:57], v[8:9], s[14:15] op_sel:[0,0] op_sel_hi:[0,1]
	v_pk_fma_f32 v[56:57], v[8:9], s[14:15], v[56:57] op_sel:[1,1,0] op_sel_hi:[1,0,1] neg_lo:[0,1,0]
	v_pk_add_f32 v[10:11], v[2:3], v[4:5]
	v_lshlrev_b32_e32 v34, 2, v0
	v_pk_add_f32 v[4:5], v[2:3], v[4:5] neg_lo:[0,1] neg_hi:[0,1]
	v_pk_add_f32 v[8:9], v[26:27], v[28:29] op_sel:[0,1] op_sel_hi:[1,0] neg_hi:[0,1]
	v_pk_add_f32 v[2:3], v[26:27], v[28:29] op_sel:[0,1] op_sel_hi:[1,0] neg_lo:[0,1]
	v_pk_add_f32 v[26:27], v[14:15], v[12:13]
	v_pk_add_f32 v[28:29], v[24:25], v[6:7]
	v_add_u32_e32 v1, 0x400, v34
	v_pk_add_f32 v[14:15], v[14:15], v[12:13] neg_lo:[0,1] neg_hi:[0,1]
	v_pk_add_f32 v[30:31], v[24:25], v[6:7] neg_lo:[0,1] neg_hi:[0,1]
	v_pk_add_f32 v[12:13], v[26:27], v[28:29]
	v_pk_add_f32 v[6:7], v[26:27], v[28:29] neg_lo:[0,1] neg_hi:[0,1]
	v_add_u32_e32 v24, 0x800, v34
	v_add_u32_e32 v25, 0xc00, v34
	v_add_u32_e32 v26, 0x1000, v34
	v_add_u32_e32 v27, 0x1400, v34
	v_add_u32_e32 v28, 0x1800, v34
	v_add_u32_e32 v29, 0x1c00, v34
	v_add_u32_e32 v35, 0x2000, v34
	s_waitcnt vmcnt(0)
	v_mov_b32_e32 v1, v113
	s_nop 0
	v_mov_b32_e32 v36, v114
	v_mov_b32_e32 v37, v115
	v_mov_b32_e32 v38, v116
	v_mov_b32_e32 v39, v117
	v_mov_b32_e32 v40, v118
	v_mov_b32_e32 v41, v119
	v_mov_b32_e32 v42, v120
	v_add_u32_e32 v24, 0x2400, v34
	v_add_u32_e32 v25, 0x2800, v34
	v_add_u32_e32 v26, 0x2c00, v34
	v_add_u32_e32 v27, 0x3000, v34
	v_add_u32_e32 v28, 0x3400, v34
	v_add_u32_e32 v35, 0x3800, v34
	v_mov_b32_e32 v52, v112
	v_mov_b32_e32 v43, v126
	v_add_u32_e32 v29, 0x3c00, v34
	v_mov_b32_e32 v47, v121
	v_mov_b32_e32 v48, v122
	v_mov_b32_e32 v49, v123
	v_mov_b32_e32 v50, v124
	v_mov_b32_e32 v51, v125
	v_mov_b32_e32 v46, v127
	v_pk_add_f32 v[26:27], v[16:17], v[20:21] op_sel:[0,1] op_sel_hi:[1,0] neg_hi:[0,1]
	v_pk_add_f32 v[16:17], v[16:17], v[20:21] op_sel:[0,1] op_sel_hi:[1,0] neg_lo:[0,1]
	v_pk_add_f32 v[20:21], v[44:45], v[32:33]
	v_pk_add_f32 v[28:29], v[44:45], v[32:33] neg_lo:[0,1] neg_hi:[0,1]
	v_pk_add_f32 v[24:25], v[14:15], v[30:31] op_sel:[0,1] op_sel_hi:[1,0] neg_hi:[0,1]
	v_pk_add_f32 v[14:15], v[14:15], v[30:31] op_sel:[0,1] op_sel_hi:[1,0] neg_lo:[0,1]
	v_pk_add_f32 v[30:31], v[20:21], v[26:27]
	v_pk_add_f32 v[20:21], v[26:27], v[20:21] neg_lo:[0,1] neg_hi:[0,1]
	v_pk_add_f32 v[26:27], v[16:17], v[28:29] op_sel:[0,1] op_sel_hi:[1,0] neg_hi:[0,1]
	v_pk_add_f32 v[16:17], v[16:17], v[28:29] op_sel:[0,1] op_sel_hi:[1,0] neg_lo:[0,1]
	v_pk_add_f32 v[28:29], v[18:19], v[54:55]
	v_pk_add_f32 v[44:45], v[22:23], v[56:57]
	s_mov_b32 s2, 0xff61b1e6
	v_pk_add_f32 v[18:19], v[18:19], v[54:55] neg_lo:[0,1] neg_hi:[0,1]
	v_pk_add_f32 v[54:55], v[22:23], v[56:57] neg_lo:[0,1] neg_hi:[0,1]
	v_pk_add_f32 v[32:33], v[28:29], v[44:45]
	v_pk_add_f32 v[22:23], v[28:29], v[44:45] neg_lo:[0,1] neg_hi:[0,1]
	v_max3_f32 v44, v10, s2, v12
	v_max3_f32 v44, v44, v30, v32
	v_max3_f32 v44, v44, v8, v24
	v_pk_add_f32 v[28:29], v[18:19], v[54:55] op_sel:[0,1] op_sel_hi:[1,0] neg_hi:[0,1]
	v_pk_add_f32 v[18:19], v[18:19], v[54:55] op_sel:[0,1] op_sel_hi:[1,0] neg_lo:[0,1]
	v_max3_f32 v45, -v11, s2, -v13
	v_max3_f32 v44, v44, v26, v28
	v_max3_f32 v44, v44, v4, v6
	v_max3_f32 v44, v44, v20, v22
	v_max3_f32 v44, v44, v2, v14
	v_max3_f32 v44, v44, v16, v18
	v_max3_f32 v45, v45, -v31, -v33
	v_max3_f32 v45, v45, -v9, -v25
	v_mov_b32_dpp v53, v44 quad_perm:[1,0,3,2] row_mask:0xf bank_mask:0xf
	v_max_f32_e32 v53, v53, v53
	v_max_f32_e32 v44, v44, v53
	v_mov_b32_e32 v53, 0
	v_max3_f32 v45, v45, -v27, -v29
	v_max3_f32 v45, v45, -v5, -v7
	v_mov_b32_dpp v53, v44 quad_perm:[2,3,0,1] row_mask:0xf bank_mask:0xf
	v_max_f32_e32 v53, v53, v53
	v_max_f32_e32 v44, v44, v53
	v_mov_b32_e32 v53, 0
	v_max3_f32 v45, v45, -v21, -v23
	v_max3_f32 v45, v45, -v3, -v15
	v_mov_b32_dpp v53, v44 row_half_mirror row_mask:0xf bank_mask:0xf
	v_max_f32_e32 v53, v53, v53
	v_max_f32_e32 v44, v44, v53
	v_mov_b32_e32 v53, 0
	v_max3_f32 v45, v45, -v17, -v19
	s_nop 0
	v_mov_b32_dpp v53, v44 row_mirror row_mask:0xf bank_mask:0xf
	v_max_f32_e32 v53, v53, v53
	v_max_f32_e32 v44, v44, v53
	s_nop 0
	v_readlane_b32 s5, v44, 0
	v_readlane_b32 s6, v44, 16
	v_readlane_b32 s7, v44, 32
	v_readlane_b32 s8, v44, 48
	v_mov_b32_e32 v44, 0
	s_nop 1
	v_mov_b32_dpp v44, v45 quad_perm:[1,0,3,2] row_mask:0xf bank_mask:0xf
	v_max_f32_e32 v44, v44, v44
	v_max_f32_e32 v44, v45, v44
	v_mov_b32_e32 v45, 0
	s_nop 1
	v_mov_b32_dpp v45, v44 quad_perm:[2,3,0,1] row_mask:0xf bank_mask:0xf
	v_max_f32_e32 v45, v45, v45
	v_max_f32_e32 v44, v44, v45
	v_mov_b32_e32 v45, 0
	s_nop 1
	v_mov_b32_dpp v45, v44 row_half_mirror row_mask:0xf bank_mask:0xf
	v_max_f32_e32 v45, v45, v45
	v_max_f32_e32 v44, v44, v45
	v_mov_b32_e32 v45, 0
	s_nop 1
	v_mov_b32_dpp v45, v44 row_mirror row_mask:0xf bank_mask:0xf
	v_max_f32_e32 v45, v45, v45
	v_max_f32_e32 v44, v44, v45
	v_and_b32_e32 v45, 63, v0
	v_readlane_b32 s9, v44, 0
	v_readlane_b32 s10, v44, 16
	v_readlane_b32 s11, v44, 32
	v_readlane_b32 s12, v44, 48
	v_ashrrev_i32_e32 v44, 6, v0
	v_cmp_eq_u32_e32 vcc, 0, v45
	v_lshlrev_b32_e32 v61, 3, v44
	s_and_saveexec_b64 s[2:3], vcc
	s_cbranch_execz .LBB1_10
	v_max_f32_e64 v44, s12, s12
	v_max_f32_e64 v45, s11, s11
	v_max_f32_e32 v44, v45, v44
	v_mov_b32_e32 v45, s10
	v_max3_f32 v45, s9, v45, v44
	v_max_f32_e64 v44, s8, s8
	v_max_f32_e64 v53, s7, s7
	v_max_f32_e32 v44, v53, v44
	v_mov_b32_e32 v53, s6
	v_max3_f32 v44, s5, v53, v44
	ds_write_b64 v61, v[44:45] offset:36864

.LBB2_7:
	s_cmp_lt_u32 s94, 0x800
	s_cbranch_scc1 .Lg2_qk_epi
	v_fmamk_f32 v126, v126, 0x3a800000, v158
	v_fmamk_f32 v127, v127, 0x3a800000, v159
	v_mov_b32_e32 v178, v163
	v_cvt_pk_fp8_f32 v178, v126, v127
	v_fmamk_f32 v126, v128, 0x3a800000, v160
	v_fmamk_f32 v122, v122, 0x3a800000, v158
	v_fmamk_f32 v123, v123, 0x3a800000, v159
	v_mov_b32_e32 v128, v163
	v_cvt_pk_fp8_f32 v128, v122, v123
	v_fmamk_f32 v124, v124, 0x3a800000, v160
	v_fmamk_f32 v125, v125, 0x3a800000, v161
	v_fmamk_f32 v118, v118, 0x3a800000, v158
	v_cvt_pk_fp8_f32 v128, v124, v125 op_sel:[0,0,1]
	v_fmamk_f32 v119, v119, 0x3a800000, v159
	v_mov_b32_e32 v124, v163
	v_cvt_pk_fp8_f32 v124, v118, v119
	v_fmamk_f32 v114, v114, 0x3a800000, v158
	v_fmamk_f32 v115, v115, 0x3a800000, v159
	v_mov_b32_e32 v118, v163
	v_cvt_pk_fp8_f32 v118, v114, v115
	v_fmamk_f32 v114, v116, 0x3a800000, v160
	v_fmamk_f32 v110, v110, 0x3a800000, v154
	v_fmamk_f32 v111, v111, 0x3a800000, v155
	v_mov_b32_e32 v116, v163
	v_cvt_pk_fp8_f32 v116, v110, v111
	v_fmamk_f32 v112, v112, 0x3a800000, v156
	v_fmamk_f32 v113, v113, 0x3a800000, v157
	v_fmamk_f32 v98, v98, 0x3a800000, v154
	v_cvt_pk_fp8_f32 v116, v112, v113 op_sel:[0,0,1]
	v_fmamk_f32 v99, v99, 0x3a800000, v155
	v_mov_b32_e32 v112, v163
	v_cvt_pk_fp8_f32 v112, v98, v99
	v_fmamk_f32 v100, v100, 0x3a800000, v156
	v_fmamk_f32 v101, v101, 0x3a800000, v157
	v_and_b32_e32 v162, 15, v175
	v_cvt_pk_fp8_f32 v112, v100, v101 op_sel:[0,0,1]
	v_fmamk_f32 v100, v106, 0x3a800000, v154
	v_fmamk_f32 v101, v107, 0x3a800000, v155
	v_fmamk_f32 v106, v108, 0x3a800000, v156
	v_mov_b32_e32 v108, v163
	v_cvt_pk_fp8_f32 v108, v100, v101
	v_fmamk_f32 v100, v102, 0x3a800000, v154
	v_fmamk_f32 v101, v103, 0x3a800000, v155
	v_mov_b32_e32 v102, v163
	v_cvt_pk_fp8_f32 v102, v100, v101
	v_lshrrev_b32_e32 v175, 1, v175
	v_and_b32_e32 v175, 0x60, v175
	v_or3_b32 v162, v175, v162, s50
	v_lshrrev_b32_e32 v175, 2, v173
	v_fmamk_f32 v107, v109, 0x3a800000, v157
	v_fmamk_f32 v100, v104, 0x3a800000, v156
	v_fmac_f32_e32 v157, 0x3a800000, v105
	v_and_b32_e32 v175, 0xf0, v175
	v_cvt_pk_fp8_f32 v102, v100, v157 op_sel:[0,0,1]
	v_fmamk_f32 v86, v86, 0x3a800000, v150
	v_fmamk_f32 v87, v87, 0x3a800000, v151
	v_mov_b32_e32 v100, v163
	s_ashr_i32 s45, s50, 4
	v_or_b32_e32 v175, s56, v175
	v_fmamk_f32 v127, v129, 0x3a800000, v161
	v_fmamk_f32 v121, v121, 0x3a800000, v161
	v_fmac_f32_e32 v161, 0x3a800000, v117
	v_cvt_pk_fp8_f32 v100, v86, v87
	s_and_b32 s45, s45, 0xffffff00
	v_cvt_pk_fp8_f32 v118, v114, v161 op_sel:[0,0,1]
	v_or_b32_e32 v114, 4, v175
	v_add_u32_e32 v176, s45, v175
	v_add_u32_e32 v114, s45, v114
	v_or_b32_e32 v176, v176, v172
	v_or_b32_e32 v114, v114, v172
	v_fmamk_f32 v88, v88, 0x3a800000, v152
	v_fmamk_f32 v89, v89, 0x3a800000, v153
	v_ashrrev_i32_e32 v177, 31, v176
	v_cvt_pk_fp8_f32 v178, v126, v127 op_sel:[0,0,1]
	v_ashrrev_i32_e32 v115, 31, v114
	v_cvt_pk_fp8_f32 v100, v88, v89 op_sel:[0,0,1]
	v_fmamk_f32 v82, v82, 0x3a800000, v150
	v_fmamk_f32 v83, v83, 0x3a800000, v151
	v_mov_b32_e32 v88, v163
	v_lshlrev_b64 v[176:177], 14, v[176:177]
	v_lshlrev_b32_e32 v162, 2, v162
	v_fmamk_f32 v120, v120, 0x3a800000, v160
	v_lshlrev_b64 v[110:111], 14, v[114:115]
	v_cvt_pk_fp8_f32 v88, v82, v83
	v_and_b32_e32 v162, 0x3dbc, v162
	v_lshl_add_u64 v[126:127], s[18:19], 0, v[176:177]
	v_cvt_pk_fp8_f32 v124, v120, v121 op_sel:[0,0,1]
	v_lshl_add_u64 v[110:111], s[18:19], 0, v[110:111]
	v_cvt_pk_fp8_f32 v108, v106, v107 op_sel:[0,0,1]
	v_lshl_add_u64 v[122:123], v[126:127], 0, v[162:163]
	v_lshl_add_u64 v[98:99], v[110:111], 0, v[162:163]
	global_store_dword v[122:123], v178, off
	global_store_dword v[122:123], v128, off offset:64
	global_store_dword v[122:123], v124, off offset:512
	global_store_dword v[122:123], v118, off offset:576
	global_store_dword v[98:99], v116, off
	global_store_dword v[98:99], v112, off offset:64
	global_store_dword v[98:99], v108, off offset:512
	global_store_dword v[98:99], v102, off offset:576
	v_or_b32_e32 v98, 8, v175
	v_fmamk_f32 v84, v84, 0x3a800000, v152
	v_fmamk_f32 v85, v85, 0x3a800000, v153
	v_add_u32_e32 v98, s45, v98
	v_cvt_pk_fp8_f32 v88, v84, v85 op_sel:[0,0,1]
	v_fmamk_f32 v84, v94, 0x3a800000, v150
	v_fmamk_f32 v85, v95, 0x3a800000, v151
	v_mov_b32_e32 v89, v163
	v_or_b32_e32 v98, v98, v172
	v_cvt_pk_fp8_f32 v89, v84, v85
	v_fmamk_f32 v84, v90, 0x3a800000, v150
	v_fmamk_f32 v85, v91, 0x3a800000, v151
	v_mov_b32_e32 v90, v163
	v_ashrrev_i32_e32 v99, 31, v98
	v_cvt_pk_fp8_f32 v90, v84, v85
	v_lshlrev_b64 v[86:87], 14, v[98:99]
	v_lshl_add_u64 v[86:87], s[18:19], 0, v[86:87]
	v_lshl_add_u64 v[82:83], v[86:87], 0, v[162:163]
	v_fmamk_f32 v87, v97, 0x3a800000, v153
	v_fmamk_f32 v84, v92, 0x3a800000, v152
	v_fmac_f32_e32 v153, 0x3a800000, v93
	v_cvt_pk_fp8_f32 v90, v84, v153 op_sel:[0,0,1]
	v_fmamk_f32 v66, v66, 0x3a800000, v146
	v_fmamk_f32 v67, v67, 0x3a800000, v147
	v_mov_b32_e32 v84, v163
	v_cvt_pk_fp8_f32 v84, v66, v67
	v_fmamk_f32 v68, v68, 0x3a800000, v148
	v_fmamk_f32 v69, v69, 0x3a800000, v149
	v_fmamk_f32 v50, v50, 0x3a800000, v146
	v_cvt_pk_fp8_f32 v84, v68, v69 op_sel:[0,0,1]
	v_fmamk_f32 v51, v51, 0x3a800000, v147
	v_mov_b32_e32 v68, v163
	v_fmamk_f32 v86, v96, 0x3a800000, v152
	v_cvt_pk_fp8_f32 v68, v50, v51
	v_cvt_pk_fp8_f32 v89, v86, v87 op_sel:[0,0,1]
	global_store_dword v[82:83], v100, off
	global_store_dword v[82:83], v88, off offset:64
	global_store_dword v[82:83], v89, off offset:512
	global_store_dword v[82:83], v90, off offset:576
	v_or_b32_e32 v82, 12, v175
	v_fmamk_f32 v52, v52, 0x3a800000, v148
	v_fmamk_f32 v53, v53, 0x3a800000, v149
	v_add_u32_e32 v82, s45, v82
	v_cvt_pk_fp8_f32 v68, v52, v53 op_sel:[0,0,1]
	v_fmamk_f32 v52, v78, 0x3a800000, v146
	v_fmamk_f32 v53, v79, 0x3a800000, v147
	v_mov_b32_e32 v69, v163
	v_or_b32_e32 v82, v82, v172
	v_cvt_pk_fp8_f32 v69, v52, v53
	v_fmamk_f32 v52, v74, 0x3a800000, v146
	v_fmamk_f32 v53, v75, 0x3a800000, v147
	v_mov_b32_e32 v74, v163
	v_ashrrev_i32_e32 v83, 31, v82
	v_cvt_pk_fp8_f32 v74, v52, v53
	v_lshlrev_b64 v[66:67], 14, v[82:83]
	v_lshl_add_u64 v[66:67], s[18:19], 0, v[66:67]
	v_lshl_add_u64 v[50:51], v[66:67], 0, v[162:163]
	v_fmamk_f32 v67, v81, 0x3a800000, v149
	v_fmamk_f32 v52, v76, 0x3a800000, v148
	v_fmac_f32_e32 v149, 0x3a800000, v77
	v_cvt_pk_fp8_f32 v74, v52, v149 op_sel:[0,0,1]
	v_fmamk_f32 v52, v62, 0x3a800000, v142
	v_fmamk_f32 v53, v63, 0x3a800000, v143
	v_mov_b32_e32 v62, v163
	v_cvt_pk_fp8_f32 v62, v52, v53
	v_fmamk_f32 v52, v64, 0x3a800000, v144
	v_fmamk_f32 v53, v65, 0x3a800000, v145
	v_fmamk_f32 v66, v80, 0x3a800000, v148
	v_cvt_pk_fp8_f32 v62, v52, v53 op_sel:[0,0,1]
	v_fmamk_f32 v52, v54, 0x3a800000, v142
	v_fmamk_f32 v53, v55, 0x3a800000, v143
	v_mov_b32_e32 v54, v163
	v_cvt_pk_fp8_f32 v54, v52, v53
	v_fmamk_f32 v52, v56, 0x3a800000, v144
	v_fmamk_f32 v53, v57, 0x3a800000, v145
	v_mov_b32_e32 v57, v163
	v_cvt_pk_fp8_f32 v54, v52, v53 op_sel:[0,0,1]
	v_fmamk_f32 v52, v70, 0x3a800000, v142
	v_fmamk_f32 v53, v71, 0x3a800000, v143
	v_cvt_pk_fp8_f32 v69, v66, v67 op_sel:[0,0,1]
	v_cvt_pk_fp8_f32 v57, v52, v53
	v_fmamk_f32 v52, v58, 0x3a800000, v142
	v_fmamk_f32 v53, v59, 0x3a800000, v143
	v_mov_b32_e32 v58, v163
	v_cvt_pk_fp8_f32 v58, v52, v53
	global_store_dword v[50:51], v84, off
	global_store_dword v[50:51], v68, off offset:64
	global_store_dword v[50:51], v69, off offset:512
	global_store_dword v[50:51], v74, off offset:576
	v_lshrrev_b32_e32 v50, 2, v174
	v_and_b32_e32 v50, 0xf0, v50
	v_or_b32_e32 v50, s56, v50
	v_fmamk_f32 v56, v73, 0x3a800000, v145
	v_fmamk_f32 v52, v60, 0x3a800000, v144
	v_fmac_f32_e32 v145, 0x3a800000, v61
	v_add_u32_e32 v50, s45, v50
	v_cvt_pk_fp8_f32 v58, v52, v145 op_sel:[0,0,1]
	v_fmamk_f32 v42, v42, 0x3a800000, v138
	v_fmamk_f32 v43, v43, 0x3a800000, v139
	v_mov_b32_e32 v52, v163
	v_or_b32_e32 v50, v50, v172
	v_cvt_pk_fp8_f32 v52, v42, v43
	v_ashrrev_i32_e32 v51, 31, v50
	v_lshlrev_b64 v[50:51], 14, v[50:51]
	v_fmamk_f32 v55, v72, 0x3a800000, v144
	v_lshl_add_u64 v[50:51], s[18:19], 0, v[50:51]
	v_cvt_pk_fp8_f32 v57, v55, v56 op_sel:[0,0,1]
	v_fmamk_f32 v44, v44, 0x3a800000, v140
	v_fmamk_f32 v45, v45, 0x3a800000, v141
	v_lshl_add_u64 v[50:51], v[50:51], 0, v[162:163]
	v_cvt_pk_fp8_f32 v52, v44, v45 op_sel:[0,0,1]
	v_fmamk_f32 v34, v34, 0x3a800000, v138
	v_fmamk_f32 v35, v35, 0x3a800000, v139
	v_mov_b32_e32 v44, v163
	global_store_dword v[50:51], v62, off
	global_store_dword v[50:51], v54, off offset:64
	global_store_dword v[50:51], v57, off offset:512
	global_store_dword v[50:51], v58, off offset:576
	v_add_u32_e32 v50, 0x90, v173
	v_cvt_pk_fp8_f32 v44, v34, v35
	v_lshrrev_b32_e32 v50, 2, v50
	v_and_b32_e32 v50, 0xf4, v50
	v_or_b32_e32 v50, s56, v50
	v_fmamk_f32 v36, v36, 0x3a800000, v140
	v_fmamk_f32 v37, v37, 0x3a800000, v141
	v_add_u32_e32 v50, s45, v50
	v_cvt_pk_fp8_f32 v44, v36, v37 op_sel:[0,0,1]
	v_fmamk_f32 v36, v46, 0x3a800000, v138
	v_fmamk_f32 v37, v47, 0x3a800000, v139
	v_mov_b32_e32 v45, v163
	v_or_b32_e32 v50, v50, v172
	v_cvt_pk_fp8_f32 v45, v36, v37
	v_fmamk_f32 v36, v38, 0x3a800000, v138
	v_fmamk_f32 v37, v39, 0x3a800000, v139
	v_mov_b32_e32 v38, v163
	v_ashrrev_i32_e32 v51, 31, v50
	v_cvt_pk_fp8_f32 v38, v36, v37
	v_lshlrev_b64 v[42:43], 14, v[50:51]
	v_lshl_add_u64 v[42:43], s[18:19], 0, v[42:43]
	v_lshl_add_u64 v[34:35], v[42:43], 0, v[162:163]
	v_fmamk_f32 v43, v49, 0x3a800000, v141
	v_fmamk_f32 v36, v40, 0x3a800000, v140
	v_fmac_f32_e32 v141, 0x3a800000, v41
	v_cvt_pk_fp8_f32 v38, v36, v141 op_sel:[0,0,1]
	v_fmamk_f32 v26, v26, 0x3a800000, v134
	v_fmamk_f32 v27, v27, 0x3a800000, v135
	v_mov_b32_e32 v36, v163
	v_cvt_pk_fp8_f32 v36, v26, v27
	v_fmamk_f32 v42, v48, 0x3a800000, v140
	v_cvt_pk_fp8_f32 v45, v42, v43 op_sel:[0,0,1]
	v_fmamk_f32 v28, v28, 0x3a800000, v136
	v_fmamk_f32 v29, v29, 0x3a800000, v137
	v_cvt_pk_fp8_f32 v36, v28, v29 op_sel:[0,0,1]
	v_fmamk_f32 v18, v18, 0x3a800000, v134
	v_fmamk_f32 v19, v19, 0x3a800000, v135
	v_mov_b32_e32 v28, v163
	global_store_dword v[34:35], v52, off
	global_store_dword v[34:35], v44, off offset:64
	global_store_dword v[34:35], v45, off offset:512
	global_store_dword v[34:35], v38, off offset:576
	v_add_u32_e32 v34, 0xa0, v173
	v_cvt_pk_fp8_f32 v28, v18, v19
	v_lshrrev_b32_e32 v34, 2, v34
	v_and_b32_e32 v34, 0xf8, v34
	v_or_b32_e32 v34, s56, v34
	v_fmamk_f32 v20, v20, 0x3a800000, v136
	v_fmamk_f32 v21, v21, 0x3a800000, v137
	v_add_u32_e32 v34, s45, v34
	v_cvt_pk_fp8_f32 v28, v20, v21 op_sel:[0,0,1]
	v_fmamk_f32 v20, v30, 0x3a800000, v134
	v_fmamk_f32 v21, v31, 0x3a800000, v135
	v_mov_b32_e32 v29, v163
	v_or_b32_e32 v34, v34, v172
	v_cvt_pk_fp8_f32 v29, v20, v21
	v_fmamk_f32 v20, v22, 0x3a800000, v134
	v_fmamk_f32 v21, v23, 0x3a800000, v135
	v_mov_b32_e32 v22, v163
	v_ashrrev_i32_e32 v35, 31, v34
	v_cvt_pk_fp8_f32 v22, v20, v21
	v_lshlrev_b64 v[26:27], 14, v[34:35]
	v_lshl_add_u64 v[26:27], s[18:19], 0, v[26:27]
	v_lshl_add_u64 v[18:19], v[26:27], 0, v[162:163]
	v_fmamk_f32 v27, v33, 0x3a800000, v137
	v_fmamk_f32 v20, v24, 0x3a800000, v136
	v_fmac_f32_e32 v137, 0x3a800000, v25
	v_cvt_pk_fp8_f32 v22, v20, v137 op_sel:[0,0,1]
	v_fmamk_f32 v10, v10, 0x3a800000, v130
	v_fmamk_f32 v11, v11, 0x3a800000, v131
	v_mov_b32_e32 v20, v163
	v_cvt_pk_fp8_f32 v20, v10, v11
	v_fmamk_f32 v26, v32, 0x3a800000, v136
	v_cvt_pk_fp8_f32 v29, v26, v27 op_sel:[0,0,1]
	v_fmamk_f32 v12, v12, 0x3a800000, v132
	v_fmamk_f32 v13, v13, 0x3a800000, v133
	global_store_dword v[18:19], v36, off
	global_store_dword v[18:19], v28, off offset:64
	global_store_dword v[18:19], v29, off offset:512
	global_store_dword v[18:19], v22, off offset:576
	v_add_u32_e32 v18, 0xb0, v173
	v_cvt_pk_fp8_f32 v20, v12, v13 op_sel:[0,0,1]
	v_fmamk_f32 v2, v2, 0x3a800000, v130
	v_fmamk_f32 v3, v3, 0x3a800000, v131
	v_mov_b32_e32 v12, v163
	v_lshrrev_b32_e32 v18, 2, v18
	v_cvt_pk_fp8_f32 v12, v2, v3
	v_and_b32_e32 v18, 0xfc, v18
	v_or_b32_e32 v18, s56, v18
	v_add_u32_e32 v18, s45, v18
	v_fmamk_f32 v4, v4, 0x3a800000, v132
	v_fmamk_f32 v5, v5, 0x3a800000, v133
	v_or_b32_e32 v18, v18, v172
	v_cvt_pk_fp8_f32 v12, v4, v5 op_sel:[0,0,1]
	v_fmamk_f32 v4, v14, 0x3a800000, v130
	v_fmamk_f32 v5, v15, 0x3a800000, v131
	v_mov_b32_e32 v13, v163
	v_ashrrev_i32_e32 v19, 31, v18
	v_cvt_pk_fp8_f32 v13, v4, v5
	v_fmamk_f32 v4, v6, 0x3a800000, v130
	v_fmamk_f32 v5, v7, 0x3a800000, v131
	v_mov_b32_e32 v6, v163
	v_lshlrev_b64 v[10:11], 14, v[18:19]
	v_cvt_pk_fp8_f32 v6, v4, v5
	v_lshl_add_u64 v[10:11], s[18:19], 0, v[10:11]
	v_lshl_add_u64 v[2:3], v[10:11], 0, v[162:163]
	v_fmamk_f32 v10, v16, 0x3a800000, v132
	v_fmamk_f32 v11, v17, 0x3a800000, v133
	v_cvt_pk_fp8_f32 v13, v10, v11 op_sel:[0,0,1]
	v_fmamk_f32 v4, v8, 0x3a800000, v132
	v_fmac_f32_e32 v133, 0x3a800000, v9
	v_cvt_pk_fp8_f32 v6, v4, v133 op_sel:[0,0,1]
	s_mov_b64 s[56:57], 0
	s_andn2_b64 vcc, exec, s[52:53]
	s_mov_b32 s50, s54
	global_store_dword v[2:3], v20, off
	global_store_dword v[2:3], v12, off offset:64
	global_store_dword v[2:3], v13, off offset:512
	global_store_dword v[2:3], v6, off offset:576
	s_cbranch_vccz .LBB2_26

.LBB2_14:
	s_ashr_i32 s51, s50, 31
	s_lshl_b64 s[52:53], s[50:51], 10
	s_add_u32 s52, s10, s52
	s_addc_u32 s53, s11, s53
	v_mov_b32_e32 v162, v1
	s_barrier
	s_add_i32 s78, s70, 0x18000
	v_lshl_add_u64 v[2:3], s[52:53], 0, v[162:163]
	s_ashr_i32 s45, s44, 31
	v_lshl_add_u64 v[2:3], v[2:3], 0, s[20:21]
	s_mov_b32 m0, s78
	v_mov_b32_e32 v162, v1
	s_add_i32 s79, s70, 0x1a000
	s_lshl_b64 s[54:55], s[44:45], 10
	global_load_lds_dwordx4 v[2:3], off
	s_add_u32 s54, s8, s54
	v_lshl_add_u64 v[2:3], s[52:53], 0, v[162:163]
	v_lshl_add_u64 v[2:3], v[2:3], 0, s[22:23]
	s_mov_b32 m0, s79
	s_addc_u32 s55, s9, s55
	v_mov_b32_e32 v162, v1
	s_or_b32 s56, s50, 0x80
	global_load_lds_dwordx4 v[2:3], off
	s_add_i32 s45, s70, 0x8000
	v_lshl_add_u64 v[2:3], s[54:55], 0, v[162:163]
	s_ashr_i32 s57, s56, 31
	v_lshl_add_u64 v[2:3], v[2:3], 0, s[20:21]
	s_mov_b32 m0, s45
	v_mov_b32_e32 v162, v1
	s_add_i32 s80, s70, 0xa000
	s_lshl_b64 s[56:57], s[56:57], 10
	global_load_lds_dwordx4 v[2:3], off
	s_add_u32 s56, s10, s56
	v_lshl_add_u64 v[2:3], s[54:55], 0, v[162:163]
	v_lshl_add_u64 v[2:3], v[2:3], 0, s[22:23]
	s_mov_b32 m0, s80
	s_addc_u32 s57, s11, s57
	v_mov_b32_e32 v162, v1
	global_load_lds_dwordx4 v[2:3], off
	s_add_i32 s82, s70, 0x1c000
	v_lshl_add_u64 v[2:3], s[56:57], 0, v[162:163]
	v_lshl_add_u64 v[2:3], v[2:3], 0, s[20:21]
	s_mov_b32 m0, s82
	v_mov_b32_e32 v162, v1
	global_load_lds_dwordx4 v[2:3], off
	s_add_i32 s84, s70, 0x1e000
	v_lshl_add_u64 v[2:3], s[56:57], 0, v[162:163]
	v_lshl_add_u64 v[2:3], v[2:3], 0, s[22:23]
	s_mov_b32 m0, s84
	v_mov_b32_e32 v50, 0
	global_load_lds_dwordx4 v[2:3], off
	s_waitcnt lgkmcnt(0)
	s_cmp_lt_u32 s44, 0x800
	s_cbranch_scc1 .Lg2_bias_qk
	s_lshr_b32 s86, s44, 10
	s_cmp_eq_u32 s86, 1
	s_cselect_b32 s88, s14, s6
	s_cselect_b32 s89, s15, s7
	s_cmp_eq_u32 s86, 0
	s_cselect_b32 s88, s12, s88
	s_cselect_b32 s89, s13, s89
	s_and_b32 s86, s44, 0x3ff
	s_lshl_b32 s86, s86, 2
	s_add_u32 s88, s88, s86
	s_addc_u32 s89, s89, 0
	v_and_b32_e32 v184, 63, v0
	v_lshlrev_b32_e32 v184, 4, v184
	s_mov_b32 m0, 0x20000
	s_nop 0
	global_load_lds_dwordx4 v184, s[88:89]
	s_branch .Lg2_bias_done
.Lg2_bias_qk:
	s_lshr_b32 s86, s44, 8
	s_lshl_b32 s86, s86, 9
	v_and_b32_e32 v184, 63, v0
	v_cmp_lt_u32_e64 s[98:99], 31, v184
	v_and_b32_e32 v186, 31, v184
	v_lshlrev_b32_e32 v186, 4, v186
	v_add_u32_e32 v186, s86, v186
	v_mov_b32_e32 v187, 0
	v_mov_b32_e32 v188, s12
	v_mov_b32_e32 v189, s13
	v_mov_b32_e32 v190, s14
	v_mov_b32_e32 v191, s15
	s_nop 1
	v_cndmask_b32_e64 v184, v188, v190, s[98:99]
	v_cndmask_b32_e64 v185, v189, v191, s[98:99]
	v_lshl_add_u64 v[184:185], v[184:185], 0, v[186:187]
	s_mov_b32 m0, 0x20000
	s_nop 0
	global_load_lds_dwordx4 v[184:185], off
.Lg2_bias_done:
	s_cmp_eq_u32 s87, 0
	s_cbranch_scc1 .Lg2_w6
	s_waitcnt vmcnt(39)
	s_branch .Lg2_wd

.LBB2_21:
	s_or_b64 exec, exec, s[52:53]
	s_mov_b32 s94, s44
	v_mov_b32_e32 v175, v0
	s_addk_i32 s2, 0x100
	v_ashrrev_i32_e32 v130, 2, v175
	v_and_b32_e32 v130, 0xffffffc0, v130
	v_bfe_u32 v172, v175, 4, 2
	s_and_b32 s56, s44, 0xfffffc00
	v_add_u32_e32 v173, s44, v130
	s_cmpk_eq_i32 s56, 0x400
	v_lshlrev_b32_e32 v130, 2, v172
	v_add_u32_e32 v174, 0x80, v173
	s_cselect_b32 s45, s14, s6
	s_cselect_b32 s52, s15, s7
	s_cmpk_lt_u32 s44, 0x400
	v_and_or_b32 v131, v173, s74, v130
	v_and_or_b32 v130, v174, s74, v130
	s_cselect_b32 s53, s13, s52
	s_cselect_b32 s52, s12, s45
	v_lshlrev_b32_e32 v131, 2, v131
	v_lshlrev_b32_e32 v130, 2, v130
	v_lshrrev_b32_e32 v184, 8, v0
	v_bfe_u32 v185, v0, 4, 2
	v_lshlrev_b32_e32 v184, 8, v184
	v_lshl_add_u32 v184, v185, 4, v184
	v_add_u32_e32 v184, 0x20000, v184
	ds_read_b128 v[158:161], v184
	ds_read_b128 v[154:157], v184 offset:64
	ds_read_b128 v[150:153], v184 offset:128
	ds_read_b128 v[146:149], v184 offset:192
	ds_read_b128 v[142:145], v184 offset:512
	ds_read_b128 v[138:141], v184 offset:576
	ds_read_b128 v[134:137], v184 offset:640
	ds_read_b128 v[130:133], v184 offset:704
	s_cmp_ge_i32 s2, s33
	s_waitcnt vmcnt(0) lgkmcnt(0)
	s_cselect_b64 s[52:53], -1, 0
	s_and_b64 vcc, exec, s[52:53]
	s_mov_b32 s54, s50
	s_cbranch_vccnz .LBB2_7
	s_ashr_i32 s44, s2, 31
	s_lshr_b32 s44, s44, 29
	s_add_i32 s54, s2, s44
	s_and_b32 s44, s54, -8
	s_sub_i32 s55, s2, s44
	s_cmp_ge_i32 s55, s63
	s_mov_b64 s[44:45], -1
	s_cbranch_scc0 .LBB2_24
	s_sub_i32 s44, s55, s63
	s_mul_i32 s44, s44, s62
	s_add_i32 s57, s44, s65
	s_mov_b64 s[44:45], 0

.Lg2_qk_epi:
	s_lshr_b32 s95, s50, 12
	s_lshl_b32 s95, s95, 9
	s_lshr_b32 s96, s94, 2
	s_add_u32 s95, s95, s96
	s_lshl_b32 s95, s95, 14
	s_add_u32 s96, s18, s95
	s_addc_u32 s97, s19, 0
	v_lshrrev_b32_e32 v200, 8, v0
	v_bfe_u32 v201, v0, 4, 2
	v_lshlrev_b32_e32 v200, 5, v200
	v_lshl_add_u32 v200, v201, 1, v200
	v_lshlrev_b32_e32 v200, 14, v200
	v_and_b32_e32 v202, 15, v0
	v_lshrrev_b32_e32 v201, 1, v0
	v_and_b32_e32 v201, 0x60, v201
	v_or3_b32 v202, v201, v202, s50
	v_and_b32_e32 v202, 0xfff, v202
	v_lshl_add_u32 v203, v202, 2, v200
	v_mov_b32_e32 v204, v203
	v_add_u32_e32 v205, 0x4000, v203
	v_add_u32_e32 v206, 0x20000, v203
	v_add_u32_e32 v207, 0x24000, v203
	v_add_u32_e32 v208, 0x40000, v203
	v_add_u32_e32 v209, 0x44000, v203
	v_add_u32_e32 v210, 0x60000, v203
	v_add_u32_e32 v211, 0x64000, v203
	v_fmamk_f32 v126, v126, 0x3a800000, v158
	v_fmamk_f32 v127, v127, 0x3a800000, v159
	v_fmamk_f32 v128, v128, 0x3a800000, v160
	v_fmamk_f32 v129, v129, 0x3a800000, v161
	v_fmamk_f32 v62, v62, 0x3a800000, v142
	v_fmamk_f32 v63, v63, 0x3a800000, v143
	v_fmamk_f32 v64, v64, 0x3a800000, v144
	v_fmamk_f32 v65, v65, 0x3a800000, v145
	v_cvt_pk_fp8_f32 v212, v126, v127
	v_cvt_pk_fp8_f32 v213, v128, v129
	s_nop 0
	v_cvt_pk_fp8_f32 v212, v62, v63 op_sel:[0,0,1]
	v_cvt_pk_fp8_f32 v213, v64, v65 op_sel:[0,0,1]
	s_nop 1
	global_store_dword v204, v212, s[96:97]
	global_store_dword v205, v213, s[96:97]
	v_fmamk_f32 v122, v122, 0x3a800000, v158
	v_fmamk_f32 v123, v123, 0x3a800000, v159
	v_fmamk_f32 v124, v124, 0x3a800000, v160
	v_fmamk_f32 v125, v125, 0x3a800000, v161
	v_fmamk_f32 v54, v54, 0x3a800000, v142
	v_fmamk_f32 v55, v55, 0x3a800000, v143
	v_fmamk_f32 v56, v56, 0x3a800000, v144
	v_fmamk_f32 v57, v57, 0x3a800000, v145
	v_cvt_pk_fp8_f32 v214, v122, v123
	v_cvt_pk_fp8_f32 v215, v124, v125
	s_nop 0
	v_cvt_pk_fp8_f32 v214, v54, v55 op_sel:[0,0,1]
	v_cvt_pk_fp8_f32 v215, v56, v57 op_sel:[0,0,1]
	s_nop 1
	global_store_dword v204, v214, s[96:97] offset:64
	global_store_dword v205, v215, s[96:97] offset:64
	v_fmamk_f32 v118, v118, 0x3a800000, v158
	v_fmamk_f32 v119, v119, 0x3a800000, v159
	v_fmamk_f32 v120, v120, 0x3a800000, v160
	v_fmamk_f32 v121, v121, 0x3a800000, v161
	v_fmamk_f32 v70, v70, 0x3a800000, v142
	v_fmamk_f32 v71, v71, 0x3a800000, v143
	v_fmamk_f32 v72, v72, 0x3a800000, v144
	v_fmamk_f32 v73, v73, 0x3a800000, v145
	v_cvt_pk_fp8_f32 v216, v118, v119
	v_cvt_pk_fp8_f32 v217, v120, v121
	s_nop 0
	v_cvt_pk_fp8_f32 v216, v70, v71 op_sel:[0,0,1]
	v_cvt_pk_fp8_f32 v217, v72, v73 op_sel:[0,0,1]
	s_nop 1
	global_store_dword v204, v216, s[96:97] offset:512
	global_store_dword v205, v217, s[96:97] offset:512
	v_fmamk_f32 v114, v114, 0x3a800000, v158
	v_fmamk_f32 v115, v115, 0x3a800000, v159
	v_fmamk_f32 v116, v116, 0x3a800000, v160
	v_fmamk_f32 v117, v117, 0x3a800000, v161
	v_fmamk_f32 v58, v58, 0x3a800000, v142
	v_fmamk_f32 v59, v59, 0x3a800000, v143
	v_fmamk_f32 v60, v60, 0x3a800000, v144
	v_fmamk_f32 v61, v61, 0x3a800000, v145
	v_cvt_pk_fp8_f32 v218, v114, v115
	v_cvt_pk_fp8_f32 v219, v116, v117
	s_nop 0
	v_cvt_pk_fp8_f32 v218, v58, v59 op_sel:[0,0,1]
	v_cvt_pk_fp8_f32 v219, v60, v61 op_sel:[0,0,1]
	s_nop 1
	global_store_dword v204, v218, s[96:97] offset:576
	global_store_dword v205, v219, s[96:97] offset:576
	v_fmamk_f32 v110, v110, 0x3a800000, v154
	v_fmamk_f32 v111, v111, 0x3a800000, v155
	v_fmamk_f32 v112, v112, 0x3a800000, v156
	v_fmamk_f32 v113, v113, 0x3a800000, v157
	v_fmamk_f32 v42, v42, 0x3a800000, v138
	v_fmamk_f32 v43, v43, 0x3a800000, v139
	v_fmamk_f32 v44, v44, 0x3a800000, v140
	v_fmamk_f32 v45, v45, 0x3a800000, v141
	v_cvt_pk_fp8_f32 v220, v110, v111
	v_cvt_pk_fp8_f32 v221, v112, v113
	s_nop 0
	v_cvt_pk_fp8_f32 v220, v42, v43 op_sel:[0,0,1]
	v_cvt_pk_fp8_f32 v221, v44, v45 op_sel:[0,0,1]
	s_nop 1
	global_store_dword v206, v220, s[96:97]
	global_store_dword v207, v221, s[96:97]
	v_fmamk_f32 v98, v98, 0x3a800000, v154
	v_fmamk_f32 v99, v99, 0x3a800000, v155
	v_fmamk_f32 v100, v100, 0x3a800000, v156
	v_fmamk_f32 v101, v101, 0x3a800000, v157
	v_fmamk_f32 v34, v34, 0x3a800000, v138
	v_fmamk_f32 v35, v35, 0x3a800000, v139
	v_fmamk_f32 v36, v36, 0x3a800000, v140
	v_fmamk_f32 v37, v37, 0x3a800000, v141
	v_cvt_pk_fp8_f32 v222, v98, v99
	v_cvt_pk_fp8_f32 v223, v100, v101
	s_nop 0
	v_cvt_pk_fp8_f32 v222, v34, v35 op_sel:[0,0,1]
	v_cvt_pk_fp8_f32 v223, v36, v37 op_sel:[0,0,1]
	s_nop 1
	global_store_dword v206, v222, s[96:97] offset:64
	global_store_dword v207, v223, s[96:97] offset:64
	v_fmamk_f32 v106, v106, 0x3a800000, v154
	v_fmamk_f32 v107, v107, 0x3a800000, v155
	v_fmamk_f32 v108, v108, 0x3a800000, v156
	v_fmamk_f32 v109, v109, 0x3a800000, v157
	v_fmamk_f32 v46, v46, 0x3a800000, v138
	v_fmamk_f32 v47, v47, 0x3a800000, v139
	v_fmamk_f32 v48, v48, 0x3a800000, v140
	v_fmamk_f32 v49, v49, 0x3a800000, v141
	v_cvt_pk_fp8_f32 v224, v106, v107
	v_cvt_pk_fp8_f32 v225, v108, v109
	s_nop 0
	v_cvt_pk_fp8_f32 v224, v46, v47 op_sel:[0,0,1]
	v_cvt_pk_fp8_f32 v225, v48, v49 op_sel:[0,0,1]
	s_nop 1
	global_store_dword v206, v224, s[96:97] offset:512
	global_store_dword v207, v225, s[96:97] offset:512
	v_fmamk_f32 v102, v102, 0x3a800000, v154
	v_fmamk_f32 v103, v103, 0x3a800000, v155
	v_fmamk_f32 v104, v104, 0x3a800000, v156
	v_fmamk_f32 v105, v105, 0x3a800000, v157
	v_fmamk_f32 v38, v38, 0x3a800000, v138
	v_fmamk_f32 v39, v39, 0x3a800000, v139
	v_fmamk_f32 v40, v40, 0x3a800000, v140
	v_fmamk_f32 v41, v41, 0x3a800000, v141
	v_cvt_pk_fp8_f32 v226, v102, v103
	v_cvt_pk_fp8_f32 v227, v104, v105
	s_nop 0
	v_cvt_pk_fp8_f32 v226, v38, v39 op_sel:[0,0,1]
	v_cvt_pk_fp8_f32 v227, v40, v41 op_sel:[0,0,1]
	s_nop 1
	global_store_dword v206, v226, s[96:97] offset:576
	global_store_dword v207, v227, s[96:97] offset:576
	v_fmamk_f32 v86, v86, 0x3a800000, v150
	v_fmamk_f32 v87, v87, 0x3a800000, v151
	v_fmamk_f32 v88, v88, 0x3a800000, v152
	v_fmamk_f32 v89, v89, 0x3a800000, v153
	v_fmamk_f32 v26, v26, 0x3a800000, v134
	v_fmamk_f32 v27, v27, 0x3a800000, v135
	v_fmamk_f32 v28, v28, 0x3a800000, v136
	v_fmamk_f32 v29, v29, 0x3a800000, v137
	v_cvt_pk_fp8_f32 v228, v86, v87
	v_cvt_pk_fp8_f32 v229, v88, v89
	s_nop 0
	v_cvt_pk_fp8_f32 v228, v26, v27 op_sel:[0,0,1]
	v_cvt_pk_fp8_f32 v229, v28, v29 op_sel:[0,0,1]
	s_nop 1
	global_store_dword v208, v228, s[96:97]
	global_store_dword v209, v229, s[96:97]
	v_fmamk_f32 v82, v82, 0x3a800000, v150
	v_fmamk_f32 v83, v83, 0x3a800000, v151
	v_fmamk_f32 v84, v84, 0x3a800000, v152
	v_fmamk_f32 v85, v85, 0x3a800000, v153
	v_fmamk_f32 v18, v18, 0x3a800000, v134
	v_fmamk_f32 v19, v19, 0x3a800000, v135
	v_fmamk_f32 v20, v20, 0x3a800000, v136
	v_fmamk_f32 v21, v21, 0x3a800000, v137
	v_cvt_pk_fp8_f32 v230, v82, v83
	v_cvt_pk_fp8_f32 v231, v84, v85
	s_nop 0
	v_cvt_pk_fp8_f32 v230, v18, v19 op_sel:[0,0,1]
	v_cvt_pk_fp8_f32 v231, v20, v21 op_sel:[0,0,1]
	s_nop 1
	global_store_dword v208, v230, s[96:97] offset:64
	global_store_dword v209, v231, s[96:97] offset:64
	v_fmamk_f32 v94, v94, 0x3a800000, v150
	v_fmamk_f32 v95, v95, 0x3a800000, v151
	v_fmamk_f32 v96, v96, 0x3a800000, v152
	v_fmamk_f32 v97, v97, 0x3a800000, v153
	v_fmamk_f32 v30, v30, 0x3a800000, v134
	v_fmamk_f32 v31, v31, 0x3a800000, v135
	v_fmamk_f32 v32, v32, 0x3a800000, v136
	v_fmamk_f32 v33, v33, 0x3a800000, v137
	v_cvt_pk_fp8_f32 v232, v94, v95
	v_cvt_pk_fp8_f32 v233, v96, v97
	s_nop 0
	v_cvt_pk_fp8_f32 v232, v30, v31 op_sel:[0,0,1]
	v_cvt_pk_fp8_f32 v233, v32, v33 op_sel:[0,0,1]
	s_nop 1
	global_store_dword v208, v232, s[96:97] offset:512
	global_store_dword v209, v233, s[96:97] offset:512
	v_fmamk_f32 v90, v90, 0x3a800000, v150
	v_fmamk_f32 v91, v91, 0x3a800000, v151
	v_fmamk_f32 v92, v92, 0x3a800000, v152
	v_fmamk_f32 v93, v93, 0x3a800000, v153
	v_fmamk_f32 v22, v22, 0x3a800000, v134
	v_fmamk_f32 v23, v23, 0x3a800000, v135
	v_fmamk_f32 v24, v24, 0x3a800000, v136
	v_fmamk_f32 v25, v25, 0x3a800000, v137
	v_cvt_pk_fp8_f32 v234, v90, v91
	v_cvt_pk_fp8_f32 v235, v92, v93
	s_nop 0
	v_cvt_pk_fp8_f32 v234, v22, v23 op_sel:[0,0,1]
	v_cvt_pk_fp8_f32 v235, v24, v25 op_sel:[0,0,1]
	s_nop 1
	global_store_dword v208, v234, s[96:97] offset:576
	global_store_dword v209, v235, s[96:97] offset:576
	v_fmamk_f32 v66, v66, 0x3a800000, v146
	v_fmamk_f32 v67, v67, 0x3a800000, v147
	v_fmamk_f32 v68, v68, 0x3a800000, v148
	v_fmamk_f32 v69, v69, 0x3a800000, v149
	v_fmamk_f32 v10, v10, 0x3a800000, v130
	v_fmamk_f32 v11, v11, 0x3a800000, v131
	v_fmamk_f32 v12, v12, 0x3a800000, v132
	v_fmamk_f32 v13, v13, 0x3a800000, v133
	v_cvt_pk_fp8_f32 v236, v66, v67
	v_cvt_pk_fp8_f32 v237, v68, v69
	s_nop 0
	v_cvt_pk_fp8_f32 v236, v10, v11 op_sel:[0,0,1]
	v_cvt_pk_fp8_f32 v237, v12, v13 op_sel:[0,0,1]
	s_nop 1
	global_store_dword v210, v236, s[96:97]
	global_store_dword v211, v237, s[96:97]
	v_fmamk_f32 v50, v50, 0x3a800000, v146
	v_fmamk_f32 v51, v51, 0x3a800000, v147
	v_fmamk_f32 v52, v52, 0x3a800000, v148
	v_fmamk_f32 v53, v53, 0x3a800000, v149
	v_fmamk_f32 v2, v2, 0x3a800000, v130
	v_fmamk_f32 v3, v3, 0x3a800000, v131
	v_fmamk_f32 v4, v4, 0x3a800000, v132
	v_fmamk_f32 v5, v5, 0x3a800000, v133
	v_cvt_pk_fp8_f32 v238, v50, v51
	v_cvt_pk_fp8_f32 v239, v52, v53
	s_nop 0
	v_cvt_pk_fp8_f32 v238, v2, v3 op_sel:[0,0,1]
	v_cvt_pk_fp8_f32 v239, v4, v5 op_sel:[0,0,1]
	s_nop 1
	global_store_dword v210, v238, s[96:97] offset:64
	global_store_dword v211, v239, s[96:97] offset:64
	v_fmamk_f32 v78, v78, 0x3a800000, v146
	v_fmamk_f32 v79, v79, 0x3a800000, v147
	v_fmamk_f32 v80, v80, 0x3a800000, v148
	v_fmamk_f32 v81, v81, 0x3a800000, v149
	v_fmamk_f32 v14, v14, 0x3a800000, v130
	v_fmamk_f32 v15, v15, 0x3a800000, v131
	v_fmamk_f32 v16, v16, 0x3a800000, v132
	v_fmamk_f32 v17, v17, 0x3a800000, v133
	v_cvt_pk_fp8_f32 v240, v78, v79
	v_cvt_pk_fp8_f32 v241, v80, v81
	s_nop 0
	v_cvt_pk_fp8_f32 v240, v14, v15 op_sel:[0,0,1]
	v_cvt_pk_fp8_f32 v241, v16, v17 op_sel:[0,0,1]
	s_nop 1
	global_store_dword v210, v240, s[96:97] offset:512
	global_store_dword v211, v241, s[96:97] offset:512
	v_fmamk_f32 v74, v74, 0x3a800000, v146
	v_fmamk_f32 v75, v75, 0x3a800000, v147
	v_fmamk_f32 v76, v76, 0x3a800000, v148
	v_fmamk_f32 v77, v77, 0x3a800000, v149
	v_fmamk_f32 v6, v6, 0x3a800000, v130
	v_fmamk_f32 v7, v7, 0x3a800000, v131
	v_fmamk_f32 v8, v8, 0x3a800000, v132
	v_fmamk_f32 v9, v9, 0x3a800000, v133
	v_cvt_pk_fp8_f32 v242, v74, v75
	v_cvt_pk_fp8_f32 v243, v76, v77
	s_nop 0
	v_cvt_pk_fp8_f32 v242, v6, v7 op_sel:[0,0,1]
	v_cvt_pk_fp8_f32 v243, v8, v9 op_sel:[0,0,1]
	s_nop 1
	global_store_dword v210, v242, s[96:97] offset:576
	global_store_dword v211, v243, s[96:97] offset:576
	s_mov_b64 s[56:57], 0
	s_andn2_b64 vcc, exec, s[52:53]
	s_mov_b32 s50, s54
	s_cbranch_vccz .LBB2_26
	s_branch .LBB2_8
.LBB2_26:
	s_endpgm
	s_nop 0
	s_nop 0
	s_nop 0
	s_nop 0
	s_nop 0
	s_nop 0
	s_endpgm

	.amdhsa_kernel _Z6k_gemmILi2EEvPKtS1_PvPKfS4_S4_ii
		.amdhsa_group_segment_fixed_size 1024
		.amdhsa_private_segment_fixed_size 0
		.amdhsa_kernarg_size 56
		.amdhsa_user_sgpr_count 2
		.amdhsa_user_sgpr_dispatch_ptr 0
		.amdhsa_user_sgpr_queue_ptr 0
		.amdhsa_user_sgpr_kernarg_segment_ptr 1
		.amdhsa_user_sgpr_dispatch_id 0
		.amdhsa_user_sgpr_kernarg_preload_length 0
		.amdhsa_user_sgpr_kernarg_preload_offset 0
		.amdhsa_user_sgpr_private_segment_size 0
		.amdhsa_uses_dynamic_stack 0
		.amdhsa_enable_private_segment 0
		.amdhsa_system_sgpr_workgroup_id_x 1
		.amdhsa_system_sgpr_workgroup_id_y 0
		.amdhsa_system_sgpr_workgroup_id_z 0
		.amdhsa_system_sgpr_workgroup_info 0
		.amdhsa_system_vgpr_workitem_id 0
		.amdhsa_next_free_vgpr 256
		.amdhsa_next_free_sgpr 100
		.amdhsa_accum_offset 256
		.amdhsa_reserve_vcc 1
		.amdhsa_float_round_mode_32 0
		.amdhsa_float_round_mode_16_64 0
		.amdhsa_float_denorm_mode_32 3
		.amdhsa_float_denorm_mode_16_64 3
		.amdhsa_dx10_clamp 1
		.amdhsa_ieee_mode 1
		.amdhsa_fp16_overflow 0
		.amdhsa_tg_split 0
		.amdhsa_exception_fp_ieee_invalid_op 0
		.amdhsa_exception_fp_denorm_src 0
		.amdhsa_exception_fp_ieee_div_zero 0
		.amdhsa_exception_fp_ieee_overflow 0
		.amdhsa_exception_fp_ieee_underflow 0
		.amdhsa_exception_fp_ieee_inexact 0
		.amdhsa_exception_int_div_zero 0
	.end_amdhsa_kernel

amdhsa.kernels:
  - .agpr_count:     0
    .args:
      - .actual_access:  read_only
        .address_space:  global
        .offset:         0
        .size:           8
        .value_kind:     global_buffer
      - .actual_access:  write_only
        .address_space:  global
        .offset:         8
        .size:           8
        .value_kind:     global_buffer
      - .offset:         16
        .size:           4
        .value_kind:     by_value
      - .actual_access:  read_only
        .address_space:  global
        .offset:         24
        .size:           8
        .value_kind:     global_buffer
      - .actual_access:  read_only
        .address_space:  global
        .offset:         32
        .size:           8
        .value_kind:     global_buffer
      - .actual_access:  read_only
        .address_space:  global
        .offset:         40
        .size:           8
        .value_kind:     global_buffer
      - .actual_access:  read_only
        .address_space:  global
        .offset:         48
        .size:           8
        .value_kind:     global_buffer
      - .actual_access:  write_only
        .address_space:  global
        .offset:         56
        .size:           8
        .value_kind:     global_buffer
      - .actual_access:  write_only
        .address_space:  global
        .offset:         64
        .size:           8
        .value_kind:     global_buffer
      - .actual_access:  write_only
        .address_space:  global
        .offset:         72
        .size:           8
        .value_kind:     global_buffer
    .group_segment_fixed_size: 16640
    .kernarg_segment_align: 8
    .kernarg_segment_size: 80
    .language:       OpenCL C
    .language_version:
      - 2
      - 0
    .max_flat_workgroup_size: 256
    .name:           _Z6k_prepPK15HIP_vector_typeIfLj4EEPS_IjLj4EEiPKfS6_S6_S6_PtS7_PS_IfLj2EE
    .private_segment_fixed_size: 0
    .sgpr_count:     26
    .sgpr_spill_count: 0
    .symbol:         _Z6k_prepPK15HIP_vector_typeIfLj4EEPS_IjLj4EEiPKfS6_S6_S6_PtS7_PS_IfLj2EE.kd
    .uniform_work_group_size: 1
    .uses_dynamic_stack: false
    .vgpr_count:     45
    .vgpr_spill_count: 0
    .wavefront_size: 64
  - .agpr_count:     0
    .args:
      - .actual_access:  read_only
        .address_space:  global
        .offset:         0
        .size:           8
        .value_kind:     global_buffer
      - .actual_access:  write_only
        .address_space:  global
        .offset:         8
        .size:           8
        .value_kind:     global_buffer
      - .actual_access:  read_only
        .address_space:  global
        .offset:         16
        .size:           8
        .value_kind:     global_buffer
    .group_segment_fixed_size: 36928
    .kernarg_segment_align: 8
    .kernarg_segment_size: 24
    .language:       OpenCL C
    .language_version:
      - 2
      - 0
    .max_flat_workgroup_size: 256
    .name:           _Z5k_fftPKtPtPKDv2_f
    .private_segment_fixed_size: 0
    .sgpr_count:     23
    .sgpr_spill_count: 0
    .symbol:         _Z5k_fftPKtPtPKDv2_f.kd
    .uniform_work_group_size: 1
    .uses_dynamic_stack: false
    .vgpr_count:     128
    .vgpr_spill_count: 0
    .wavefront_size: 64
  - .agpr_count:     0
    .args:
      - .address_space:  global
        .offset:         0
        .size:           8
        .value_kind:     global_buffer
      - .address_space:  global
        .offset:         8
        .size:           8
        .value_kind:     global_buffer
      - .actual_access:  write_only
        .address_space:  global
        .offset:         16
        .size:           8
        .value_kind:     global_buffer
      - .actual_access:  read_only
        .address_space:  global
        .offset:         24
        .size:           8
        .value_kind:     global_buffer
      - .actual_access:  read_only
        .address_space:  global
        .offset:         32
        .size:           8
        .value_kind:     global_buffer
      - .actual_access:  read_only
        .address_space:  global
        .offset:         40
        .size:           8
        .value_kind:     global_buffer
      - .offset:         48
        .size:           4
        .value_kind:     by_value
      - .offset:         52
        .size:           4
        .value_kind:     by_value
    .group_segment_fixed_size: 1024
    .kernarg_segment_align: 8
    .kernarg_segment_size: 56
    .language:       OpenCL C
    .language_version:
      - 2
      - 0
    .max_flat_workgroup_size: 512
    .name:           _Z6k_gemmILi2EEvPKtS1_PvPKfS4_S4_ii
    .private_segment_fixed_size: 0
    .sgpr_count:     106
    .sgpr_spill_count: 0
    .symbol:         _Z6k_gemmILi2EEvPKtS1_PvPKfS4_S4_ii.kd
    .uniform_work_group_size: 1
    .uses_dynamic_stack: false
    .vgpr_count:     256
    .vgpr_spill_count: 0
    .wavefront_size: 64
  - .agpr_count:     0
    .args:
      - .address_space:  global
        .offset:         0
        .size:           8
        .value_kind:     global_buffer
      - .address_space:  global
        .offset:         8
        .size:           8
        .value_kind:     global_buffer
      - .actual_access:  write_only
        .address_space:  global
        .offset:         16
        .size:           8
        .value_kind:     global_buffer
      - .actual_access:  read_only
        .address_space:  global
        .offset:         24
        .size:           8
        .value_kind:     global_buffer
      - .actual_access:  read_only
        .address_space:  global
        .offset:         32
        .size:           8
        .value_kind:     global_buffer
      - .actual_access:  read_only
        .address_space:  global
        .offset:         40
        .size:           8
        .value_kind:     global_buffer
      - .offset:         48
        .size:           4
        .value_kind:     by_value
      - .offset:         52
        .size:           4
        .value_kind:     by_value
    .group_segment_fixed_size: 1024
    .kernarg_segment_align: 8
    .kernarg_segment_size: 56
    .language:       OpenCL C
    .language_version:
      - 2
      - 0
    .max_flat_workgroup_size: 512
    .name:           _Z6k_gemmILi4EEvPKtS1_PvPKfS4_S4_ii
    .private_segment_fixed_size: 0
    .sgpr_count:     66
    .sgpr_spill_count: 0
    .symbol:         _Z6k_gemmILi4EEvPKtS1_PvPKfS4_S4_ii.kd
    .uniform_work_group_size: 1
    .uses_dynamic_stack: false
    .vgpr_count:     256
    .vgpr_spill_count: 0
    .wavefront_size: 64
